# forgetting attention: a_t row term fed as QK MFMA accumulator init, one subtract per score instead of sub+add
# speedup vs baseline: 1.0011x; 1.0011x over previous
.LBB0_508:
	v_pk_add_f32 v[0:1], v[0:1], v[16:17] op_sel_hi:[1,0]
	v_pk_add_f32 v[2:3], v[2:3], v[16:17] op_sel_hi:[1,0]
	v_pk_mul_f32 v[18:19], v[0:1], s[88:89] op_sel_hi:[1,0]
	v_pk_add_f32 v[0:1], v[4:5], v[16:17] op_sel_hi:[1,0]
	v_pk_mul_f32 v[2:3], v[2:3], s[88:89] op_sel_hi:[1,0]
	v_pk_mul_f32 v[20:21], v[0:1], s[88:89] op_sel_hi:[1,0]
	v_pk_add_f32 v[0:1], v[6:7], v[16:17] op_sel_hi:[1,0]
	s_sub_i32 s15, 63, s59
	v_pk_mul_f32 v[0:1], v[0:1], s[88:89] op_sel_hi:[1,0]
	ds_write_b128 v114, v[0:3] offset:16
	v_pk_add_f32 v[0:1], v[8:9], v[16:17] op_sel_hi:[1,0]
	v_pk_add_f32 v[2:3], v[10:11], v[16:17] op_sel_hi:[1,0]
	v_pk_mul_f32 v[0:1], v[0:1], s[88:89] op_sel_hi:[1,0]
	v_pk_mul_f32 v[2:3], v[2:3], s[88:89] op_sel_hi:[1,0]
	ds_write_b128 v114, v[0:3] offset:32
	v_pk_add_f32 v[0:1], v[12:13], v[16:17] op_sel_hi:[1,0]
	v_pk_add_f32 v[2:3], v[14:15], v[16:17] op_sel_hi:[1,0]
	v_pk_mul_f32 v[0:1], v[0:1], s[88:89] op_sel_hi:[1,0]
	v_pk_mul_f32 v[2:3], v[2:3], s[88:89] op_sel_hi:[1,0]
	ds_write_b128 v114, v[18:21]
	ds_write_b128 v114, v[0:3] offset:48
	s_waitcnt lgkmcnt(0)
	s_barrier
	s_load_dwordx2 s[0:1], s[76:77], 0x108
	s_load_dwordx2 s[50:51], s[76:77], 0x138
	v_mov_b32_e32 v126, v108
	s_lshl_b32 s14, s15, 7
	s_add_i32 s10, s14, s89
	v_and_b32_e32 v32, 15, v126
	v_or_b32_e32 v125, s10, v32
	v_readlane_b32 s10, v247, 36
	s_lshl_b32 s62, s10, 1
	s_waitcnt lgkmcnt(0)
	s_add_u32 s48, s0, s62
	v_and_b32_e32 v0, -16, v126
	s_addc_u32 s49, s1, 0
	v_mad_u64_u32 v[8:9], s[0:1], v125, s75, v[0:1]
	v_add_u32_e32 v4, 64, v8
	v_add_u32_e32 v9, 0x80, v8
	v_add_u32_e32 v12, 0xc0, v8
	global_load_dwordx4 v[0:3], v8, s[48:49] offset:3072
	s_nop 0
	global_load_dwordx4 v[4:7], v4, s[48:49] offset:3072
	s_nop 0
	global_load_dwordx4 v[8:11], v9, s[48:49] offset:3072
	s_nop 0
	global_load_dwordx4 v[12:15], v12, s[48:49] offset:3072
	v_lshl_add_u32 v16, v125, 2, s85
	ds_read_b32 v127, v16
	s_lshl_b32 s68, s15, 1
	s_add_u32 s0, s48, 0x1000
	s_addc_u32 s1, s49, 0
	s_or_b32 s16, s68, 1
	s_add_u32 s52, s48, 0x1400
	s_addc_u32 s53, s49, 0
	s_waitcnt lgkmcnt(0)
	v_mov_b32_e32 v240, v127
	v_mov_b32_e32 v241, v127
	v_mov_b32_e32 v242, v127
	v_mov_b32_e32 v243, v127
	s_waitcnt lgkmcnt(0)
	s_barrier
	s_mul_i32 s17, s16, 0x178000
	s_add_u32 s10, s0, s17
	s_addc_u32 s11, s1, 0
	v_lshl_add_u64 v[20:21], s[10:11], 0, v[104:105]
	global_load_dwordx4 v[16:19], v[20:21], off
	v_add_co_u32_e32 v20, vcc, s86, v20
	v_add_u32_e32 v100, 0, v110
	s_nop 0
	v_addc_co_u32_e32 v21, vcc, 0, v21, vcc
	global_load_dwordx4 v[20:23], v[20:21], off
	v_add_u32_e32 v124, 0, v111
	s_waitcnt vmcnt(1)
	ds_write_b128 v100, v[16:19]
	s_waitcnt vmcnt(0)
	ds_write_b128 v124, v[20:23]
	s_waitcnt lgkmcnt(0)
	s_waitcnt lgkmcnt(0)
	s_barrier
	v_cndmask_b32_e64 v24, 0, 1, s[82:83]
	v_cmp_ne_u32_e64 s[10:11], 1, v24
	s_andn2_b64 vcc, exec, s[82:83]
	s_mul_i32 s15, s15, 0x2f0000
	s_cbranch_vccnz .LBB0_510
	s_add_u32 s12, s0, s15
	s_addc_u32 s13, s1, 0
	v_lshl_add_u64 v[16:17], s[12:13], 0, v[104:105]
	s_add_u32 s12, s52, s17
	v_add_co_u32_e32 v20, vcc, 0xbc000, v16
	s_addc_u32 s13, s53, 0
	s_nop 0
	v_addc_co_u32_e32 v21, vcc, 0, v17, vcc
	v_lshl_add_u64 v[24:25], s[12:13], 0, v[104:105]
	v_add_co_u32_e32 v28, vcc, 0xbc000, v24
	global_load_dwordx4 v[16:19], v[16:17], off
	s_nop 0
	global_load_dwordx4 v[20:23], v[20:21], off
	v_addc_co_u32_e32 v29, vcc, 0, v25, vcc
	global_load_dwordx4 v[24:27], v[24:25], off
	s_nop 0
	global_load_dwordx4 v[28:31], v[28:29], off
	s_waitcnt lgkmcnt(0)

.LBB0_512:
	v_lshlrev_b32_e32 v33, 1, v32
	v_and_b32_e32 v34, 3, v126
	v_ashrrev_i32_e32 v96, 4, v126
	v_and_or_b32 v33, v33, 24, v34
	v_lshlrev_b32_e32 v46, 8, v33
	v_xor_b32_e32 v33, v96, v32
	v_lshl_add_u32 v33, v33, 4, v46
	v_add_u32_e32 v34, 4, v96
	v_xor_b32_e32 v34, v34, v32
	v_add_u32_e32 v129, 0, v33
	v_lshl_add_u32 v38, v34, 4, v46
	ds_read_b128 v[34:37], v129
	v_add_u32_e32 v130, 0, v38
	ds_read_b128 v[38:41], v130
	v_add_u32_e32 v33, 8, v96
	s_waitcnt lgkmcnt(1)
	v_mfma_f32_16x16x32_bf16 v[34:37], v[34:37], v[0:3], v[240:243]
	v_xor_b32_e32 v33, v33, v32
	v_lshl_add_u32 v33, v33, 4, v46
	v_add_u32_e32 v131, 0, v33
	v_add_u32_e32 v33, 12, v96
	ds_read_b128 v[42:45], v131
	ds_read_b128 v[48:51], v129 offset:1024
	v_xor_b32_e32 v47, v33, v32
	s_waitcnt lgkmcnt(2)
	v_mfma_f32_16x16x32_bf16 v[32:35], v[38:41], v[4:7], v[34:37]
	ds_read_b128 v[52:55], v130 offset:1024
	s_and_b64 vcc, exec, s[10:11]
	s_nop 0
	v_lshl_add_u32 v36, v47, 4, v46
	v_add_u32_e32 v132, 0, v36
	ds_read_b128 v[36:39], v131 offset:1024
	s_waitcnt lgkmcnt(3)
	v_mfma_f32_16x16x32_bf16 v[32:35], v[42:45], v[8:11], v[32:35]
	ds_read_b128 v[40:43], v132
	ds_read_b128 v[56:59], v132 offset:1024
	s_waitcnt lgkmcnt(1)
	v_mfma_f32_16x16x32_bf16 v[44:47], v[40:43], v[12:15], v[32:35]
	v_mfma_f32_16x16x32_bf16 v[32:35], v[48:51], v[0:3], v[240:243]
	v_mfma_f32_16x16x32_bf16 v[32:35], v[52:55], v[4:7], v[32:35]
	v_mfma_f32_16x16x32_bf16 v[32:35], v[36:39], v[8:11], v[32:35]
	s_waitcnt lgkmcnt(0)
	v_mfma_f32_16x16x32_bf16 v[40:43], v[56:59], v[12:15], v[32:35]
	s_nop 5
	ds_read_b128 v[32:35], v129 offset:8192
	ds_read_b128 v[48:51], v129 offset:9216
	ds_read_b128 v[36:39], v130 offset:8192
	ds_read_b128 v[52:55], v130 offset:9216
	s_waitcnt lgkmcnt(3)
	v_mfma_f32_16x16x32_bf16 v[32:35], v[32:35], v[0:3], v[240:243]
	s_waitcnt lgkmcnt(1)
	v_mfma_f32_16x16x32_bf16 v[32:35], v[36:39], v[4:7], v[32:35]
	ds_read_b128 v[36:39], v131 offset:8192
	ds_read_b128 v[56:59], v131 offset:9216
	s_waitcnt lgkmcnt(1)
	v_mfma_f32_16x16x32_bf16 v[32:35], v[36:39], v[8:11], v[32:35]
	ds_read_b128 v[36:39], v132 offset:8192
	ds_read_b128 v[60:63], v132 offset:9216
	s_waitcnt lgkmcnt(1)
	v_mfma_f32_16x16x32_bf16 v[36:39], v[36:39], v[12:15], v[32:35]
	v_mfma_f32_16x16x32_bf16 v[32:35], v[48:51], v[0:3], v[240:243]
	v_mfma_f32_16x16x32_bf16 v[32:35], v[52:55], v[4:7], v[32:35]
	v_mfma_f32_16x16x32_bf16 v[32:35], v[56:59], v[8:11], v[32:35]
	s_waitcnt lgkmcnt(0)
	v_mfma_f32_16x16x32_bf16 v[32:35], v[60:63], v[12:15], v[32:35]
	s_cbranch_vccnz .LBB0_514
	v_add_u32_e32 v48, 0, v109
	s_waitcnt vmcnt(3)
	ds_write_b128 v100, v[16:19] offset:16384
	s_waitcnt vmcnt(2)
	ds_write_b128 v124, v[20:23] offset:16384
	s_waitcnt vmcnt(1)
	ds_write_b128 v48, v[24:27] offset:32768
	v_add_u32_e32 v48, 0, v112
	s_waitcnt vmcnt(0)
	ds_write_b128 v48, v[28:31] offset:32768

.LBB0_520:
	v_sub_f32_e32 v44, v44, v60
	v_exp_f32_e32 v44, v44
	v_sub_f32_e32 v45, v45, v61
	v_cmp_le_i32_e32 vcc, v64, v125
	v_exp_f32_e32 v45, v45
	v_bfe_u32 v84, v126, 1, 1
	v_cndmask_b32_e32 v97, 0, v44, vcc
	v_sub_f32_e32 v44, v46, v62
	v_exp_f32_e32 v44, v44
	v_cmp_lt_i32_e32 vcc, v64, v125
	v_sub_f32_e32 v46, v47, v63
	v_cndmask_b32_e32 v98, 0, v45, vcc
	v_or_b32_e32 v45, 2, v64
	v_cmp_le_i32_e32 vcc, v45, v125
	v_exp_f32_e32 v46, v46
	v_cndmask_b32_e32 v99, 0, v44, vcc
	v_or_b32_e32 v44, 3, v64
	v_cmp_le_i32_e32 vcc, v44, v125
	v_sub_f32_e32 v40, v40, v56
	v_exp_f32_e32 v40, v40
	v_or_b32_e32 v44, 4, v64
	v_sub_f32_e32 v41, v41, v57
	v_cndmask_b32_e32 v150, 0, v46, vcc
	v_exp_f32_e32 v41, v41
	v_cmp_le_i32_e32 vcc, v44, v125
	v_or_b32_e32 v68, 10, v84
	v_cvt_pk_bf16_f32 v44, v97, v98
	v_cndmask_b32_e32 v151, 0, v40, vcc
	v_or_b32_e32 v40, 5, v64
	v_cmp_le_i32_e32 vcc, v40, v125
	v_sub_f32_e32 v40, v42, v58
	v_cndmask_b32_e32 v152, 0, v41, vcc
	v_exp_f32_e32 v40, v40
	v_or_b32_e32 v41, 6, v64
	v_sub_f32_e32 v42, v43, v59
	v_cmp_le_i32_e32 vcc, v41, v125
	v_exp_f32_e32 v42, v42
	v_sub_f32_e32 v36, v36, v52
	v_exp_f32_e32 v36, v36
	v_cndmask_b32_e32 v153, 0, v40, vcc
	v_or_b32_e32 v40, 7, v64
	v_cmp_le_i32_e32 vcc, v40, v125
	v_add_u32_e32 v40, 32, v64
	v_cndmask_b32_e32 v154, 0, v42, vcc
	v_cmp_le_i32_e32 vcc, v40, v125
	v_sub_f32_e32 v37, v37, v53
	v_exp_f32_e32 v37, v37
	v_cndmask_b32_e32 v155, 0, v36, vcc
	v_add_u32_e32 v36, 33, v64
	v_cmp_le_i32_e32 vcc, v36, v125
	v_sub_f32_e32 v36, v38, v54
	v_exp_f32_e32 v36, v36
	v_cndmask_b32_e32 v156, 0, v37, vcc
	v_add_u32_e32 v37, 34, v64
	v_cmp_le_i32_e32 vcc, v37, v125
	v_sub_f32_e32 v38, v39, v55
	v_cndmask_b32_e32 v157, 0, v36, vcc
	v_add_u32_e32 v36, 35, v64
	v_cmp_le_i32_e32 vcc, v36, v125
	v_exp_f32_e32 v38, v38
	v_sub_f32_e32 v32, v32, v48
	v_exp_f32_e32 v32, v32
	v_add_u32_e32 v36, 36, v64
	v_cndmask_b32_e32 v158, 0, v38, vcc
	v_cmp_le_i32_e32 vcc, v36, v125
	v_sub_f32_e32 v33, v33, v49
	v_exp_f32_e32 v33, v33
	v_cndmask_b32_e32 v159, 0, v32, vcc
	v_add_u32_e32 v32, 37, v64
	v_cmp_le_i32_e32 vcc, v32, v125
	v_sub_f32_e32 v32, v34, v50
	v_exp_f32_e32 v32, v32
	v_sub_f32_e32 v34, v35, v51
	v_cndmask_b32_e32 v160, 0, v33, vcc
	v_add_u32_e32 v33, 38, v64
	v_exp_f32_e32 v34, v34
	v_cmp_le_i32_e32 vcc, v33, v125
	v_lshrrev_b32_e32 v33, 1, v126
	v_and_b32_e32 v33, 0x7ffffff8, v33
	v_cndmask_b32_e32 v161, 0, v32, vcc
	v_add_u32_e32 v32, 39, v64
	v_cmp_le_i32_e32 vcc, v32, v125
	v_bfe_u32 v32, v126, 2, 2
	v_lshlrev_b32_e32 v85, 2, v32
	v_cndmask_b32_e32 v162, 0, v34, vcc
	v_lshlrev_b32_e32 v34, 3, v126
	v_and_b32_e32 v92, 8, v34
	v_or_b32_e32 v34, v33, v32
	v_or_b32_e32 v33, 4, v33
	v_or_b32_e32 v32, v33, v32
	v_bfe_u32 v88, v33, 2, 2
	v_lshlrev_b32_e32 v86, 8, v34
	v_lshrrev_b32_e32 v34, 3, v126
	v_lshlrev_b32_e32 v93, 8, v32
	v_bitop3_b32 v32, v88, v84, v85 bitop3:0x36
	v_and_b32_e32 v87, 2, v34
	v_lshlrev_b32_e32 v32, 4, v32
	v_or_b32_e32 v34, v85, v87
	v_or3_b32 v61, v32, v93, v92
	v_or_b32_e32 v32, 2, v84
	v_or_b32_e32 v34, v34, v84
	v_bitop3_b32 v33, v85, v32, v87 bitop3:0x36
	v_lshlrev_b32_e32 v34, 4, v34
	v_lshlrev_b32_e32 v33, 4, v33
	v_or3_b32 v60, v34, v86, v92
	v_or3_b32 v62, v33, v86, v92
	v_bitop3_b32 v36, v88, v32, v85 bitop3:0x36
	ds_read_b128 v[32:35], v129 offset:16384
	v_lshlrev_b32_e32 v36, 4, v36
	v_or3_b32 v63, v36, v93, v92
	ds_read_b128 v[36:39], v130 offset:16384
	s_waitcnt lgkmcnt(1)
	v_mfma_f32_16x16x32_bf16 v[32:35], v[32:35], v[0:3], v[240:243]
	v_or_b32_e32 v64, 4, v84
	v_bitop3_b32 v40, v85, v64, v87 bitop3:0x36
	v_lshlrev_b32_e32 v52, 4, v40
	ds_read_b128 v[40:43], v131 offset:16384
	ds_read_b128 v[48:51], v129 offset:17408
	s_waitcnt lgkmcnt(2)
	v_mfma_f32_16x16x32_bf16 v[32:35], v[36:39], v[4:7], v[32:35]
	v_or3_b32 v89, v52, v86, v92
	ds_read_b128 v[52:55], v132 offset:16384
	ds_read_b128 v[56:59], v130 offset:17408
	v_bitop3_b32 v36, v88, v64, v85 bitop3:0x36
	s_waitcnt lgkmcnt(3)
	v_mfma_f32_16x16x32_bf16 v[32:35], v[40:43], v[8:11], v[32:35]
	v_lshlrev_b32_e32 v64, 4, v36
	v_or3_b32 v90, v64, v93, v92
	v_or_b32_e32 v64, 6, v84
	s_waitcnt lgkmcnt(1)
	v_mfma_f32_16x16x32_bf16 v[76:79], v[52:55], v[12:15], v[32:35]
	ds_read_b128 v[36:39], v131 offset:17408
	ds_read_b128 v[40:43], v132 offset:17408
	v_or_b32_e32 v52, 8, v84
	v_bitop3_b32 v32, v85, v64, v87 bitop3:0x36
	v_lshlrev_b32_e32 v32, 4, v32
	v_or3_b32 v91, v32, v86, v92
	v_mfma_f32_16x16x32_bf16 v[32:35], v[48:51], v[0:3], v[240:243]
	v_bitop3_b32 v48, v88, v64, v85 bitop3:0x36
	v_lshlrev_b32_e32 v48, 4, v48
	v_or3_b32 v94, v48, v93, v92
	s_waitcnt lgkmcnt(2)
	v_mfma_f32_16x16x32_bf16 v[32:35], v[56:59], v[4:7], v[32:35]
	ds_read_b128 v[48:51], v129 offset:24576
	v_bitop3_b32 v53, v85, v52, v87 bitop3:0x36
	v_bitop3_b32 v52, v88, v52, v85 bitop3:0x36
	s_waitcnt lgkmcnt(2)
	v_mfma_f32_16x16x32_bf16 v[32:35], v[36:39], v[8:11], v[32:35]
	v_lshlrev_b32_e32 v36, 4, v53
	v_or3_b32 v95, v36, v86, v92
	ds_read_b128 v[36:39], v130 offset:24576
	s_waitcnt lgkmcnt(1)
	v_mfma_f32_16x16x32_bf16 v[48:51], v[48:51], v[0:3], v[240:243]
	v_lshlrev_b32_e32 v64, 4, v52
	v_or3_b32 v133, v64, v93, v92
	v_add_u32_e32 v142, 0, v60
	v_mfma_f32_16x16x32_bf16 v[72:75], v[40:43], v[12:15], v[32:35]
	s_nop 2
	ds_read_b128 v[32:35], v131 offset:24576
	ds_read_b128 v[40:43], v129 offset:25600
	ds_read_b128 v[52:55], v132 offset:24576
	ds_read_b128 v[56:59], v130 offset:25600
	v_add_u32_e32 v146, 0, v61
	s_waitcnt lgkmcnt(4)
	v_mfma_f32_16x16x32_bf16 v[36:39], v[36:39], v[4:7], v[48:51]
	v_cvt_pk_bf16_f32 v45, v99, v150
	v_cvt_pk_bf16_f32 v46, v151, v152
	v_cvt_pk_bf16_f32 v47, v153, v154
	s_waitcnt lgkmcnt(3)
	v_mfma_f32_16x16x32_bf16 v[32:35], v[32:35], v[8:11], v[36:39]
	ds_read_b128 v[48:51], v131 offset:25600
	v_add_u32_e32 v136, 0, v62
	v_add_u32_e32 v137, 0, v63
	s_waitcnt lgkmcnt(2)
	v_mfma_f32_16x16x32_bf16 v[64:67], v[52:55], v[12:15], v[32:35]
	v_bitop3_b32 v36, v85, v68, v87 bitop3:0x36
	v_lshlrev_b32_e32 v69, 4, v36
	ds_read_b128 v[36:39], v132 offset:25600
	v_bitop3_b32 v32, v88, v68, v85 bitop3:0x36
	v_lshlrev_b32_e32 v52, 4, v32
	v_mfma_f32_16x16x32_bf16 v[32:35], v[40:43], v[0:3], v[240:243]
	v_or_b32_e32 v40, 12, v84
	v_bitop3_b32 v41, v85, v40, v87 bitop3:0x36
	v_lshlrev_b32_e32 v41, 4, v41
	s_waitcnt lgkmcnt(2)
	v_mfma_f32_16x16x32_bf16 v[32:35], v[56:59], v[4:7], v[32:35]
	v_or3_b32 v135, v52, v93, v92
	v_or3_b32 v138, v41, v86, v92
	v_bitop3_b32 v52, v88, v40, v85 bitop3:0x36
	s_waitcnt lgkmcnt(1)
	v_mfma_f32_16x16x32_bf16 v[32:35], v[48:51], v[8:11], v[32:35]
	ds_read_b64_tr_b16 v[40:41], v142 offset:32768
	ds_read_b64_tr_b16 v[42:43], v146 offset:32768
	v_or3_b32 v134, v69, v86, v92
	v_cvt_pk_bf16_f32 v80, v155, v156
	s_waitcnt lgkmcnt(2)
	v_mfma_f32_16x16x32_bf16 v[68:71], v[36:39], v[12:15], v[32:35]
	s_nop 2
	ds_read_b64_tr_b16 v[34:35], v146 offset:40960
	ds_read_b64_tr_b16 v[32:33], v142 offset:40960
	ds_read_b64_tr_b16 v[36:37], v136 offset:32768
	ds_read_b64_tr_b16 v[38:39], v137 offset:32768
	v_cvt_pk_bf16_f32 v81, v157, v158
	s_waitcnt lgkmcnt(4)
	v_mfma_f32_16x16x32_bf16 v[40:43], v[40:43], v[44:47], 0
	v_cvt_pk_bf16_f32 v82, v159, v160
	v_cvt_pk_bf16_f32 v83, v161, v162
	v_add_u32_e32 v139, 0, v89
	ds_read_b64_tr_b16 v[50:51], v137 offset:40960
	ds_read_b64_tr_b16 v[48:49], v136 offset:40960
	s_waitcnt lgkmcnt(4)
	v_mfma_f32_16x16x32_bf16 v[60:63], v[32:35], v[80:83], v[40:43]
	v_add_u32_e32 v145, 0, v90
	ds_read_b64_tr_b16 v[32:33], v139 offset:32768
	ds_read_b64_tr_b16 v[34:35], v145 offset:32768
	ds_read_b64_tr_b16 v[42:43], v145 offset:40960
	ds_read_b64_tr_b16 v[40:41], v139 offset:40960
	s_waitcnt lgkmcnt(6)
	v_mfma_f32_16x16x32_bf16 v[36:39], v[36:39], v[44:47], 0
	v_add_u32_e32 v140, 0, v91
	v_lshlrev_b32_e32 v56, 4, v52
	v_add_u32_e32 v147, 0, v94
	s_waitcnt lgkmcnt(4)
	v_mfma_f32_16x16x32_bf16 v[52:55], v[48:51], v[80:83], v[36:39]
	s_nop 2
	ds_read_b64_tr_b16 v[36:37], v140 offset:32768
	ds_read_b64_tr_b16 v[38:39], v147 offset:32768
	v_or3_b32 v89, v56, v93, v92
	v_or_b32_e32 v56, 14, v84
	s_waitcnt lgkmcnt(4)
	v_mfma_f32_16x16x32_bf16 v[32:35], v[32:35], v[44:47], 0
	v_bitop3_b32 v57, v85, v56, v87 bitop3:0x36
	v_add_u32_e32 v148, 0, v95
	v_add_u32_e32 v149, 0, v133
	s_waitcnt lgkmcnt(2)
	v_mfma_f32_16x16x32_bf16 v[48:51], v[40:43], v[80:83], v[32:35]
	s_nop 2
	ds_read_b64_tr_b16 v[34:35], v147 offset:40960
	ds_read_b64_tr_b16 v[32:33], v140 offset:40960
	v_lshlrev_b32_e32 v40, 4, v57
	v_or3_b32 v94, v40, v86, v92
	s_waitcnt lgkmcnt(2)
	v_mfma_f32_16x16x32_bf16 v[36:39], v[36:39], v[44:47], 0
	ds_read_b64_tr_b16 v[40:41], v148 offset:32768
	ds_read_b64_tr_b16 v[42:43], v149 offset:32768
	v_add_u32_e32 v133, 0, v134
	v_bitop3_b32 v88, v88, v56, v85 bitop3:0x36
	s_waitcnt lgkmcnt(2)
	v_mfma_f32_16x16x32_bf16 v[56:59], v[32:35], v[80:83], v[36:39]
	ds_read_b64_tr_b16 v[34:35], v149 offset:40960
	ds_read_b64_tr_b16 v[32:33], v148 offset:40960
	v_add_u32_e32 v134, 0, v135
	ds_read_b64_tr_b16 v[36:37], v133 offset:32768
	ds_read_b64_tr_b16 v[38:39], v134 offset:32768
	s_waitcnt lgkmcnt(4)
	v_mfma_f32_16x16x32_bf16 v[40:43], v[40:43], v[44:47], 0
	ds_read_b64_tr_b16 v[86:87], v134 offset:40960
	ds_read_b64_tr_b16 v[84:85], v133 offset:40960
	v_add_u32_e32 v135, 0, v138
	v_add_u32_e32 v138, 0, v89
	s_waitcnt lgkmcnt(4)
	v_mfma_f32_16x16x32_bf16 v[32:35], v[32:35], v[80:83], v[40:43]
	s_nop 2
	ds_read_b64_tr_b16 v[40:41], v135 offset:32768
	ds_read_b64_tr_b16 v[42:43], v138 offset:32768
	v_lshlrev_b32_e32 v95, 4, v88
	ds_read_b64_tr_b16 v[90:91], v138 offset:40960
	ds_read_b64_tr_b16 v[88:89], v135 offset:40960
	s_waitcnt lgkmcnt(6)
	v_mfma_f32_16x16x32_bf16 v[36:39], v[36:39], v[44:47], 0
	v_add_u32_e32 v141, 0, v94
	s_and_b64 vcc, exec, s[10:11]
	s_waitcnt lgkmcnt(4)
	v_mfma_f32_16x16x32_bf16 v[36:39], v[84:87], v[80:83], v[36:39]
	v_or3_b32 v84, v95, v93, v92
	v_add_u32_e32 v143, 0, v84
	ds_read_b64_tr_b16 v[84:85], v141 offset:32768
	ds_read_b64_tr_b16 v[86:87], v143 offset:32768
	s_waitcnt lgkmcnt(4)
	v_mfma_f32_16x16x32_bf16 v[40:43], v[40:43], v[44:47], 0
	s_waitcnt lgkmcnt(2)
	v_mfma_f32_16x16x32_bf16 v[40:43], v[88:91], v[80:83], v[40:43]
	ds_read_b64_tr_b16 v[90:91], v143 offset:40960
	ds_read_b64_tr_b16 v[88:89], v141 offset:40960
	s_waitcnt lgkmcnt(2)
	v_mfma_f32_16x16x32_bf16 v[44:47], v[84:87], v[44:47], 0
	s_waitcnt lgkmcnt(0)
	v_mfma_f32_16x16x32_bf16 v[44:47], v[88:91], v[80:83], v[44:47]
	s_cbranch_vccnz .LBB0_522
	v_add_u32_e32 v80, 0, v109
	s_waitcnt vmcnt(3)
	ds_write_b128 v100, v[16:19]
	s_waitcnt vmcnt(2)
	ds_write_b128 v124, v[20:23]
	s_waitcnt vmcnt(1)
	ds_write_b128 v80, v[24:27] offset:49152
	v_add_u32_e32 v80, 0, v112
	s_waitcnt vmcnt(0)
	ds_write_b128 v80, v[28:31] offset:49152

.LBB0_526:
	s_waitcnt lgkmcnt(2)
	v_sub_f32_e32 v72, v72, v88
	v_sub_f32_e32 v73, v73, v89
	v_sub_f32_e32 v74, v74, v90
	v_sub_f32_e32 v75, v75, v91
	v_add_f32_e32 v88, 0, v97
	v_add_f32_e32 v88, v98, v88
	v_add_f32_e32 v88, v99, v88
	v_add_f32_e32 v88, v150, v88
	v_add_f32_e32 v88, v151, v88
	v_add_f32_e32 v88, v152, v88
	v_add_f32_e32 v88, v153, v88
	v_add_f32_e32 v88, v154, v88
	v_add_f32_e32 v88, v155, v88
	v_sub_f32_e32 v76, v76, v92
	s_waitcnt lgkmcnt(1)
	v_add_f32_e32 v88, v156, v88
	v_sub_f32_e32 v77, v77, v93
	v_sub_f32_e32 v64, v64, v84
	v_add_f32_e32 v88, v157, v88
	v_exp_f32_e32 v76, v76
	v_exp_f32_e32 v77, v77
	v_exp_f32_e32 v64, v64
	v_add_f32_e32 v88, v158, v88
	v_sub_f32_e32 v78, v78, v94
	v_add_f32_e32 v88, v159, v88
	v_exp_f32_e32 v78, v78
	v_sub_f32_e32 v79, v79, v95
	v_sub_f32_e32 v65, v65, v85
	v_add_f32_e32 v88, v160, v88
	v_exp_f32_e32 v79, v79
	v_sub_f32_e32 v66, v66, v86
	v_add_f32_e32 v88, v161, v88
	v_cndmask_b32_e64 v76, 0, v76, s[40:41]
	v_cndmask_b32_e64 v77, 0, v77, s[42:43]
	v_exp_f32_e32 v72, v72
	v_exp_f32_e32 v73, v73
	v_exp_f32_e32 v66, v66
	v_sub_f32_e32 v67, v67, v87
	v_cndmask_b32_e64 v84, 0, v64, s[22:23]
	s_waitcnt lgkmcnt(0)
	v_add_f32_e32 v88, v162, v88
	v_sub_f32_e32 v64, v68, v80
	v_cvt_pk_bf16_f32 v68, v76, v77
	v_add_f32_e32 v76, v88, v76
	v_cndmask_b32_e64 v78, 0, v78, s[44:45]
	v_exp_f32_e32 v74, v74
	v_add_f32_e32 v76, v77, v76
	v_cndmask_b32_e64 v79, 0, v79, s[46:47]
	v_exp_f32_e32 v75, v75
	v_exp_f32_e32 v65, v65
	v_add_f32_e32 v76, v78, v76
	v_cndmask_b32_e64 v72, 0, v72, s[30:31]
	v_cndmask_b32_e64 v73, 0, v73, s[34:35]
	v_cndmask_b32_e64 v86, 0, v66, s[26:27]
	v_add_f32_e32 v76, v79, v76
	v_exp_f32_e32 v67, v67
	v_sub_f32_e32 v66, v70, v82
	v_cvt_pk_bf16_f32 v70, v72, v73
	v_add_f32_e32 v72, v72, v76
	v_cndmask_b32_e64 v74, 0, v74, s[36:37]
	v_add_f32_e32 v72, v73, v72
	v_cndmask_b32_e64 v75, 0, v75, s[38:39]
	v_cndmask_b32_e64 v85, 0, v65, s[24:25]
	v_add_f32_e32 v72, v74, v72
	v_exp_f32_e32 v64, v64
	v_sub_f32_e32 v65, v69, v81
	v_add_f32_e32 v72, v75, v72
	v_cndmask_b32_e64 v87, 0, v67, s[28:29]
	v_exp_f32_e32 v65, v65
	v_add_f32_e32 v72, v84, v72
	v_exp_f32_e32 v66, v66
	v_sub_f32_e32 v67, v71, v83
	v_add_f32_e32 v72, v85, v72
	v_exp_f32_e32 v67, v67
	v_add_f32_e32 v72, v86, v72
	v_cndmask_b32_e64 v80, 0, v64, s[14:15]
	v_add_f32_e32 v72, v87, v72
	v_cndmask_b32_e64 v81, 0, v65, s[16:17]
	v_add_f32_e32 v72, v80, v72
	v_cndmask_b32_e64 v82, 0, v66, s[18:19]
	v_add_f32_e32 v72, v81, v72
	v_cndmask_b32_e64 v83, 0, v67, s[20:21]
	v_add_f32_e32 v72, v82, v72
	v_cvt_pk_bf16_f32 v69, v78, v79
	v_cvt_pk_bf16_f32 v71, v74, v75
	v_cvt_pk_bf16_f32 v64, v84, v85
	v_cvt_pk_bf16_f32 v65, v86, v87
	v_cvt_pk_bf16_f32 v66, v80, v81
	v_cvt_pk_bf16_f32 v67, v82, v83
	v_add_f32_e32 v150, v83, v72
	s_waitcnt lgkmcnt(0)
	s_barrier
	v_lshlrev_b32_e32 v151, 5, v96
	s_mov_b32 s17, 2
	s_mov_b32 s14, s4
	s_mov_b32 s15, s8
	s_mov_b32 s16, s7
	s_and_b64 vcc, exec, s[12:13]
	s_cbranch_vccnz .LBB0_528

.LBB0_528:
	ds_read_b128 v[88:91], v129
	ds_read_b128 v[92:95], v129 offset:1024
	ds_read_b128 v[96:99], v130
	ds_read_b128 v[152:155], v130 offset:1024
	ds_read_b128 v[176:179], v131
	ds_read_b128 v[180:183], v131 offset:1024
	ds_read_b128 v[184:187], v132
	ds_read_b128 v[188:191], v132 offset:1024
	ds_read_b128 v[192:195], v129 offset:8192
	ds_read_b128 v[196:199], v129 offset:9216
	ds_read_b128 v[200:203], v130 offset:8192
	ds_read_b128 v[204:207], v130 offset:9216
	ds_read_b128 v[208:211], v131 offset:8192
	ds_read_b128 v[212:215], v131 offset:9216
	ds_read_b128 v[216:219], v132 offset:8192
	s_and_b64 vcc, exec, s[10:11]
	s_waitcnt lgkmcnt(11)
	v_mfma_f32_16x16x32_bf16 v[72:75], v[88:91], v[0:3], v[240:243]
	ds_read_b128 v[220:223], v132 offset:9216
	ds_read_b64_tr_b16 v[224:225], v142 offset:49152
	ds_read_b64_tr_b16 v[226:227], v146 offset:49152
	ds_read_b64_tr_b16 v[230:231], v146 offset:57344
	v_mfma_f32_16x16x32_bf16 v[72:75], v[96:99], v[4:7], v[72:75]
	v_mfma_f32_16x16x32_bf16 v[76:79], v[92:95], v[0:3], v[240:243]
	s_waitcnt lgkmcnt(11)
	v_mfma_f32_16x16x32_bf16 v[72:75], v[176:179], v[8:11], v[72:75]
	ds_read_b64_tr_b16 v[228:229], v142 offset:57344
	ds_read_b64_tr_b16 v[88:89], v136 offset:49152
	ds_read_b64_tr_b16 v[90:91], v137 offset:49152
	ds_read_b64_tr_b16 v[98:99], v137 offset:57344
	v_mfma_f32_16x16x32_bf16 v[84:87], v[184:187], v[12:15], v[72:75]
	v_mfma_f32_16x16x32_bf16 v[72:75], v[152:155], v[4:7], v[76:79]
	v_mfma_f32_16x16x32_bf16 v[72:75], v[180:183], v[8:11], v[72:75]
	v_mfma_f32_16x16x32_bf16 v[80:83], v[188:191], v[12:15], v[72:75]
	s_waitcnt lgkmcnt(11)
	s_nop 5
	v_mfma_f32_16x16x32_bf16 v[72:75], v[192:195], v[0:3], v[240:243]
	ds_read_b64_tr_b16 v[96:97], v136 offset:57344
	ds_read_b64_tr_b16 v[92:93], v139 offset:49152
	ds_read_b64_tr_b16 v[94:95], v145 offset:49152
	ds_read_b64_tr_b16 v[178:179], v145 offset:57344
	v_mfma_f32_16x16x32_bf16 v[72:75], v[200:203], v[4:7], v[72:75]
	s_waitcnt lgkmcnt(11)
	v_mfma_f32_16x16x32_bf16 v[72:75], v[208:211], v[8:11], v[72:75]
	ds_read_b64_tr_b16 v[176:177], v139 offset:57344
	ds_read_b64_tr_b16 v[184:185], v140 offset:49152
	ds_read_b64_tr_b16 v[186:187], v147 offset:49152
	ds_read_b64_tr_b16 v[154:155], v147 offset:57344
	v_mfma_f32_16x16x32_bf16 v[76:79], v[216:219], v[12:15], v[72:75]
	v_mfma_f32_16x16x32_bf16 v[72:75], v[196:199], v[0:3], v[240:243]
	v_mfma_f32_16x16x32_bf16 v[72:75], v[204:207], v[4:7], v[72:75]
	s_waitcnt lgkmcnt(10)
	v_mfma_f32_16x16x32_bf16 v[60:63], v[224:227], v[68:71], v[60:63]
	ds_read_b64_tr_b16 v[152:153], v140 offset:57344
	ds_read_b64_tr_b16 v[180:181], v148 offset:49152
	ds_read_b64_tr_b16 v[182:183], v149 offset:49152
	ds_read_b64_tr_b16 v[190:191], v149 offset:57344
	ds_read_b64_tr_b16 v[188:189], v148 offset:57344
	v_mfma_f32_16x16x32_bf16 v[60:63], v[228:231], v[64:67], v[60:63]
	s_waitcnt lgkmcnt(11)
	v_mfma_f32_16x16x32_bf16 v[52:55], v[88:91], v[68:71], v[52:55]
	ds_read_b64_tr_b16 v[192:193], v133 offset:49152
	ds_read_b64_tr_b16 v[194:195], v134 offset:49152
	ds_read_b64_tr_b16 v[202:203], v134 offset:57344
	ds_read_b64_tr_b16 v[200:201], v133 offset:57344
	v_mfma_f32_16x16x32_bf16 v[52:55], v[96:99], v[64:67], v[52:55]
	s_waitcnt lgkmcnt(11)
	v_mfma_f32_16x16x32_bf16 v[48:51], v[92:95], v[68:71], v[48:51]
	ds_read_b64_tr_b16 v[208:209], v135 offset:49152
	ds_read_b64_tr_b16 v[210:211], v138 offset:49152
	ds_read_b64_tr_b16 v[218:219], v138 offset:57344
	ds_read_b64_tr_b16 v[216:217], v135 offset:57344
	v_mfma_f32_16x16x32_bf16 v[48:51], v[176:179], v[64:67], v[48:51]
	s_waitcnt lgkmcnt(11)
	v_mfma_f32_16x16x32_bf16 v[56:59], v[184:187], v[68:71], v[56:59]
	ds_read_b64_tr_b16 v[196:197], v141 offset:49152
	ds_read_b64_tr_b16 v[198:199], v143 offset:49152
	ds_read_b64_tr_b16 v[206:207], v143 offset:57344
	ds_read_b64_tr_b16 v[204:205], v141 offset:57344
	v_mfma_f32_16x16x32_bf16 v[56:59], v[152:155], v[64:67], v[56:59]
	s_waitcnt lgkmcnt(11)
	v_mfma_f32_16x16x32_bf16 v[32:35], v[180:183], v[68:71], v[32:35]
	v_mfma_f32_16x16x32_bf16 v[32:35], v[188:191], v[64:67], v[32:35]
	s_waitcnt lgkmcnt(7)
	v_mfma_f32_16x16x32_bf16 v[36:39], v[192:195], v[68:71], v[36:39]
	v_mfma_f32_16x16x32_bf16 v[36:39], v[200:203], v[64:67], v[36:39]
	s_waitcnt lgkmcnt(3)
	v_mfma_f32_16x16x32_bf16 v[40:43], v[208:211], v[68:71], v[40:43]
	v_mfma_f32_16x16x32_bf16 v[40:43], v[216:219], v[64:67], v[40:43]
	v_mfma_f32_16x16x32_bf16 v[72:75], v[212:215], v[8:11], v[72:75]
	s_waitcnt lgkmcnt(0)
	v_mfma_f32_16x16x32_bf16 v[44:47], v[196:199], v[68:71], v[44:47]
	v_mfma_f32_16x16x32_bf16 v[72:75], v[220:223], v[12:15], v[72:75]
	v_mfma_f32_16x16x32_bf16 v[44:47], v[204:207], v[64:67], v[44:47]
	s_cbranch_vccnz .LBB0_530
	v_add_u32_e32 v64, 0, v109
	s_waitcnt vmcnt(3)
	ds_write_b128 v100, v[16:19] offset:16384
	s_waitcnt vmcnt(2)
	ds_write_b128 v124, v[20:23] offset:16384
	s_waitcnt vmcnt(1)
	ds_write_b128 v64, v[24:27] offset:32768
	v_add_u32_e32 v64, 0, v112
	s_waitcnt vmcnt(0)
	ds_write_b128 v64, v[28:31] offset:32768

.LBB0_536:
	ds_read_b128 v[168:171], v129 offset:16384
	ds_read_b128 v[172:175], v130 offset:16384
	ds_read_b128 v[176:179], v131 offset:16384
	ds_read_b128 v[180:183], v129 offset:17408
	ds_read_b128 v[184:187], v132 offset:16384
	ds_read_b128 v[188:191], v130 offset:17408
	ds_read_b128 v[192:195], v131 offset:17408
	ds_read_b128 v[196:199], v129 offset:24576
	ds_read_b128 v[200:203], v132 offset:17408
	ds_read_b128 v[204:207], v130 offset:24576
	ds_read_b128 v[208:211], v131 offset:24576
	ds_read_b128 v[212:215], v129 offset:25600
	ds_read_b128 v[216:219], v132 offset:24576
	ds_read_b128 v[220:223], v130 offset:25600
	ds_read_b128 v[224:227], v131 offset:25600
	v_sub_f32_e32 v64, v84, v96
	v_exp_f32_e32 v96, v64
	v_sub_f32_e32 v64, v85, v97
	v_exp_f32_e32 v97, v64
	v_sub_f32_e32 v64, v86, v98
	v_exp_f32_e32 v98, v64
	v_sub_f32_e32 v64, v87, v99
	v_exp_f32_e32 v99, v64
	v_sub_f32_e32 v64, v80, v92
	v_exp_f32_e32 v153, v64
	v_sub_f32_e32 v64, v81, v93
	v_exp_f32_e32 v154, v64
	v_sub_f32_e32 v64, v82, v94
	v_exp_f32_e32 v155, v64
	v_sub_f32_e32 v64, v83, v95
	s_waitcnt lgkmcnt(11)
	v_mfma_f32_16x16x32_bf16 v[84:87], v[168:171], v[0:3], v[240:243]
	ds_read_b128 v[228:231], v132 offset:25600
	ds_read_b64_tr_b16 v[168:169], v142 offset:32768
	ds_read_b64_tr_b16 v[170:171], v146 offset:32768
	v_exp_f32_e32 v156, v64
	v_sub_f32_e32 v64, v76, v88
	v_exp_f32_e32 v157, v64
	v_mfma_f32_16x16x32_bf16 v[92:95], v[180:183], v[0:3], v[240:243]
	ds_read_b64_tr_b16 v[182:183], v146 offset:40960
	v_sub_f32_e32 v64, v77, v89
	v_sub_f32_e32 v70, v73, v67
	v_mfma_f32_16x16x32_bf16 v[84:87], v[172:175], v[4:7], v[84:87]
	v_exp_f32_e32 v158, v64
	v_sub_f32_e32 v64, v78, v90
	v_exp_f32_e32 v159, v64
	v_sub_f32_e32 v64, v79, v91
	s_waitcnt lgkmcnt(10)
	v_mfma_f32_16x16x32_bf16 v[88:91], v[188:191], v[4:7], v[92:95]
	ds_read_b64_tr_b16 v[180:181], v142 offset:40960
	ds_read_b64_tr_b16 v[172:173], v136 offset:32768
	ds_read_b64_tr_b16 v[174:175], v137 offset:32768
	ds_read_b64_tr_b16 v[190:191], v137 offset:40960
	ds_read_b64_tr_b16 v[188:189], v136 offset:40960
	v_exp_f32_e32 v160, v64
	v_mfma_f32_16x16x32_bf16 v[80:83], v[176:179], v[8:11], v[84:87]
	v_sub_f32_e32 v64, v72, v66
	v_exp_f32_e32 v161, v64
	v_mfma_f32_16x16x32_bf16 v[76:79], v[192:195], v[8:11], v[88:91]
	v_sub_f32_e32 v68, v74, v68
	s_and_b64 vcc, exec, s[10:11]
	v_mfma_f32_16x16x32_bf16 v[92:95], v[196:199], v[0:3], v[240:243]
	v_mfma_f32_16x16x32_bf16 v[80:83], v[184:187], v[12:15], v[80:83]
	v_exp_f32_e32 v162, v70
	v_exp_f32_e32 v163, v68
	v_mfma_f32_16x16x32_bf16 v[76:79], v[200:203], v[12:15], v[76:79]
	s_waitcnt lgkmcnt(11)
	v_mfma_f32_16x16x32_bf16 v[88:91], v[204:207], v[4:7], v[92:95]
	ds_read_b64_tr_b16 v[176:177], v139 offset:32768
	ds_read_b64_tr_b16 v[178:179], v145 offset:32768
	ds_read_b64_tr_b16 v[194:195], v145 offset:40960
	ds_read_b64_tr_b16 v[192:193], v139 offset:40960
	v_sub_f32_e32 v68, v75, v69
	v_mfma_f32_16x16x32_bf16 v[84:87], v[208:211], v[8:11], v[88:91]
	v_cvt_pk_bf16_f32 v92, v96, v97
	v_cvt_pk_bf16_f32 v93, v98, v99
	v_cvt_pk_bf16_f32 v94, v153, v154
	v_mfma_f32_16x16x32_bf16 v[64:67], v[216:219], v[12:15], v[84:87]
	v_cvt_pk_bf16_f32 v95, v155, v156
	v_mfma_f32_16x16x32_bf16 v[84:87], v[212:215], v[0:3], v[240:243]
	v_exp_f32_e32 v164, v68
	s_waitcnt lgkmcnt(11)
	v_mfma_f32_16x16x32_bf16 v[84:87], v[220:223], v[4:7], v[84:87]
	ds_read_b64_tr_b16 v[196:197], v140 offset:32768
	ds_read_b64_tr_b16 v[198:199], v147 offset:32768
	ds_read_b64_tr_b16 v[186:187], v147 offset:40960
	ds_read_b64_tr_b16 v[184:185], v140 offset:40960
	v_mfma_f32_16x16x32_bf16 v[68:71], v[224:227], v[8:11], v[84:87]
	s_nop 2
	v_cvt_pk_bf16_f32 v84, v157, v158
	v_mfma_f32_16x16x32_bf16 v[68:71], v[228:231], v[12:15], v[68:71]
	v_cvt_pk_bf16_f32 v85, v159, v160
	v_cvt_pk_bf16_f32 v86, v161, v162
	s_waitcnt lgkmcnt(11)
	v_mfma_f32_16x16x32_bf16 v[60:63], v[168:171], v[92:95], v[60:63]
	ds_read_b64_tr_b16 v[200:201], v148 offset:32768
	ds_read_b64_tr_b16 v[202:203], v149 offset:32768
	ds_read_b64_tr_b16 v[206:207], v149 offset:40960
	ds_read_b64_tr_b16 v[204:205], v148 offset:40960
	v_cvt_pk_bf16_f32 v87, v163, v164
	s_nop 1
	v_mfma_f32_16x16x32_bf16 v[60:63], v[180:183], v[84:87], v[60:63]
	s_waitcnt lgkmcnt(11)
	v_mfma_f32_16x16x32_bf16 v[52:55], v[172:175], v[92:95], v[52:55]
	ds_read_b64_tr_b16 v[208:209], v133 offset:32768
	ds_read_b64_tr_b16 v[210:211], v134 offset:32768
	ds_read_b64_tr_b16 v[218:219], v134 offset:40960
	ds_read_b64_tr_b16 v[216:217], v133 offset:40960
	v_mfma_f32_16x16x32_bf16 v[52:55], v[188:191], v[84:87], v[52:55]
	s_waitcnt lgkmcnt(11)
	v_mfma_f32_16x16x32_bf16 v[48:51], v[176:179], v[92:95], v[48:51]
	ds_read_b64_tr_b16 v[212:213], v135 offset:32768
	ds_read_b64_tr_b16 v[214:215], v138 offset:32768
	ds_read_b64_tr_b16 v[222:223], v138 offset:40960
	ds_read_b64_tr_b16 v[220:221], v135 offset:40960
	v_mfma_f32_16x16x32_bf16 v[48:51], v[192:195], v[84:87], v[48:51]
	s_waitcnt lgkmcnt(11)
	v_mfma_f32_16x16x32_bf16 v[56:59], v[196:199], v[92:95], v[56:59]
	ds_read_b64_tr_b16 v[224:225], v141 offset:32768
	ds_read_b64_tr_b16 v[226:227], v143 offset:32768
	ds_read_b64_tr_b16 v[230:231], v143 offset:40960
	ds_read_b64_tr_b16 v[228:229], v141 offset:40960
	v_mfma_f32_16x16x32_bf16 v[56:59], v[184:187], v[84:87], v[56:59]
	s_waitcnt lgkmcnt(11)
	v_mfma_f32_16x16x32_bf16 v[32:35], v[200:203], v[92:95], v[32:35]
	v_mfma_f32_16x16x32_bf16 v[32:35], v[204:207], v[84:87], v[32:35]
	s_waitcnt lgkmcnt(7)
	v_mfma_f32_16x16x32_bf16 v[36:39], v[208:211], v[92:95], v[36:39]
	v_mfma_f32_16x16x32_bf16 v[36:39], v[216:219], v[84:87], v[36:39]
	s_waitcnt lgkmcnt(3)
	v_mfma_f32_16x16x32_bf16 v[40:43], v[212:215], v[92:95], v[40:43]
	v_mfma_f32_16x16x32_bf16 v[40:43], v[220:223], v[84:87], v[40:43]
	s_waitcnt lgkmcnt(0)
	v_mfma_f32_16x16x32_bf16 v[44:47], v[224:227], v[92:95], v[44:47]
	v_mfma_f32_16x16x32_bf16 v[44:47], v[228:231], v[84:87], v[44:47]
	s_cbranch_vccnz .LBB0_538
	v_add_u32_e32 v72, 0, v109
	s_waitcnt vmcnt(3)
	ds_write_b128 v100, v[16:19]
	s_waitcnt vmcnt(2)
	ds_write_b128 v124, v[20:23]
	s_waitcnt vmcnt(1)
	ds_write_b128 v72, v[24:27] offset:49152
	v_add_u32_e32 v72, 0, v112
	s_waitcnt vmcnt(0)
	ds_write_b128 v72, v[28:31] offset:49152

.LBB0_542:
	v_add_f32_e32 v96, v150, v96
	v_add_f32_e32 v96, v97, v96
	v_add_f32_e32 v96, v98, v96
	v_add_f32_e32 v96, v99, v96
	v_add_f32_e32 v96, v153, v96
	v_add_f32_e32 v96, v154, v96
	v_add_f32_e32 v96, v155, v96
	v_add_f32_e32 v96, v156, v96
	v_add_f32_e32 v96, v157, v96
	v_add_f32_e32 v96, v158, v96
	v_add_f32_e32 v96, v159, v96
	s_waitcnt lgkmcnt(3)
	v_add_f32_e32 v96, v160, v96
	v_sub_f32_e32 v80, v80, v92
	v_add_f32_e32 v96, v161, v96
	v_exp_f32_e32 v80, v80
	v_sub_f32_e32 v81, v81, v93
	v_add_f32_e32 v96, v162, v96
	v_exp_f32_e32 v81, v81
	v_sub_f32_e32 v82, v82, v94
	v_add_f32_e32 v96, v163, v96
	v_exp_f32_e32 v82, v82
	v_sub_f32_e32 v83, v83, v95
	s_waitcnt lgkmcnt(2)
	v_add_f32_e32 v96, v164, v96
	v_exp_f32_e32 v83, v83
	v_sub_f32_e32 v76, v76, v88
	v_add_f32_e32 v92, v96, v80
	v_exp_f32_e32 v76, v76
	v_sub_f32_e32 v77, v77, v89
	v_add_f32_e32 v92, v81, v92
	v_exp_f32_e32 v77, v77
	v_sub_f32_e32 v78, v78, v90
	v_add_f32_e32 v92, v82, v92
	v_exp_f32_e32 v78, v78
	v_sub_f32_e32 v79, v79, v91
	s_waitcnt lgkmcnt(1)
	v_add_f32_e32 v92, v83, v92
	v_exp_f32_e32 v79, v79
	v_sub_f32_e32 v64, v64, v84
	s_waitcnt lgkmcnt(0)
	v_add_f32_e32 v88, v76, v92
	v_exp_f32_e32 v64, v64
	v_sub_f32_e32 v65, v65, v85
	v_sub_f32_e32 v68, v68, v72
	v_add_f32_e32 v88, v77, v88
	v_exp_f32_e32 v65, v65
	v_sub_f32_e32 v66, v66, v86
	v_exp_f32_e32 v72, v68
	v_add_f32_e32 v88, v78, v88
	v_exp_f32_e32 v66, v66
	v_sub_f32_e32 v67, v67, v87
	v_sub_f32_e32 v68, v69, v73
	v_add_f32_e32 v88, v79, v88
	v_exp_f32_e32 v67, v67
	v_exp_f32_e32 v73, v68
	v_add_f32_e32 v84, v64, v88
	v_sub_f32_e32 v68, v70, v74
	v_add_f32_e32 v84, v65, v84
	v_exp_f32_e32 v74, v68
	v_add_f32_e32 v84, v66, v84
	v_sub_f32_e32 v68, v71, v75
	v_add_f32_e32 v84, v67, v84
	v_exp_f32_e32 v75, v68
	v_add_f32_e32 v68, v72, v84
	v_add_f32_e32 v68, v73, v68
	v_add_f32_e32 v68, v74, v68
	v_add_f32_e32 v150, v75, v68
	v_cvt_pk_bf16_f32 v68, v80, v81
	v_cvt_pk_bf16_f32 v69, v82, v83
	v_cvt_pk_bf16_f32 v70, v76, v77
	v_cvt_pk_bf16_f32 v71, v78, v79
	v_cvt_pk_bf16_f32 v64, v64, v65
	v_cvt_pk_bf16_f32 v65, v66, v67
	v_cvt_pk_bf16_f32 v66, v72, v73
	v_cvt_pk_bf16_f32 v67, v74, v75
	s_waitcnt lgkmcnt(0)
	s_barrier
	s_add_i32 s18, s17, 2
	s_add_i32 s16, s16, -2
	s_add_i32 s15, s15, 0xffd10000
	s_addk_i32 s14, 0xfe00
	s_cmp_ge_u32 s17, s68
	s_cbranch_scc1 .LBB0_544
	s_mov_b32 s17, s18
	s_and_b64 vcc, exec, s[12:13]
	s_cbranch_vccz .LBB0_527
	s_branch .LBB0_528

.LBB0_546:
	ds_read_b64_tr_b16 v[0:1], v142 offset:49152
	ds_read_b64_tr_b16 v[2:3], v146 offset:49152
	ds_read_b64_tr_b16 v[6:7], v146 offset:57344
	ds_read_b64_tr_b16 v[4:5], v142 offset:57344
	ds_read_b64_tr_b16 v[8:9], v136 offset:49152
	ds_read_b64_tr_b16 v[10:11], v137 offset:49152
	ds_read_b64_tr_b16 v[14:15], v137 offset:57344
	ds_read_b64_tr_b16 v[12:13], v136 offset:57344
	s_waitcnt lgkmcnt(6)
	v_mfma_f32_16x16x32_bf16 v[0:3], v[0:3], v[68:71], v[60:63]
	s_waitcnt lgkmcnt(2)
	v_mfma_f32_16x16x32_bf16 v[8:11], v[8:11], v[68:71], v[52:55]
	v_mfma_f32_16x16x32_bf16 v[0:3], v[4:7], v[64:67], v[0:3]
	ds_read_b64_tr_b16 v[4:5], v139 offset:49152
	ds_read_b64_tr_b16 v[6:7], v145 offset:49152
	s_waitcnt lgkmcnt(2)
	v_mfma_f32_16x16x32_bf16 v[8:11], v[12:15], v[64:67], v[8:11]
	ds_read_b64_tr_b16 v[14:15], v145 offset:57344
	ds_read_b64_tr_b16 v[12:13], v139 offset:57344
	s_waitcnt vmcnt(3)
	ds_read_b64_tr_b16 v[16:17], v140 offset:49152
	ds_read_b64_tr_b16 v[18:19], v147 offset:49152
	s_waitcnt lgkmcnt(4)
	v_mfma_f32_16x16x32_bf16 v[4:7], v[4:7], v[68:71], v[48:51]
	s_waitcnt lgkmcnt(2)
	v_mfma_f32_16x16x32_bf16 v[4:7], v[12:15], v[64:67], v[4:7]
	ds_read_b64_tr_b16 v[14:15], v147 offset:57344
	ds_read_b64_tr_b16 v[12:13], v140 offset:57344
	s_waitcnt vmcnt(2)
	ds_read_b64_tr_b16 v[20:21], v148 offset:49152
	ds_read_b64_tr_b16 v[22:23], v149 offset:49152
	s_waitcnt vmcnt(1)
	ds_read_b64_tr_b16 v[26:27], v149 offset:57344
	ds_read_b64_tr_b16 v[24:25], v148 offset:57344
	v_lshlrev_b32_e32 v48, 2, v126
	s_waitcnt lgkmcnt(6)
	v_mfma_f32_16x16x32_bf16 v[16:19], v[16:19], v[68:71], v[56:59]
	s_waitcnt vmcnt(0)
	v_xor_b32_e32 v28, 64, v48
	v_mov_b32_e32 v126, v108
	s_waitcnt lgkmcnt(2)
	v_mfma_f32_16x16x32_bf16 v[20:23], v[20:23], v[68:71], v[32:35]
	s_nop 2
	ds_bpermute_b32 v32, v28, v150
	v_mfma_f32_16x16x32_bf16 v[12:15], v[12:15], v[64:67], v[16:19]
	s_nop 2
	ds_read_b64_tr_b16 v[16:17], v133 offset:49152
	ds_read_b64_tr_b16 v[18:19], v134 offset:49152
	ds_read_b64_tr_b16 v[30:31], v134 offset:57344
	ds_read_b64_tr_b16 v[28:29], v133 offset:57344
	s_waitcnt lgkmcnt(4)
	v_add_f32_e32 v49, v150, v32
	v_xor_b32_e32 v32, 0x80, v48
	v_mfma_f32_16x16x32_bf16 v[20:23], v[24:27], v[64:67], v[20:23]
	ds_read_b64_tr_b16 v[24:25], v135 offset:49152
	ds_read_b64_tr_b16 v[26:27], v138 offset:49152
	s_waitcnt lgkmcnt(4)
	v_mfma_f32_16x16x32_bf16 v[16:19], v[16:19], v[68:71], v[36:39]
	s_nop 2
	ds_bpermute_b32 v36, v32, v49
	ds_read_b64_tr_b16 v[34:35], v138 offset:57344
	ds_read_b64_tr_b16 v[32:33], v135 offset:57344
	s_waitcnt lgkmcnt(5)
	v_mfma_f32_16x16x32_bf16 v[16:19], v[28:31], v[64:67], v[16:19]
	ds_read_b64_tr_b16 v[28:29], v141 offset:49152
	ds_read_b64_tr_b16 v[30:31], v143 offset:49152
	s_waitcnt lgkmcnt(4)
	v_add_f32_e32 v36, v49, v36
	v_mfma_f32_16x16x32_bf16 v[24:27], v[24:27], v[68:71], v[40:43]
	v_div_scale_f32 v37, s[14:15], v36, v36, 1.0
	v_rcp_f32_e32 v38, v37
	s_waitcnt lgkmcnt(2)
	v_mfma_f32_16x16x32_bf16 v[24:27], v[32:35], v[64:67], v[24:27]
	ds_read_b64_tr_b16 v[34:35], v143 offset:57344
	ds_read_b64_tr_b16 v[32:33], v141 offset:57344
	s_add_u32 s14, s50, s62
	v_fma_f32 v39, -v37, v38, 1.0
	s_waitcnt lgkmcnt(2)
	v_mfma_f32_16x16x32_bf16 v[28:31], v[28:31], v[68:71], v[44:47]
	v_fmac_f32_e32 v38, v39, v38
	v_div_scale_f32 v39, vcc, 1.0, v36, 1.0
	v_mul_f32_e32 v40, v39, v38
	s_waitcnt lgkmcnt(0)
	v_mfma_f32_16x16x32_bf16 v[28:31], v[32:35], v[64:67], v[28:31]
	v_fma_f32 v32, -v37, v40, v39
	v_fmac_f32_e32 v40, v32, v38
	v_fma_f32 v32, -v37, v40, v39
	v_div_fmas_f32 v32, v32, v38, v40
	v_div_fixup_f32 v32, v32, v36, 1.0
	v_lshl_add_u32 v33, v125, 12, v128
	v_pk_mul_f32 v[0:1], v[0:1], v[32:33] op_sel_hi:[1,0]
	v_pk_mul_f32 v[2:3], v[2:3], v[32:33] op_sel_hi:[1,0]
	s_addc_u32 s15, s51, 0
	v_cvt_pk_bf16_f32 v0, v0, v1
	v_cvt_pk_bf16_f32 v1, v2, v3
	global_store_dwordx2 v33, v[0:1], s[14:15]
	v_pk_mul_f32 v[0:1], v[8:9], v[32:33] op_sel_hi:[1,0]
	v_pk_mul_f32 v[2:3], v[10:11], v[32:33] op_sel_hi:[1,0]
	v_cvt_pk_bf16_f32 v0, v0, v1
	v_cvt_pk_bf16_f32 v1, v2, v3
	global_store_dwordx2 v33, v[0:1], s[14:15] offset:32
	v_pk_mul_f32 v[0:1], v[4:5], v[32:33] op_sel_hi:[1,0]
	v_pk_mul_f32 v[2:3], v[6:7], v[32:33] op_sel_hi:[1,0]
	v_cvt_pk_bf16_f32 v0, v0, v1
	v_cvt_pk_bf16_f32 v1, v2, v3
	global_store_dwordx2 v33, v[0:1], s[14:15] offset:64
	v_pk_mul_f32 v[0:1], v[12:13], v[32:33] op_sel_hi:[1,0]
	v_pk_mul_f32 v[2:3], v[14:15], v[32:33] op_sel_hi:[1,0]
	v_cvt_pk_bf16_f32 v0, v0, v1
	v_cvt_pk_bf16_f32 v1, v2, v3
	global_store_dwordx2 v33, v[0:1], s[14:15] offset:96
	v_pk_mul_f32 v[0:1], v[20:21], v[32:33] op_sel_hi:[1,0]
	v_pk_mul_f32 v[2:3], v[22:23], v[32:33] op_sel_hi:[1,0]
	v_cvt_pk_bf16_f32 v0, v0, v1
	v_cvt_pk_bf16_f32 v1, v2, v3
	global_store_dwordx2 v33, v[0:1], s[14:15] offset:128
	v_pk_mul_f32 v[0:1], v[16:17], v[32:33] op_sel_hi:[1,0]
	v_pk_mul_f32 v[2:3], v[18:19], v[32:33] op_sel_hi:[1,0]
	v_cvt_pk_bf16_f32 v0, v0, v1
	v_cvt_pk_bf16_f32 v1, v2, v3
	global_store_dwordx2 v33, v[0:1], s[14:15] offset:160
	v_pk_mul_f32 v[0:1], v[24:25], v[32:33] op_sel_hi:[1,0]
	v_pk_mul_f32 v[2:3], v[26:27], v[32:33] op_sel_hi:[1,0]
	v_cvt_pk_bf16_f32 v0, v0, v1
	v_cvt_pk_bf16_f32 v1, v2, v3
	global_store_dwordx2 v33, v[0:1], s[14:15] offset:192
	v_pk_mul_f32 v[0:1], v[28:29], v[32:33] op_sel_hi:[1,0]
	v_pk_mul_f32 v[2:3], v[30:31], v[32:33] op_sel_hi:[1,0]
	v_cvt_pk_bf16_f32 v0, v0, v1
	v_cvt_pk_bf16_f32 v1, v2, v3
	s_lshl_b32 s17, s59, 7
	global_store_dwordx2 v33, v[0:1], s[14:15] offset:224
	s_add_i32 s16, s17, s89
	v_and_b32_e32 v32, 15, v126
	v_or_b32_e32 v125, s16, v32
	v_and_b32_e32 v0, -16, v126
	v_mad_u64_u32 v[8:9], s[18:19], v125, s75, v[0:1]
	v_add_u32_e32 v4, 64, v8
	v_add_u32_e32 v9, 0x80, v8
	v_add_u32_e32 v12, 0xc0, v8
	global_load_dwordx4 v[0:3], v8, s[48:49] offset:3072
	s_nop 0
	global_load_dwordx4 v[4:7], v4, s[48:49] offset:3072
	s_nop 0
	global_load_dwordx4 v[8:11], v9, s[48:49] offset:3072
	s_nop 0
	global_load_dwordx4 v[12:15], v12, s[48:49] offset:3072
	v_lshl_add_u32 v16, v125, 2, 0
	v_add_u32_e32 v16, 0x10000, v16
	ds_read_b32 v128, v16
	s_lshl_b32 s16, s59, 1
	s_or_b32 s18, s16, 1
	s_waitcnt lgkmcnt(0)
	v_mov_b32_e32 v240, v128
	v_mov_b32_e32 v241, v128
	v_mov_b32_e32 v242, v128
	v_mov_b32_e32 v243, v128
	s_waitcnt lgkmcnt(0)
	s_barrier
	s_mul_i32 s19, s18, 0x178000
	s_add_u32 s20, s0, s19
	s_addc_u32 s21, s1, 0
	v_lshl_add_u64 v[16:17], s[20:21], 0, v[104:105]
	v_add_co_u32_e32 v20, vcc, 0xbc000, v16
	s_nop 1
	v_addc_co_u32_e32 v21, vcc, 0, v17, vcc
	global_load_dwordx4 v[16:19], v[16:17], off
	s_nop 0
	global_load_dwordx4 v[20:23], v[20:21], off
	s_waitcnt vmcnt(1)
	ds_write_b128 v100, v[16:19]
	s_waitcnt vmcnt(0)
	ds_write_b128 v124, v[20:23]
	s_waitcnt lgkmcnt(0)
	s_waitcnt lgkmcnt(0)
	s_barrier
	s_and_b64 vcc, exec, s[10:11]
	s_cbranch_vccnz .LBB0_548
	s_mul_i32 s20, s59, 0x2f0000
	s_add_u32 s20, s0, s20
	s_addc_u32 s21, s1, 0
	v_lshl_add_u64 v[16:17], s[20:21], 0, v[104:105]
	s_add_u32 s20, s52, s19
	v_add_co_u32_e32 v20, vcc, 0xbc000, v16
	s_addc_u32 s21, s53, 0
	s_nop 0
	v_addc_co_u32_e32 v21, vcc, 0, v17, vcc
	v_lshl_add_u64 v[24:25], s[20:21], 0, v[104:105]
	v_add_co_u32_e32 v28, vcc, 0xbc000, v24
	global_load_dwordx4 v[16:19], v[16:17], off
	s_nop 0
	global_load_dwordx4 v[20:23], v[20:21], off
	v_addc_co_u32_e32 v29, vcc, 0, v25, vcc
	global_load_dwordx4 v[24:27], v[24:25], off
	s_nop 0
	global_load_dwordx4 v[28:31], v[28:29], off
	s_waitcnt lgkmcnt(0)

.LBB0_558:
	v_sub_f32_e32 v44, v44, v60
	v_exp_f32_e32 v44, v44
	v_sub_f32_e32 v45, v45, v61
	v_cmp_le_i32_e32 vcc, v64, v125
	v_exp_f32_e32 v45, v45
	v_bfe_u32 v84, v126, 1, 1
	v_cndmask_b32_e32 v97, 0, v44, vcc
	v_sub_f32_e32 v44, v46, v62
	v_exp_f32_e32 v44, v44
	v_cmp_lt_i32_e32 vcc, v64, v125
	v_sub_f32_e32 v46, v47, v63
	v_cndmask_b32_e32 v98, 0, v45, vcc
	v_or_b32_e32 v45, 2, v64
	v_cmp_le_i32_e32 vcc, v45, v125
	v_exp_f32_e32 v46, v46
	v_cndmask_b32_e32 v99, 0, v44, vcc
	v_or_b32_e32 v44, 3, v64
	v_cmp_le_i32_e32 vcc, v44, v125
	v_sub_f32_e32 v40, v40, v56
	v_exp_f32_e32 v40, v40
	v_or_b32_e32 v44, 4, v64
	v_sub_f32_e32 v41, v41, v57
	v_cndmask_b32_e32 v150, 0, v46, vcc
	v_exp_f32_e32 v41, v41
	v_cmp_le_i32_e32 vcc, v44, v125
	v_cvt_pk_bf16_f32 v44, v97, v98
	v_cvt_pk_bf16_f32 v45, v99, v150
	v_cndmask_b32_e32 v151, 0, v40, vcc
	v_or_b32_e32 v40, 5, v64
	v_cmp_le_i32_e32 vcc, v40, v125
	v_sub_f32_e32 v40, v42, v58
	v_cndmask_b32_e32 v152, 0, v41, vcc
	v_exp_f32_e32 v40, v40
	v_or_b32_e32 v41, 6, v64
	v_sub_f32_e32 v42, v43, v59
	v_cmp_le_i32_e32 vcc, v41, v125
	v_exp_f32_e32 v42, v42
	v_sub_f32_e32 v36, v36, v52
	v_exp_f32_e32 v36, v36
	v_cndmask_b32_e32 v153, 0, v40, vcc
	v_or_b32_e32 v40, 7, v64
	v_cmp_le_i32_e32 vcc, v40, v125
	v_add_u32_e32 v40, 32, v64
	v_cndmask_b32_e32 v154, 0, v42, vcc
	v_cmp_le_i32_e32 vcc, v40, v125
	v_sub_f32_e32 v37, v37, v53
	v_exp_f32_e32 v37, v37
	v_cndmask_b32_e32 v155, 0, v36, vcc
	v_add_u32_e32 v36, 33, v64
	v_cmp_le_i32_e32 vcc, v36, v125
	v_sub_f32_e32 v36, v38, v54
	v_exp_f32_e32 v36, v36
	v_cndmask_b32_e32 v156, 0, v37, vcc
	v_add_u32_e32 v37, 34, v64
	v_cmp_le_i32_e32 vcc, v37, v125
	v_sub_f32_e32 v38, v39, v55
	v_cndmask_b32_e32 v157, 0, v36, vcc
	v_add_u32_e32 v36, 35, v64
	v_cmp_le_i32_e32 vcc, v36, v125
	v_exp_f32_e32 v38, v38
	v_sub_f32_e32 v32, v32, v48
	v_exp_f32_e32 v32, v32
	v_add_u32_e32 v36, 36, v64
	v_cndmask_b32_e32 v158, 0, v38, vcc
	v_cmp_le_i32_e32 vcc, v36, v125
	v_sub_f32_e32 v33, v33, v49
	v_exp_f32_e32 v33, v33
	v_cndmask_b32_e32 v159, 0, v32, vcc
	v_add_u32_e32 v32, 37, v64
	v_cmp_le_i32_e32 vcc, v32, v125
	v_sub_f32_e32 v32, v34, v50
	v_exp_f32_e32 v32, v32
	v_sub_f32_e32 v34, v35, v51
	v_cndmask_b32_e32 v160, 0, v33, vcc
	v_add_u32_e32 v33, 38, v64
	v_exp_f32_e32 v34, v34
	v_cmp_le_i32_e32 vcc, v33, v125
	v_lshrrev_b32_e32 v33, 1, v126
	v_and_b32_e32 v33, 0x7ffffff8, v33
	v_cndmask_b32_e32 v161, 0, v32, vcc
	v_add_u32_e32 v32, 39, v64
	v_cmp_le_i32_e32 vcc, v32, v125
	v_bfe_u32 v32, v126, 2, 2
	v_lshlrev_b32_e32 v85, 2, v32
	v_cndmask_b32_e32 v162, 0, v34, vcc
	v_lshlrev_b32_e32 v34, 3, v126
	v_and_b32_e32 v92, 8, v34
	v_or_b32_e32 v34, v33, v32
	v_or_b32_e32 v33, 4, v33
	v_or_b32_e32 v32, v33, v32
	v_bfe_u32 v88, v33, 2, 2
	v_lshlrev_b32_e32 v86, 8, v34
	v_lshrrev_b32_e32 v34, 3, v126
	v_lshlrev_b32_e32 v93, 8, v32
	v_bitop3_b32 v32, v88, v84, v85 bitop3:0x36
	v_and_b32_e32 v87, 2, v34
	v_lshlrev_b32_e32 v32, 4, v32
	v_or_b32_e32 v34, v85, v87
	v_or3_b32 v61, v32, v93, v92
	v_or_b32_e32 v32, 2, v84
	v_or_b32_e32 v34, v34, v84
	v_bitop3_b32 v33, v85, v32, v87 bitop3:0x36
	v_lshlrev_b32_e32 v34, 4, v34
	v_lshlrev_b32_e32 v33, 4, v33
	v_or3_b32 v60, v34, v86, v92
	v_or3_b32 v62, v33, v86, v92
	v_bitop3_b32 v36, v88, v32, v85 bitop3:0x36
	ds_read_b128 v[32:35], v129 offset:16384
	v_lshlrev_b32_e32 v36, 4, v36
	v_or3_b32 v63, v36, v93, v92
	ds_read_b128 v[36:39], v130 offset:16384
	s_waitcnt lgkmcnt(1)
	v_mfma_f32_16x16x32_bf16 v[32:35], v[32:35], v[0:3], v[240:243]
	v_or_b32_e32 v64, 4, v84
	v_bitop3_b32 v40, v85, v64, v87 bitop3:0x36
	v_lshlrev_b32_e32 v52, 4, v40
	ds_read_b128 v[40:43], v131 offset:16384
	ds_read_b128 v[48:51], v129 offset:17408
	s_waitcnt lgkmcnt(2)
	v_mfma_f32_16x16x32_bf16 v[32:35], v[36:39], v[4:7], v[32:35]
	v_or3_b32 v89, v52, v86, v92
	ds_read_b128 v[52:55], v132 offset:16384
	ds_read_b128 v[56:59], v130 offset:17408
	v_bitop3_b32 v36, v88, v64, v85 bitop3:0x36
	s_waitcnt lgkmcnt(3)
	v_mfma_f32_16x16x32_bf16 v[32:35], v[40:43], v[8:11], v[32:35]
	v_lshlrev_b32_e32 v64, 4, v36
	v_or3_b32 v90, v64, v93, v92
	v_or_b32_e32 v64, 6, v84
	s_waitcnt lgkmcnt(1)
	v_mfma_f32_16x16x32_bf16 v[76:79], v[52:55], v[12:15], v[32:35]
	ds_read_b128 v[36:39], v131 offset:17408
	ds_read_b128 v[40:43], v132 offset:17408
	v_or_b32_e32 v52, 8, v84
	v_bitop3_b32 v32, v85, v64, v87 bitop3:0x36
	v_lshlrev_b32_e32 v32, 4, v32
	v_or3_b32 v91, v32, v86, v92
	v_mfma_f32_16x16x32_bf16 v[32:35], v[48:51], v[0:3], v[240:243]
	v_bitop3_b32 v48, v88, v64, v85 bitop3:0x36
	v_lshlrev_b32_e32 v48, 4, v48
	v_or3_b32 v94, v48, v93, v92
	s_waitcnt lgkmcnt(2)
	v_mfma_f32_16x16x32_bf16 v[32:35], v[56:59], v[4:7], v[32:35]
	ds_read_b128 v[48:51], v129 offset:24576
	v_bitop3_b32 v53, v85, v52, v87 bitop3:0x36
	v_bitop3_b32 v52, v88, v52, v85 bitop3:0x36
	s_waitcnt lgkmcnt(2)
	v_mfma_f32_16x16x32_bf16 v[32:35], v[36:39], v[8:11], v[32:35]
	v_lshlrev_b32_e32 v36, 4, v53
	v_or3_b32 v95, v36, v86, v92
	ds_read_b128 v[36:39], v130 offset:24576
	s_waitcnt lgkmcnt(1)
	v_mfma_f32_16x16x32_bf16 v[48:51], v[48:51], v[0:3], v[240:243]
	v_lshlrev_b32_e32 v64, 4, v52
	v_or3_b32 v133, v64, v93, v92
	v_or_b32_e32 v64, 10, v84
	v_mfma_f32_16x16x32_bf16 v[72:75], v[40:43], v[12:15], v[32:35]
	s_nop 2
	ds_read_b128 v[32:35], v131 offset:24576
	ds_read_b128 v[40:43], v129 offset:25600
	ds_read_b128 v[52:55], v132 offset:24576
	ds_read_b128 v[56:59], v130 offset:25600
	v_add_u32_e32 v146, 0, v60
	s_waitcnt lgkmcnt(4)
	v_mfma_f32_16x16x32_bf16 v[36:39], v[36:39], v[4:7], v[48:51]
	v_add_u32_e32 v148, 0, v61
	v_cvt_pk_bf16_f32 v46, v151, v152
	v_cvt_pk_bf16_f32 v47, v153, v154
	s_waitcnt lgkmcnt(3)
	v_mfma_f32_16x16x32_bf16 v[32:35], v[32:35], v[8:11], v[36:39]
	ds_read_b128 v[48:51], v131 offset:25600
	v_add_u32_e32 v139, 0, v62
	v_add_u32_e32 v142, 0, v63
	s_waitcnt lgkmcnt(2)
	v_mfma_f32_16x16x32_bf16 v[68:71], v[52:55], v[12:15], v[32:35]
	v_bitop3_b32 v36, v85, v64, v87 bitop3:0x36
	v_lshlrev_b32_e32 v65, 4, v36
	ds_read_b128 v[36:39], v132 offset:25600
	v_bitop3_b32 v32, v88, v64, v85 bitop3:0x36
	v_lshlrev_b32_e32 v52, 4, v32
	v_mfma_f32_16x16x32_bf16 v[32:35], v[40:43], v[0:3], v[240:243]
	v_or_b32_e32 v40, 12, v84
	v_bitop3_b32 v41, v85, v40, v87 bitop3:0x36
	v_lshlrev_b32_e32 v41, 4, v41
	s_waitcnt lgkmcnt(2)
	v_mfma_f32_16x16x32_bf16 v[32:35], v[56:59], v[4:7], v[32:35]
	v_or3_b32 v135, v52, v93, v92
	v_or3_b32 v136, v41, v86, v92
	v_bitop3_b32 v52, v88, v40, v85 bitop3:0x36
	s_waitcnt lgkmcnt(1)
	v_mfma_f32_16x16x32_bf16 v[32:35], v[48:51], v[8:11], v[32:35]
	ds_read_b64_tr_b16 v[40:41], v146 offset:32768
	ds_read_b64_tr_b16 v[42:43], v148 offset:32768
	v_or3_b32 v134, v65, v86, v92
	v_cvt_pk_bf16_f32 v80, v155, v156
	s_waitcnt lgkmcnt(2)
	v_mfma_f32_16x16x32_bf16 v[64:67], v[36:39], v[12:15], v[32:35]
	s_nop 2
	ds_read_b64_tr_b16 v[34:35], v148 offset:40960
	ds_read_b64_tr_b16 v[32:33], v146 offset:40960
	ds_read_b64_tr_b16 v[36:37], v139 offset:32768
	ds_read_b64_tr_b16 v[38:39], v142 offset:32768
	v_cvt_pk_bf16_f32 v81, v157, v158
	s_waitcnt lgkmcnt(4)
	v_mfma_f32_16x16x32_bf16 v[40:43], v[40:43], v[44:47], 0
	v_cvt_pk_bf16_f32 v82, v159, v160
	v_cvt_pk_bf16_f32 v83, v161, v162
	v_add_u32_e32 v141, 0, v89
	ds_read_b64_tr_b16 v[50:51], v142 offset:40960
	ds_read_b64_tr_b16 v[48:49], v139 offset:40960
	s_waitcnt lgkmcnt(4)
	v_mfma_f32_16x16x32_bf16 v[60:63], v[32:35], v[80:83], v[40:43]
	v_add_u32_e32 v145, 0, v90
	ds_read_b64_tr_b16 v[32:33], v141 offset:32768
	ds_read_b64_tr_b16 v[34:35], v145 offset:32768
	ds_read_b64_tr_b16 v[42:43], v145 offset:40960
	ds_read_b64_tr_b16 v[40:41], v141 offset:40960
	s_waitcnt lgkmcnt(6)
	v_mfma_f32_16x16x32_bf16 v[36:39], v[36:39], v[44:47], 0
	v_add_u32_e32 v140, 0, v91
	v_add_u32_e32 v143, 0, v94
	v_lshlrev_b32_e32 v52, 4, v52
	s_waitcnt lgkmcnt(4)
	v_mfma_f32_16x16x32_bf16 v[56:59], v[48:51], v[80:83], v[36:39]
	s_nop 2
	ds_read_b64_tr_b16 v[36:37], v140 offset:32768
	ds_read_b64_tr_b16 v[38:39], v143 offset:32768
	v_or_b32_e32 v48, 14, v84
	v_bitop3_b32 v49, v85, v48, v87 bitop3:0x36
	s_waitcnt lgkmcnt(4)
	v_mfma_f32_16x16x32_bf16 v[32:35], v[32:35], v[44:47], 0
	v_or3_b32 v89, v52, v93, v92
	v_add_u32_e32 v147, 0, v95
	v_add_u32_e32 v149, 0, v133
	s_waitcnt lgkmcnt(2)
	v_mfma_f32_16x16x32_bf16 v[52:55], v[40:43], v[80:83], v[32:35]
	s_nop 2
	ds_read_b64_tr_b16 v[34:35], v143 offset:40960
	ds_read_b64_tr_b16 v[32:33], v140 offset:40960
	v_lshlrev_b32_e32 v40, 4, v49
	v_or3_b32 v94, v40, v86, v92
	s_waitcnt lgkmcnt(2)
	v_mfma_f32_16x16x32_bf16 v[36:39], v[36:39], v[44:47], 0
	ds_read_b64_tr_b16 v[40:41], v147 offset:32768
	ds_read_b64_tr_b16 v[42:43], v149 offset:32768
	v_add_u32_e32 v133, 0, v134
	v_bitop3_b32 v88, v88, v48, v85 bitop3:0x36
	s_waitcnt lgkmcnt(2)
	v_mfma_f32_16x16x32_bf16 v[48:51], v[32:35], v[80:83], v[36:39]
	ds_read_b64_tr_b16 v[34:35], v149 offset:40960
	ds_read_b64_tr_b16 v[32:33], v147 offset:40960
	v_add_u32_e32 v134, 0, v135
	ds_read_b64_tr_b16 v[36:37], v133 offset:32768
	ds_read_b64_tr_b16 v[38:39], v134 offset:32768
	s_waitcnt lgkmcnt(4)
	v_mfma_f32_16x16x32_bf16 v[40:43], v[40:43], v[44:47], 0
	ds_read_b64_tr_b16 v[86:87], v134 offset:40960
	ds_read_b64_tr_b16 v[84:85], v133 offset:40960
	v_add_u32_e32 v135, 0, v136
	v_add_u32_e32 v136, 0, v89
	s_waitcnt lgkmcnt(4)
	v_mfma_f32_16x16x32_bf16 v[32:35], v[32:35], v[80:83], v[40:43]
	s_nop 2
	ds_read_b64_tr_b16 v[40:41], v135 offset:32768
	ds_read_b64_tr_b16 v[42:43], v136 offset:32768
	v_lshlrev_b32_e32 v95, 4, v88
	ds_read_b64_tr_b16 v[90:91], v136 offset:40960
	ds_read_b64_tr_b16 v[88:89], v135 offset:40960
	s_waitcnt lgkmcnt(6)
	v_mfma_f32_16x16x32_bf16 v[36:39], v[36:39], v[44:47], 0
	v_add_u32_e32 v137, 0, v94
	s_and_b64 vcc, exec, s[10:11]
	s_waitcnt lgkmcnt(4)
	v_mfma_f32_16x16x32_bf16 v[36:39], v[84:87], v[80:83], v[36:39]
	v_or3_b32 v84, v95, v93, v92
	v_add_u32_e32 v138, 0, v84
	ds_read_b64_tr_b16 v[84:85], v137 offset:32768
	ds_read_b64_tr_b16 v[86:87], v138 offset:32768
	s_waitcnt lgkmcnt(4)
	v_mfma_f32_16x16x32_bf16 v[40:43], v[40:43], v[44:47], 0
	s_waitcnt lgkmcnt(2)
	v_mfma_f32_16x16x32_bf16 v[40:43], v[88:91], v[80:83], v[40:43]
	ds_read_b64_tr_b16 v[90:91], v138 offset:40960
	ds_read_b64_tr_b16 v[88:89], v137 offset:40960
	s_waitcnt lgkmcnt(2)
	v_mfma_f32_16x16x32_bf16 v[44:47], v[84:87], v[44:47], 0
	s_waitcnt lgkmcnt(0)
	v_mfma_f32_16x16x32_bf16 v[44:47], v[88:91], v[80:83], v[44:47]
	s_cbranch_vccnz .LBB0_560
	v_add_u32_e32 v80, 0, v109
	s_waitcnt vmcnt(3)
	ds_write_b128 v100, v[16:19]
	s_waitcnt vmcnt(2)
	ds_write_b128 v124, v[20:23]
	s_waitcnt vmcnt(1)
	ds_write_b128 v80, v[24:27] offset:49152
	v_add_u32_e32 v80, 0, v112
	s_waitcnt vmcnt(0)
	ds_write_b128 v80, v[28:31] offset:49152

.LBB0_564:
	v_add_f32_e32 v97, 0, v97
	v_add_f32_e32 v97, v98, v97
	v_add_f32_e32 v97, v99, v97
	v_add_f32_e32 v97, v150, v97
	v_add_f32_e32 v97, v151, v97
	v_add_f32_e32 v97, v152, v97
	s_waitcnt lgkmcnt(3)
	v_add_f32_e32 v97, v153, v97
	v_sub_f32_e32 v76, v76, v92
	v_add_f32_e32 v97, v154, v97
	v_exp_f32_e32 v76, v76
	v_sub_f32_e32 v77, v77, v93
	v_add_f32_e32 v97, v155, v97
	v_exp_f32_e32 v77, v77
	v_add_f32_e32 v97, v156, v97
	v_add_f32_e32 v97, v157, v97
	v_cmp_le_i32_e32 vcc, v163, v125
	v_add_f32_e32 v97, v158, v97
	v_cndmask_b32_e32 v76, 0, v76, vcc
	v_cmp_lt_i32_e32 vcc, v163, v125
	v_sub_f32_e32 v78, v78, v94
	v_or_b32_e32 v93, 2, v163
	v_add_f32_e32 v97, v159, v97
	v_cndmask_b32_e32 v77, 0, v77, vcc
	v_cmp_le_i32_e32 vcc, v93, v125
	v_add_f32_e32 v97, v160, v97
	v_exp_f32_e32 v78, v78
	v_sub_f32_e32 v79, v79, v95
	v_add_f32_e32 v97, v161, v97
	v_exp_f32_e32 v79, v79
	v_add_f32_e32 v97, v162, v97
	s_waitcnt lgkmcnt(2)
	v_add_f32_e32 v92, v97, v76
	v_or_b32_e32 v93, 3, v163
	v_sub_f32_e32 v72, v72, v88
	v_add_f32_e32 v92, v77, v92
	v_cndmask_b32_e32 v78, 0, v78, vcc
	v_cmp_le_i32_e32 vcc, v93, v125
	v_exp_f32_e32 v72, v72
	v_add_f32_e32 v92, v78, v92
	v_cndmask_b32_e32 v79, 0, v79, vcc
	v_sub_f32_e32 v73, v73, v89
	v_add_f32_e32 v88, v79, v92
	v_or_b32_e32 v92, 4, v163
	v_exp_f32_e32 v73, v73
	v_cmp_le_i32_e32 vcc, v92, v125
	v_or_b32_e32 v89, 5, v163
	s_waitcnt lgkmcnt(1)
	v_cndmask_b32_e32 v72, 0, v72, vcc
	v_cmp_le_i32_e32 vcc, v89, v125
	v_sub_f32_e32 v74, v74, v90
	v_or_b32_e32 v89, 6, v163
	v_cndmask_b32_e32 v73, 0, v73, vcc
	v_cmp_le_i32_e32 vcc, v89, v125
	v_exp_f32_e32 v74, v74
	v_sub_f32_e32 v75, v75, v91
	v_exp_f32_e32 v75, v75
	v_add_f32_e32 v88, v72, v88
	v_or_b32_e32 v89, 7, v163
	v_sub_f32_e32 v68, v68, v84
	v_add_f32_e32 v88, v73, v88
	v_cndmask_b32_e32 v74, 0, v74, vcc
	v_cmp_le_i32_e32 vcc, v89, v125
	v_exp_f32_e32 v68, v68
	v_add_f32_e32 v88, v74, v88
	v_cndmask_b32_e32 v75, 0, v75, vcc
	v_add_f32_e32 v84, v75, v88
	v_add_u32_e32 v88, 32, v163
	v_cmp_le_i32_e32 vcc, v88, v125
	s_nop 1
	v_cndmask_b32_e32 v88, 0, v68, vcc
	v_sub_f32_e32 v68, v69, v85
	v_exp_f32_e32 v68, v68
	v_add_f32_e32 v69, v88, v84
	v_add_u32_e32 v84, 33, v163
	v_cmp_le_i32_e32 vcc, v84, v125
	s_nop 1
	v_cndmask_b32_e32 v84, 0, v68, vcc
	v_sub_f32_e32 v68, v70, v86
	v_exp_f32_e32 v68, v68
	v_add_u32_e32 v70, 34, v163
	v_cmp_le_i32_e32 vcc, v70, v125
	v_add_u32_e32 v70, 35, v163
	v_add_f32_e32 v69, v84, v69
	v_cndmask_b32_e32 v85, 0, v68, vcc
	v_sub_f32_e32 v68, v71, v87
	v_exp_f32_e32 v68, v68
	v_cmp_le_i32_e32 vcc, v70, v125
	v_add_f32_e32 v69, v85, v69
	v_cvt_pk_bf16_f32 v70, v72, v73
	v_cndmask_b32_e32 v86, 0, v68, vcc
	s_waitcnt lgkmcnt(0)
	v_sub_f32_e32 v64, v64, v80
	v_exp_f32_e32 v64, v64
	v_add_f32_e32 v68, v86, v69
	v_add_u32_e32 v69, 36, v163
	v_cmp_le_i32_e32 vcc, v69, v125
	v_cvt_pk_bf16_f32 v69, v78, v79
	v_cvt_pk_bf16_f32 v71, v74, v75
	v_cndmask_b32_e32 v80, 0, v64, vcc
	v_sub_f32_e32 v64, v65, v81
	v_exp_f32_e32 v64, v64
	v_add_f32_e32 v65, v80, v68
	v_add_u32_e32 v68, 37, v163
	v_cmp_le_i32_e32 vcc, v68, v125
	v_cvt_pk_bf16_f32 v68, v76, v77
	s_nop 0
	v_cndmask_b32_e32 v81, 0, v64, vcc
	v_sub_f32_e32 v64, v66, v82
	v_exp_f32_e32 v64, v64
	v_add_u32_e32 v66, 38, v163
	v_cmp_le_i32_e32 vcc, v66, v125
	v_add_u32_e32 v66, 39, v163
	v_add_f32_e32 v65, v81, v65
	v_cndmask_b32_e32 v82, 0, v64, vcc
	v_sub_f32_e32 v64, v67, v83
	v_exp_f32_e32 v64, v64
	v_cmp_le_i32_e32 vcc, v66, v125
	v_add_f32_e32 v65, v82, v65
	v_cvt_pk_bf16_f32 v66, v80, v81
	v_cndmask_b32_e32 v67, 0, v64, vcc
	v_add_f32_e32 v150, v67, v65
	v_cvt_pk_bf16_f32 v64, v88, v84
	v_cvt_pk_bf16_f32 v65, v85, v86
	v_cvt_pk_bf16_f32 v67, v82, v67
	s_waitcnt lgkmcnt(0)
	s_barrier
	s_cmp_eq_u32 s59, 0
	s_cbranch_scc1 .LBB0_583
	v_lshl_add_u32 v151, v96, 5, s67
	s_mov_b32 s19, 2
	s_mov_b32 s17, s66
	s_mov_b32 s18, s61
	s_and_b64 vcc, exec, s[12:13]
	s_cbranch_vccnz .LBB0_567

.LBB0_567:
	ds_read_b128 v[88:91], v129
	ds_read_b128 v[92:95], v129 offset:1024
	ds_read_b128 v[96:99], v130
	ds_read_b128 v[152:155], v130 offset:1024
	ds_read_b128 v[172:175], v131
	ds_read_b128 v[176:179], v131 offset:1024
	ds_read_b128 v[180:183], v132
	ds_read_b128 v[184:187], v132 offset:1024
	ds_read_b128 v[188:191], v129 offset:8192
	ds_read_b128 v[192:195], v129 offset:9216
	ds_read_b128 v[196:199], v130 offset:8192
	ds_read_b128 v[200:203], v130 offset:9216
	ds_read_b128 v[204:207], v131 offset:8192
	ds_read_b128 v[208:211], v131 offset:9216
	ds_read_b128 v[212:215], v132 offset:8192
	s_and_b64 vcc, exec, s[10:11]
	s_waitcnt lgkmcnt(11)
	v_mfma_f32_16x16x32_bf16 v[72:75], v[88:91], v[0:3], v[240:243]
	ds_read_b128 v[216:219], v132 offset:9216
	ds_read_b64_tr_b16 v[220:221], v146 offset:49152
	ds_read_b64_tr_b16 v[222:223], v148 offset:49152
	ds_read_b64_tr_b16 v[226:227], v148 offset:57344
	v_mfma_f32_16x16x32_bf16 v[72:75], v[96:99], v[4:7], v[72:75]
	v_mfma_f32_16x16x32_bf16 v[76:79], v[92:95], v[0:3], v[240:243]
	s_waitcnt lgkmcnt(11)
	v_mfma_f32_16x16x32_bf16 v[72:75], v[172:175], v[8:11], v[72:75]
	ds_read_b64_tr_b16 v[224:225], v146 offset:57344
	ds_read_b64_tr_b16 v[228:229], v139 offset:49152
	ds_read_b64_tr_b16 v[230:231], v142 offset:49152
	ds_read_b64_tr_b16 v[90:91], v142 offset:57344
	v_mfma_f32_16x16x32_bf16 v[84:87], v[180:183], v[12:15], v[72:75]
	v_mfma_f32_16x16x32_bf16 v[72:75], v[152:155], v[4:7], v[76:79]
	v_mfma_f32_16x16x32_bf16 v[72:75], v[176:179], v[8:11], v[72:75]
	v_mfma_f32_16x16x32_bf16 v[80:83], v[184:187], v[12:15], v[72:75]
	s_waitcnt lgkmcnt(11)
	s_nop 5
	v_mfma_f32_16x16x32_bf16 v[72:75], v[188:191], v[0:3], v[240:243]
	ds_read_b64_tr_b16 v[88:89], v139 offset:57344
	ds_read_b64_tr_b16 v[96:97], v141 offset:49152
	ds_read_b64_tr_b16 v[98:99], v145 offset:49152
	ds_read_b64_tr_b16 v[94:95], v145 offset:57344
	v_mfma_f32_16x16x32_bf16 v[72:75], v[196:199], v[4:7], v[72:75]
	s_waitcnt lgkmcnt(11)
	v_mfma_f32_16x16x32_bf16 v[72:75], v[204:207], v[8:11], v[72:75]
	ds_read_b64_tr_b16 v[92:93], v141 offset:57344
	ds_read_b64_tr_b16 v[172:173], v140 offset:49152
	ds_read_b64_tr_b16 v[174:175], v143 offset:49152
	ds_read_b64_tr_b16 v[182:183], v143 offset:57344
	v_mfma_f32_16x16x32_bf16 v[76:79], v[212:215], v[12:15], v[72:75]
	v_mfma_f32_16x16x32_bf16 v[72:75], v[192:195], v[0:3], v[240:243]
	v_mfma_f32_16x16x32_bf16 v[72:75], v[200:203], v[4:7], v[72:75]
	s_waitcnt lgkmcnt(10)
	v_mfma_f32_16x16x32_bf16 v[60:63], v[220:223], v[68:71], v[60:63]
	ds_read_b64_tr_b16 v[180:181], v140 offset:57344
	ds_read_b64_tr_b16 v[152:153], v147 offset:49152
	ds_read_b64_tr_b16 v[154:155], v149 offset:49152
	ds_read_b64_tr_b16 v[178:179], v149 offset:57344
	ds_read_b64_tr_b16 v[176:177], v147 offset:57344
	v_mfma_f32_16x16x32_bf16 v[60:63], v[224:227], v[64:67], v[60:63]
	s_waitcnt lgkmcnt(11)
	v_mfma_f32_16x16x32_bf16 v[56:59], v[228:231], v[68:71], v[56:59]
	ds_read_b64_tr_b16 v[184:185], v133 offset:49152
	ds_read_b64_tr_b16 v[186:187], v134 offset:49152
	ds_read_b64_tr_b16 v[190:191], v134 offset:57344
	ds_read_b64_tr_b16 v[188:189], v133 offset:57344
	v_mfma_f32_16x16x32_bf16 v[56:59], v[88:91], v[64:67], v[56:59]
	s_waitcnt lgkmcnt(11)
	v_mfma_f32_16x16x32_bf16 v[52:55], v[96:99], v[68:71], v[52:55]
	ds_read_b64_tr_b16 v[196:197], v135 offset:49152
	ds_read_b64_tr_b16 v[198:199], v136 offset:49152
	ds_read_b64_tr_b16 v[206:207], v136 offset:57344
	ds_read_b64_tr_b16 v[204:205], v135 offset:57344
	v_mfma_f32_16x16x32_bf16 v[52:55], v[92:95], v[64:67], v[52:55]
	s_waitcnt lgkmcnt(11)
	v_mfma_f32_16x16x32_bf16 v[48:51], v[172:175], v[68:71], v[48:51]
	ds_read_b64_tr_b16 v[212:213], v137 offset:49152
	ds_read_b64_tr_b16 v[214:215], v138 offset:49152
	ds_read_b64_tr_b16 v[194:195], v138 offset:57344
	ds_read_b64_tr_b16 v[192:193], v137 offset:57344
	v_mfma_f32_16x16x32_bf16 v[48:51], v[180:183], v[64:67], v[48:51]
	s_waitcnt lgkmcnt(11)
	v_mfma_f32_16x16x32_bf16 v[32:35], v[152:155], v[68:71], v[32:35]
	v_mfma_f32_16x16x32_bf16 v[32:35], v[176:179], v[64:67], v[32:35]
	s_waitcnt lgkmcnt(7)
	v_mfma_f32_16x16x32_bf16 v[36:39], v[184:187], v[68:71], v[36:39]
	v_mfma_f32_16x16x32_bf16 v[36:39], v[188:191], v[64:67], v[36:39]
	s_waitcnt lgkmcnt(3)
	v_mfma_f32_16x16x32_bf16 v[40:43], v[196:199], v[68:71], v[40:43]
	v_mfma_f32_16x16x32_bf16 v[40:43], v[204:207], v[64:67], v[40:43]
	v_mfma_f32_16x16x32_bf16 v[72:75], v[208:211], v[8:11], v[72:75]
	s_waitcnt lgkmcnt(0)
	v_mfma_f32_16x16x32_bf16 v[44:47], v[212:215], v[68:71], v[44:47]
	v_mfma_f32_16x16x32_bf16 v[72:75], v[216:219], v[12:15], v[72:75]
	v_mfma_f32_16x16x32_bf16 v[44:47], v[192:195], v[64:67], v[44:47]
	s_cbranch_vccnz .LBB0_569
	v_add_u32_e32 v64, 0, v109
	s_waitcnt vmcnt(3)
	ds_write_b128 v100, v[16:19] offset:16384
	s_waitcnt vmcnt(2)
	ds_write_b128 v124, v[20:23] offset:16384
	s_waitcnt vmcnt(1)
	ds_write_b128 v64, v[24:27] offset:32768
	v_add_u32_e32 v64, 0, v112
	s_waitcnt vmcnt(0)
	ds_write_b128 v64, v[28:31] offset:32768

.LBB0_575:
	ds_read_b128 v[164:167], v129 offset:16384
	ds_read_b128 v[168:171], v130 offset:16384
	ds_read_b128 v[172:175], v131 offset:16384
	ds_read_b128 v[176:179], v129 offset:17408
	ds_read_b128 v[180:183], v132 offset:16384
	ds_read_b128 v[184:187], v130 offset:17408
	ds_read_b128 v[188:191], v131 offset:17408
	ds_read_b128 v[192:195], v129 offset:24576
	ds_read_b128 v[196:199], v132 offset:17408
	ds_read_b128 v[200:203], v130 offset:24576
	ds_read_b128 v[204:207], v131 offset:24576
	ds_read_b128 v[208:211], v129 offset:25600
	ds_read_b128 v[212:215], v132 offset:24576
	ds_read_b128 v[216:219], v130 offset:25600
	ds_read_b128 v[220:223], v131 offset:25600
	v_sub_f32_e32 v64, v84, v96
	v_exp_f32_e32 v96, v64
	v_sub_f32_e32 v64, v85, v97
	v_exp_f32_e32 v97, v64
	v_sub_f32_e32 v64, v86, v98
	v_exp_f32_e32 v98, v64
	v_sub_f32_e32 v64, v87, v99
	v_exp_f32_e32 v99, v64
	v_sub_f32_e32 v64, v80, v92
	v_exp_f32_e32 v152, v64
	v_sub_f32_e32 v64, v81, v93
	v_exp_f32_e32 v153, v64
	v_sub_f32_e32 v64, v82, v94
	v_exp_f32_e32 v154, v64
	v_sub_f32_e32 v64, v83, v95
	s_waitcnt lgkmcnt(11)
	v_mfma_f32_16x16x32_bf16 v[84:87], v[164:167], v[0:3], v[240:243]
	ds_read_b128 v[224:227], v132 offset:25600
	ds_read_b64_tr_b16 v[228:229], v146 offset:32768
	ds_read_b64_tr_b16 v[230:231], v148 offset:32768
	ds_read_b64_tr_b16 v[166:167], v148 offset:40960
	v_exp_f32_e32 v155, v64
	v_sub_f32_e32 v64, v76, v88
	v_mfma_f32_16x16x32_bf16 v[84:87], v[168:171], v[4:7], v[84:87]
	v_exp_f32_e32 v156, v64
	v_sub_f32_e32 v64, v77, v89
	v_mfma_f32_16x16x32_bf16 v[92:95], v[176:179], v[0:3], v[240:243]
	v_exp_f32_e32 v157, v64
	v_sub_f32_e32 v64, v78, v90
	v_exp_f32_e32 v158, v64
	v_sub_f32_e32 v64, v79, v91
	s_waitcnt lgkmcnt(10)
	v_mfma_f32_16x16x32_bf16 v[88:91], v[184:187], v[4:7], v[92:95]
	ds_read_b64_tr_b16 v[164:165], v146 offset:40960
	ds_read_b64_tr_b16 v[168:169], v139 offset:32768
	ds_read_b64_tr_b16 v[170:171], v142 offset:32768
	ds_read_b64_tr_b16 v[178:179], v142 offset:40960
	ds_read_b64_tr_b16 v[176:177], v139 offset:40960
	v_exp_f32_e32 v159, v64
	v_mfma_f32_16x16x32_bf16 v[80:83], v[172:175], v[8:11], v[84:87]
	v_sub_f32_e32 v64, v72, v66
	v_sub_f32_e32 v70, v73, v67
	v_mfma_f32_16x16x32_bf16 v[76:79], v[188:191], v[8:11], v[88:91]
	v_sub_f32_e32 v68, v74, v68
	s_and_b64 vcc, exec, s[10:11]
	v_mfma_f32_16x16x32_bf16 v[92:95], v[192:195], v[0:3], v[240:243]
	v_mfma_f32_16x16x32_bf16 v[76:79], v[196:199], v[12:15], v[76:79]
	s_waitcnt lgkmcnt(11)
	v_mfma_f32_16x16x32_bf16 v[88:91], v[200:203], v[4:7], v[92:95]
	ds_read_b64_tr_b16 v[184:185], v141 offset:32768
	ds_read_b64_tr_b16 v[186:187], v145 offset:32768
	ds_read_b64_tr_b16 v[174:175], v145 offset:40960
	ds_read_b64_tr_b16 v[172:173], v141 offset:40960
	v_mfma_f32_16x16x32_bf16 v[80:83], v[180:183], v[12:15], v[80:83]
	v_exp_f32_e32 v160, v64
	v_exp_f32_e32 v161, v70
	v_mfma_f32_16x16x32_bf16 v[84:87], v[204:207], v[8:11], v[88:91]
	v_exp_f32_e32 v162, v68
	v_mfma_f32_16x16x32_bf16 v[64:67], v[212:215], v[12:15], v[84:87]
	v_sub_f32_e32 v68, v75, v69
	v_exp_f32_e32 v163, v68
	v_mfma_f32_16x16x32_bf16 v[84:87], v[208:211], v[0:3], v[240:243]
	v_cvt_pk_bf16_f32 v92, v96, v97
	v_cvt_pk_bf16_f32 v93, v98, v99
	s_waitcnt lgkmcnt(11)
	v_mfma_f32_16x16x32_bf16 v[84:87], v[216:219], v[4:7], v[84:87]
	ds_read_b64_tr_b16 v[188:189], v140 offset:32768
	ds_read_b64_tr_b16 v[190:191], v143 offset:32768
	ds_read_b64_tr_b16 v[194:195], v143 offset:40960
	ds_read_b64_tr_b16 v[192:193], v140 offset:40960
	v_cvt_pk_bf16_f32 v94, v152, v153
	v_cvt_pk_bf16_f32 v95, v154, v155
	v_mfma_f32_16x16x32_bf16 v[68:71], v[220:223], v[8:11], v[84:87]
	s_nop 2
	v_cvt_pk_bf16_f32 v84, v156, v157
	v_mfma_f32_16x16x32_bf16 v[68:71], v[224:227], v[12:15], v[68:71]
	v_cvt_pk_bf16_f32 v85, v158, v159
	v_cvt_pk_bf16_f32 v86, v160, v161
	s_waitcnt lgkmcnt(11)
	v_mfma_f32_16x16x32_bf16 v[60:63], v[228:231], v[92:95], v[60:63]
	ds_read_b64_tr_b16 v[196:197], v147 offset:32768
	ds_read_b64_tr_b16 v[198:199], v149 offset:32768
	ds_read_b64_tr_b16 v[202:203], v149 offset:40960
	ds_read_b64_tr_b16 v[200:201], v147 offset:40960
	v_cvt_pk_bf16_f32 v87, v162, v163
	s_nop 1
	v_mfma_f32_16x16x32_bf16 v[60:63], v[164:167], v[84:87], v[60:63]
	s_waitcnt lgkmcnt(11)
	v_mfma_f32_16x16x32_bf16 v[56:59], v[168:171], v[92:95], v[56:59]
	ds_read_b64_tr_b16 v[180:181], v133 offset:32768
	ds_read_b64_tr_b16 v[182:183], v134 offset:32768
	ds_read_b64_tr_b16 v[206:207], v134 offset:40960
	ds_read_b64_tr_b16 v[204:205], v133 offset:40960
	v_mfma_f32_16x16x32_bf16 v[56:59], v[176:179], v[84:87], v[56:59]
	s_waitcnt lgkmcnt(11)
	v_mfma_f32_16x16x32_bf16 v[52:55], v[184:187], v[92:95], v[52:55]
	ds_read_b64_tr_b16 v[212:213], v135 offset:32768
	ds_read_b64_tr_b16 v[214:215], v136 offset:32768
	ds_read_b64_tr_b16 v[210:211], v136 offset:40960
	ds_read_b64_tr_b16 v[208:209], v135 offset:40960
	v_mfma_f32_16x16x32_bf16 v[52:55], v[172:175], v[84:87], v[52:55]
	s_waitcnt lgkmcnt(11)
	v_mfma_f32_16x16x32_bf16 v[48:51], v[188:191], v[92:95], v[48:51]
	ds_read_b64_tr_b16 v[216:217], v137 offset:32768
	ds_read_b64_tr_b16 v[218:219], v138 offset:32768
	ds_read_b64_tr_b16 v[222:223], v138 offset:40960
	ds_read_b64_tr_b16 v[220:221], v137 offset:40960
	v_mfma_f32_16x16x32_bf16 v[48:51], v[192:195], v[84:87], v[48:51]
	s_waitcnt lgkmcnt(11)
	v_mfma_f32_16x16x32_bf16 v[32:35], v[196:199], v[92:95], v[32:35]
	v_mfma_f32_16x16x32_bf16 v[32:35], v[200:203], v[84:87], v[32:35]
	s_waitcnt lgkmcnt(7)
	v_mfma_f32_16x16x32_bf16 v[36:39], v[180:183], v[92:95], v[36:39]
	v_mfma_f32_16x16x32_bf16 v[36:39], v[204:207], v[84:87], v[36:39]
	s_waitcnt lgkmcnt(3)
	v_mfma_f32_16x16x32_bf16 v[40:43], v[212:215], v[92:95], v[40:43]
	v_mfma_f32_16x16x32_bf16 v[40:43], v[208:211], v[84:87], v[40:43]
	s_waitcnt lgkmcnt(0)
	v_mfma_f32_16x16x32_bf16 v[44:47], v[216:219], v[92:95], v[44:47]
	v_mfma_f32_16x16x32_bf16 v[44:47], v[220:223], v[84:87], v[44:47]
	s_cbranch_vccnz .LBB0_577
	v_add_u32_e32 v72, 0, v109
	s_waitcnt vmcnt(3)
	ds_write_b128 v100, v[16:19]
	s_waitcnt vmcnt(2)
	ds_write_b128 v124, v[20:23]
	s_waitcnt vmcnt(1)
	ds_write_b128 v72, v[24:27] offset:49152
	v_add_u32_e32 v72, 0, v112
	s_waitcnt vmcnt(0)
	ds_write_b128 v72, v[28:31] offset:49152

.LBB0_581:
	v_add_f32_e32 v96, v150, v96
	v_add_f32_e32 v96, v97, v96
	v_add_f32_e32 v96, v98, v96
	v_add_f32_e32 v96, v99, v96
	v_add_f32_e32 v96, v152, v96
	v_add_f32_e32 v96, v153, v96
	v_add_f32_e32 v96, v154, v96
	v_add_f32_e32 v96, v155, v96
	v_add_f32_e32 v96, v156, v96
	v_add_f32_e32 v96, v157, v96
	v_add_f32_e32 v96, v158, v96
	s_waitcnt lgkmcnt(3)
	v_add_f32_e32 v96, v159, v96
	v_sub_f32_e32 v80, v80, v92
	v_add_f32_e32 v96, v160, v96
	v_exp_f32_e32 v80, v80
	v_sub_f32_e32 v81, v81, v93
	v_add_f32_e32 v96, v161, v96
	v_exp_f32_e32 v81, v81
	v_sub_f32_e32 v82, v82, v94
	v_add_f32_e32 v96, v162, v96
	v_exp_f32_e32 v82, v82
	v_sub_f32_e32 v83, v83, v95
	s_waitcnt lgkmcnt(2)
	v_add_f32_e32 v96, v163, v96
	v_exp_f32_e32 v83, v83
	v_sub_f32_e32 v76, v76, v88
	v_add_f32_e32 v92, v96, v80
	v_exp_f32_e32 v76, v76
	v_sub_f32_e32 v77, v77, v89
	v_add_f32_e32 v92, v81, v92
	v_exp_f32_e32 v77, v77
	v_sub_f32_e32 v78, v78, v90
	v_add_f32_e32 v92, v82, v92
	v_exp_f32_e32 v78, v78
	v_sub_f32_e32 v79, v79, v91
	s_waitcnt lgkmcnt(1)
	v_add_f32_e32 v92, v83, v92
	v_exp_f32_e32 v79, v79
	v_sub_f32_e32 v64, v64, v84
	s_waitcnt lgkmcnt(0)
	v_add_f32_e32 v88, v76, v92
	v_exp_f32_e32 v64, v64
	v_sub_f32_e32 v65, v65, v85
	v_sub_f32_e32 v68, v68, v72
	v_add_f32_e32 v88, v77, v88
	v_exp_f32_e32 v65, v65
	v_sub_f32_e32 v66, v66, v86
	v_exp_f32_e32 v72, v68
	v_add_f32_e32 v88, v78, v88
	v_exp_f32_e32 v66, v66
	v_sub_f32_e32 v67, v67, v87
	v_sub_f32_e32 v68, v69, v73
	v_add_f32_e32 v88, v79, v88
	v_exp_f32_e32 v67, v67
	v_exp_f32_e32 v73, v68
	v_add_f32_e32 v84, v64, v88
	v_sub_f32_e32 v68, v70, v74
	v_add_f32_e32 v84, v65, v84
	v_exp_f32_e32 v74, v68
	v_add_f32_e32 v84, v66, v84
	v_sub_f32_e32 v68, v71, v75
	v_add_f32_e32 v84, v67, v84
	v_exp_f32_e32 v75, v68
	v_add_f32_e32 v68, v72, v84
	v_add_f32_e32 v68, v73, v68
	v_add_f32_e32 v68, v74, v68
	v_add_f32_e32 v150, v75, v68
	v_cvt_pk_bf16_f32 v68, v80, v81
	v_cvt_pk_bf16_f32 v69, v82, v83
	v_cvt_pk_bf16_f32 v70, v76, v77
	v_cvt_pk_bf16_f32 v71, v78, v79
	v_cvt_pk_bf16_f32 v64, v64, v65
	v_cvt_pk_bf16_f32 v65, v66, v67
	v_cvt_pk_bf16_f32 v66, v72, v73
	v_cvt_pk_bf16_f32 v67, v74, v75
	s_waitcnt lgkmcnt(0)
	s_barrier
	s_add_i32 s20, s19, 2
	s_add_i32 s18, s18, -2
	s_add_i32 s17, s17, 0xffd10000
	s_cmp_ge_u32 s19, s16
	v_add_u32_e32 v151, 0xfffffe00, v151
	s_cbranch_scc1 .LBB0_583
	s_mov_b32 s19, s20
	s_and_b64 vcc, exec, s[12:13]
	s_cbranch_vccz .LBB0_566
	s_branch .LBB0_567

.LBB0_1899:
	v_pk_add_f32 v[0:1], v[0:1], v[16:17] op_sel_hi:[1,0]
	v_pk_add_f32 v[2:3], v[2:3], v[16:17] op_sel_hi:[1,0]
	v_pk_mul_f32 v[18:19], v[0:1], s[80:81] op_sel_hi:[1,0]
	v_pk_add_f32 v[0:1], v[4:5], v[16:17] op_sel_hi:[1,0]
	v_pk_mul_f32 v[2:3], v[2:3], s[80:81] op_sel_hi:[1,0]
	v_pk_mul_f32 v[20:21], v[0:1], s[80:81] op_sel_hi:[1,0]
	v_pk_add_f32 v[0:1], v[6:7], v[16:17] op_sel_hi:[1,0]
	s_sub_i32 s10, 63, s1
	v_pk_mul_f32 v[0:1], v[0:1], s[80:81] op_sel_hi:[1,0]
	ds_write_b128 v114, v[0:3] offset:16
	v_pk_add_f32 v[0:1], v[8:9], v[16:17] op_sel_hi:[1,0]
	v_pk_add_f32 v[2:3], v[10:11], v[16:17] op_sel_hi:[1,0]
	v_pk_mul_f32 v[0:1], v[0:1], s[80:81] op_sel_hi:[1,0]
	v_pk_mul_f32 v[2:3], v[2:3], s[80:81] op_sel_hi:[1,0]
	ds_write_b128 v114, v[0:3] offset:32
	v_pk_add_f32 v[0:1], v[12:13], v[16:17] op_sel_hi:[1,0]
	v_pk_add_f32 v[2:3], v[14:15], v[16:17] op_sel_hi:[1,0]
	v_pk_mul_f32 v[0:1], v[0:1], s[80:81] op_sel_hi:[1,0]
	v_pk_mul_f32 v[2:3], v[2:3], s[80:81] op_sel_hi:[1,0]
	ds_write_b128 v114, v[18:21]
	ds_write_b128 v114, v[0:3] offset:48
	s_waitcnt lgkmcnt(0)
	s_barrier
	s_load_dwordx2 s[6:7], s[52:53], 0x108
	s_load_dwordx2 s[46:47], s[52:53], 0x138
	v_mov_b32_e32 v126, v108
	s_lshl_b32 s5, s10, 7
	s_add_i32 s0, s5, s57
	v_and_b32_e32 v32, 15, v126
	v_or_b32_e32 v125, s0, v32
	v_readlane_b32 s0, v247, 37
	s_lshl_b32 s0, s0, 1
	s_waitcnt lgkmcnt(0)
	s_add_u32 s44, s6, s0
	v_and_b32_e32 v0, -16, v126
	s_addc_u32 s45, s7, 0
	v_mad_u64_u32 v[8:9], s[6:7], v125, s59, v[0:1]
	v_add_u32_e32 v4, 64, v8
	v_add_u32_e32 v9, 0x80, v8
	v_add_u32_e32 v12, 0xc0, v8
	global_load_dwordx4 v[0:3], v8, s[44:45] offset:3072
	s_nop 0
	global_load_dwordx4 v[4:7], v4, s[44:45] offset:3072
	s_nop 0
	global_load_dwordx4 v[8:11], v9, s[44:45] offset:3072
	s_nop 0
	global_load_dwordx4 v[12:15], v12, s[44:45] offset:3072
	v_lshl_add_u32 v16, v125, 2, s79
	ds_read_b32 v127, v16
	s_lshl_b32 s4, s10, 1
	s_add_u32 s48, s44, 0x1000
	s_addc_u32 s49, s45, 0
	s_or_b32 s11, s4, 1
	s_add_u32 s68, s44, 0x1400
	s_addc_u32 s69, s45, 0
	s_waitcnt lgkmcnt(0)
	v_mov_b32_e32 v240, v127
	v_mov_b32_e32 v241, v127
	v_mov_b32_e32 v242, v127
	v_mov_b32_e32 v243, v127
	s_waitcnt lgkmcnt(0)
	s_barrier
	s_mul_i32 s12, s11, 0x178000
	s_add_u32 s6, s48, s12
	s_addc_u32 s7, s49, 0
	v_lshl_add_u64 v[20:21], s[6:7], 0, v[104:105]
	global_load_dwordx4 v[16:19], v[20:21], off
	v_add_co_u32_e32 v20, vcc, s51, v20
	v_add_u32_e32 v100, 0, v110
	s_nop 0
	v_addc_co_u32_e32 v21, vcc, 0, v21, vcc
	global_load_dwordx4 v[20:23], v[20:21], off
	v_add_u32_e32 v124, 0, v111
	s_waitcnt vmcnt(1)
	ds_write_b128 v100, v[16:19]
	s_waitcnt vmcnt(0)
	ds_write_b128 v124, v[20:23]
	s_waitcnt lgkmcnt(0)
	s_waitcnt lgkmcnt(0)
	s_barrier
	v_cndmask_b32_e64 v24, 0, 1, s[74:75]
	v_cmp_ne_u32_e64 s[6:7], 1, v24
	s_andn2_b64 vcc, exec, s[74:75]
	s_mul_i32 s10, s10, 0x2f0000
	s_cbranch_vccnz .LBB0_1901
	s_add_u32 s8, s48, s10
	s_addc_u32 s9, s49, 0
	v_lshl_add_u64 v[16:17], s[8:9], 0, v[104:105]
	s_add_u32 s8, s68, s12
	v_add_co_u32_e32 v20, vcc, 0xbc000, v16
	s_addc_u32 s9, s69, 0
	s_nop 0
	v_addc_co_u32_e32 v21, vcc, 0, v17, vcc
	v_lshl_add_u64 v[24:25], s[8:9], 0, v[104:105]
	v_add_co_u32_e32 v28, vcc, 0xbc000, v24
	global_load_dwordx4 v[16:19], v[16:17], off
	s_nop 0
	global_load_dwordx4 v[20:23], v[20:21], off
	v_addc_co_u32_e32 v29, vcc, 0, v25, vcc
	global_load_dwordx4 v[24:27], v[24:25], off
	s_nop 0
	global_load_dwordx4 v[28:31], v[28:29], off
	s_waitcnt lgkmcnt(0)

.LBB0_1903:
	v_lshlrev_b32_e32 v33, 1, v32
	v_and_b32_e32 v34, 3, v126
	v_ashrrev_i32_e32 v96, 4, v126
	v_and_or_b32 v33, v33, 24, v34
	v_lshlrev_b32_e32 v46, 8, v33
	v_xor_b32_e32 v33, v96, v32
	v_lshl_add_u32 v33, v33, 4, v46
	v_add_u32_e32 v34, 4, v96
	v_xor_b32_e32 v34, v34, v32
	v_add_u32_e32 v129, 0, v33
	v_lshl_add_u32 v38, v34, 4, v46
	ds_read_b128 v[34:37], v129
	v_add_u32_e32 v130, 0, v38
	ds_read_b128 v[38:41], v130
	v_add_u32_e32 v33, 8, v96
	s_waitcnt lgkmcnt(1)
	v_mfma_f32_16x16x32_bf16 v[34:37], v[34:37], v[0:3], v[240:243]
	v_xor_b32_e32 v33, v33, v32
	v_lshl_add_u32 v33, v33, 4, v46
	v_add_u32_e32 v131, 0, v33
	v_add_u32_e32 v33, 12, v96
	ds_read_b128 v[42:45], v131
	ds_read_b128 v[48:51], v129 offset:1024
	v_xor_b32_e32 v47, v33, v32
	s_waitcnt lgkmcnt(2)
	v_mfma_f32_16x16x32_bf16 v[32:35], v[38:41], v[4:7], v[34:37]
	ds_read_b128 v[52:55], v130 offset:1024
	s_and_b64 vcc, exec, s[6:7]
	s_nop 0
	v_lshl_add_u32 v36, v47, 4, v46
	v_add_u32_e32 v132, 0, v36
	ds_read_b128 v[36:39], v131 offset:1024
	s_waitcnt lgkmcnt(3)
	v_mfma_f32_16x16x32_bf16 v[32:35], v[42:45], v[8:11], v[32:35]
	ds_read_b128 v[40:43], v132
	ds_read_b128 v[56:59], v132 offset:1024
	s_waitcnt lgkmcnt(1)
	v_mfma_f32_16x16x32_bf16 v[44:47], v[40:43], v[12:15], v[32:35]
	v_mfma_f32_16x16x32_bf16 v[32:35], v[48:51], v[0:3], v[240:243]
	v_mfma_f32_16x16x32_bf16 v[32:35], v[52:55], v[4:7], v[32:35]
	v_mfma_f32_16x16x32_bf16 v[32:35], v[36:39], v[8:11], v[32:35]
	s_waitcnt lgkmcnt(0)
	v_mfma_f32_16x16x32_bf16 v[40:43], v[56:59], v[12:15], v[32:35]
	s_nop 5
	ds_read_b128 v[32:35], v129 offset:8192
	ds_read_b128 v[48:51], v129 offset:9216
	ds_read_b128 v[36:39], v130 offset:8192
	ds_read_b128 v[52:55], v130 offset:9216
	s_waitcnt lgkmcnt(3)
	v_mfma_f32_16x16x32_bf16 v[32:35], v[32:35], v[0:3], v[240:243]
	s_waitcnt lgkmcnt(1)
	v_mfma_f32_16x16x32_bf16 v[32:35], v[36:39], v[4:7], v[32:35]
	ds_read_b128 v[36:39], v131 offset:8192
	ds_read_b128 v[56:59], v131 offset:9216
	s_waitcnt lgkmcnt(1)
	v_mfma_f32_16x16x32_bf16 v[32:35], v[36:39], v[8:11], v[32:35]
	ds_read_b128 v[36:39], v132 offset:8192
	ds_read_b128 v[60:63], v132 offset:9216
	s_waitcnt lgkmcnt(1)
	v_mfma_f32_16x16x32_bf16 v[36:39], v[36:39], v[12:15], v[32:35]
	v_mfma_f32_16x16x32_bf16 v[32:35], v[48:51], v[0:3], v[240:243]
	v_mfma_f32_16x16x32_bf16 v[32:35], v[52:55], v[4:7], v[32:35]
	v_mfma_f32_16x16x32_bf16 v[32:35], v[56:59], v[8:11], v[32:35]
	s_waitcnt lgkmcnt(0)
	v_mfma_f32_16x16x32_bf16 v[32:35], v[60:63], v[12:15], v[32:35]
	s_cbranch_vccnz .LBB0_1905
	v_add_u32_e32 v48, 0, v109
	s_waitcnt vmcnt(3)
	ds_write_b128 v100, v[16:19] offset:16384
	s_waitcnt vmcnt(2)
	ds_write_b128 v124, v[20:23] offset:16384
	s_waitcnt vmcnt(1)
	ds_write_b128 v48, v[24:27] offset:32768
	v_add_u32_e32 v48, 0, v112
	s_waitcnt vmcnt(0)
	ds_write_b128 v48, v[28:31] offset:32768

.LBB0_1911:
	v_sub_f32_e32 v44, v44, v60
	v_exp_f32_e32 v44, v44
	v_sub_f32_e32 v45, v45, v61
	v_cmp_le_i32_e32 vcc, v64, v125
	v_exp_f32_e32 v45, v45
	v_bfe_u32 v84, v126, 1, 1
	v_cndmask_b32_e32 v97, 0, v44, vcc
	v_sub_f32_e32 v44, v46, v62
	v_exp_f32_e32 v44, v44
	v_cmp_lt_i32_e32 vcc, v64, v125
	v_sub_f32_e32 v46, v47, v63
	v_cndmask_b32_e32 v98, 0, v45, vcc
	v_or_b32_e32 v45, 2, v64
	v_cmp_le_i32_e32 vcc, v45, v125
	v_exp_f32_e32 v46, v46
	v_cndmask_b32_e32 v99, 0, v44, vcc
	v_or_b32_e32 v44, 3, v64
	v_cmp_le_i32_e32 vcc, v44, v125
	v_sub_f32_e32 v40, v40, v56
	v_exp_f32_e32 v40, v40
	v_or_b32_e32 v44, 4, v64
	v_sub_f32_e32 v41, v41, v57
	v_cndmask_b32_e32 v150, 0, v46, vcc
	v_exp_f32_e32 v41, v41
	v_cmp_le_i32_e32 vcc, v44, v125
	v_or_b32_e32 v68, 10, v84
	v_cvt_pk_bf16_f32 v44, v97, v98
	v_cndmask_b32_e32 v151, 0, v40, vcc
	v_or_b32_e32 v40, 5, v64
	v_cmp_le_i32_e32 vcc, v40, v125
	v_sub_f32_e32 v40, v42, v58
	v_cndmask_b32_e32 v152, 0, v41, vcc
	v_exp_f32_e32 v40, v40
	v_or_b32_e32 v41, 6, v64
	v_sub_f32_e32 v42, v43, v59
	v_cmp_le_i32_e32 vcc, v41, v125
	v_exp_f32_e32 v42, v42
	v_sub_f32_e32 v36, v36, v52
	v_exp_f32_e32 v36, v36
	v_cndmask_b32_e32 v153, 0, v40, vcc
	v_or_b32_e32 v40, 7, v64
	v_cmp_le_i32_e32 vcc, v40, v125
	v_add_u32_e32 v40, 32, v64
	v_cndmask_b32_e32 v154, 0, v42, vcc
	v_cmp_le_i32_e32 vcc, v40, v125
	v_sub_f32_e32 v37, v37, v53
	v_exp_f32_e32 v37, v37
	v_cndmask_b32_e32 v155, 0, v36, vcc
	v_add_u32_e32 v36, 33, v64
	v_cmp_le_i32_e32 vcc, v36, v125
	v_sub_f32_e32 v36, v38, v54
	v_exp_f32_e32 v36, v36
	v_cndmask_b32_e32 v156, 0, v37, vcc
	v_add_u32_e32 v37, 34, v64
	v_cmp_le_i32_e32 vcc, v37, v125
	v_sub_f32_e32 v38, v39, v55
	v_cndmask_b32_e32 v157, 0, v36, vcc
	v_add_u32_e32 v36, 35, v64
	v_cmp_le_i32_e32 vcc, v36, v125
	v_exp_f32_e32 v38, v38
	v_sub_f32_e32 v32, v32, v48
	v_exp_f32_e32 v32, v32
	v_add_u32_e32 v36, 36, v64
	v_cndmask_b32_e32 v158, 0, v38, vcc
	v_cmp_le_i32_e32 vcc, v36, v125
	v_sub_f32_e32 v33, v33, v49
	v_exp_f32_e32 v33, v33
	v_cndmask_b32_e32 v159, 0, v32, vcc
	v_add_u32_e32 v32, 37, v64
	v_cmp_le_i32_e32 vcc, v32, v125
	v_sub_f32_e32 v32, v34, v50
	v_exp_f32_e32 v32, v32
	v_sub_f32_e32 v34, v35, v51
	v_cndmask_b32_e32 v160, 0, v33, vcc
	v_add_u32_e32 v33, 38, v64
	v_exp_f32_e32 v34, v34
	v_cmp_le_i32_e32 vcc, v33, v125
	v_lshrrev_b32_e32 v33, 1, v126
	v_and_b32_e32 v33, 0x7ffffff8, v33
	v_cndmask_b32_e32 v161, 0, v32, vcc
	v_add_u32_e32 v32, 39, v64
	v_cmp_le_i32_e32 vcc, v32, v125
	v_bfe_u32 v32, v126, 2, 2
	v_lshlrev_b32_e32 v85, 2, v32
	v_cndmask_b32_e32 v162, 0, v34, vcc
	v_lshlrev_b32_e32 v34, 3, v126
	v_and_b32_e32 v92, 8, v34
	v_or_b32_e32 v34, v33, v32
	v_or_b32_e32 v33, 4, v33
	v_or_b32_e32 v32, v33, v32
	v_bfe_u32 v88, v33, 2, 2
	v_lshlrev_b32_e32 v86, 8, v34
	v_lshrrev_b32_e32 v34, 3, v126
	v_lshlrev_b32_e32 v93, 8, v32
	v_bitop3_b32 v32, v88, v84, v85 bitop3:0x36
	v_and_b32_e32 v87, 2, v34
	v_lshlrev_b32_e32 v32, 4, v32
	v_or_b32_e32 v34, v85, v87
	v_or3_b32 v61, v32, v93, v92
	v_or_b32_e32 v32, 2, v84
	v_or_b32_e32 v34, v34, v84
	v_bitop3_b32 v33, v85, v32, v87 bitop3:0x36
	v_lshlrev_b32_e32 v34, 4, v34
	v_lshlrev_b32_e32 v33, 4, v33
	v_or3_b32 v60, v34, v86, v92
	v_or3_b32 v62, v33, v86, v92
	v_bitop3_b32 v36, v88, v32, v85 bitop3:0x36
	ds_read_b128 v[32:35], v129 offset:16384
	v_lshlrev_b32_e32 v36, 4, v36
	v_or3_b32 v63, v36, v93, v92
	ds_read_b128 v[36:39], v130 offset:16384
	s_waitcnt lgkmcnt(1)
	v_mfma_f32_16x16x32_bf16 v[32:35], v[32:35], v[0:3], v[240:243]
	v_or_b32_e32 v64, 4, v84
	v_bitop3_b32 v40, v85, v64, v87 bitop3:0x36
	v_lshlrev_b32_e32 v52, 4, v40
	ds_read_b128 v[40:43], v131 offset:16384
	ds_read_b128 v[48:51], v129 offset:17408
	s_waitcnt lgkmcnt(2)
	v_mfma_f32_16x16x32_bf16 v[32:35], v[36:39], v[4:7], v[32:35]
	v_or3_b32 v89, v52, v86, v92
	ds_read_b128 v[52:55], v132 offset:16384
	ds_read_b128 v[56:59], v130 offset:17408
	v_bitop3_b32 v36, v88, v64, v85 bitop3:0x36
	s_waitcnt lgkmcnt(3)
	v_mfma_f32_16x16x32_bf16 v[32:35], v[40:43], v[8:11], v[32:35]
	v_lshlrev_b32_e32 v64, 4, v36
	v_or3_b32 v90, v64, v93, v92
	v_or_b32_e32 v64, 6, v84
	s_waitcnt lgkmcnt(1)
	v_mfma_f32_16x16x32_bf16 v[76:79], v[52:55], v[12:15], v[32:35]
	ds_read_b128 v[36:39], v131 offset:17408
	ds_read_b128 v[40:43], v132 offset:17408
	v_or_b32_e32 v52, 8, v84
	v_bitop3_b32 v32, v85, v64, v87 bitop3:0x36
	v_lshlrev_b32_e32 v32, 4, v32
	v_or3_b32 v91, v32, v86, v92
	v_mfma_f32_16x16x32_bf16 v[32:35], v[48:51], v[0:3], v[240:243]
	v_bitop3_b32 v48, v88, v64, v85 bitop3:0x36
	v_lshlrev_b32_e32 v48, 4, v48
	v_or3_b32 v94, v48, v93, v92
	s_waitcnt lgkmcnt(2)
	v_mfma_f32_16x16x32_bf16 v[32:35], v[56:59], v[4:7], v[32:35]
	ds_read_b128 v[48:51], v129 offset:24576
	v_bitop3_b32 v53, v85, v52, v87 bitop3:0x36
	v_bitop3_b32 v52, v88, v52, v85 bitop3:0x36
	s_waitcnt lgkmcnt(2)
	v_mfma_f32_16x16x32_bf16 v[32:35], v[36:39], v[8:11], v[32:35]
	v_lshlrev_b32_e32 v36, 4, v53
	v_or3_b32 v95, v36, v86, v92
	ds_read_b128 v[36:39], v130 offset:24576
	s_waitcnt lgkmcnt(1)
	v_mfma_f32_16x16x32_bf16 v[48:51], v[48:51], v[0:3], v[240:243]
	v_lshlrev_b32_e32 v64, 4, v52
	v_or3_b32 v133, v64, v93, v92
	v_add_u32_e32 v142, 0, v60
	v_mfma_f32_16x16x32_bf16 v[72:75], v[40:43], v[12:15], v[32:35]
	s_nop 2
	ds_read_b128 v[32:35], v131 offset:24576
	ds_read_b128 v[40:43], v129 offset:25600
	ds_read_b128 v[52:55], v132 offset:24576
	ds_read_b128 v[56:59], v130 offset:25600
	v_add_u32_e32 v146, 0, v61
	s_waitcnt lgkmcnt(4)
	v_mfma_f32_16x16x32_bf16 v[36:39], v[36:39], v[4:7], v[48:51]
	v_cvt_pk_bf16_f32 v45, v99, v150
	v_cvt_pk_bf16_f32 v46, v151, v152
	v_cvt_pk_bf16_f32 v47, v153, v154
	s_waitcnt lgkmcnt(3)
	v_mfma_f32_16x16x32_bf16 v[32:35], v[32:35], v[8:11], v[36:39]
	ds_read_b128 v[48:51], v131 offset:25600
	v_add_u32_e32 v136, 0, v62
	v_add_u32_e32 v137, 0, v63
	s_waitcnt lgkmcnt(2)
	v_mfma_f32_16x16x32_bf16 v[64:67], v[52:55], v[12:15], v[32:35]
	v_bitop3_b32 v36, v85, v68, v87 bitop3:0x36
	v_lshlrev_b32_e32 v69, 4, v36
	ds_read_b128 v[36:39], v132 offset:25600
	v_bitop3_b32 v32, v88, v68, v85 bitop3:0x36
	v_lshlrev_b32_e32 v52, 4, v32
	v_mfma_f32_16x16x32_bf16 v[32:35], v[40:43], v[0:3], v[240:243]
	v_or_b32_e32 v40, 12, v84
	v_bitop3_b32 v41, v85, v40, v87 bitop3:0x36
	v_lshlrev_b32_e32 v41, 4, v41
	s_waitcnt lgkmcnt(2)
	v_mfma_f32_16x16x32_bf16 v[32:35], v[56:59], v[4:7], v[32:35]
	v_or3_b32 v135, v52, v93, v92
	v_or3_b32 v138, v41, v86, v92
	v_bitop3_b32 v52, v88, v40, v85 bitop3:0x36
	s_waitcnt lgkmcnt(1)
	v_mfma_f32_16x16x32_bf16 v[32:35], v[48:51], v[8:11], v[32:35]
	ds_read_b64_tr_b16 v[40:41], v142 offset:32768
	ds_read_b64_tr_b16 v[42:43], v146 offset:32768
	v_or3_b32 v134, v69, v86, v92
	v_cvt_pk_bf16_f32 v80, v155, v156
	s_waitcnt lgkmcnt(2)
	v_mfma_f32_16x16x32_bf16 v[68:71], v[36:39], v[12:15], v[32:35]
	s_nop 2
	ds_read_b64_tr_b16 v[34:35], v146 offset:40960
	ds_read_b64_tr_b16 v[32:33], v142 offset:40960
	ds_read_b64_tr_b16 v[36:37], v136 offset:32768
	ds_read_b64_tr_b16 v[38:39], v137 offset:32768
	v_cvt_pk_bf16_f32 v81, v157, v158
	s_waitcnt lgkmcnt(4)
	v_mfma_f32_16x16x32_bf16 v[40:43], v[40:43], v[44:47], 0
	v_cvt_pk_bf16_f32 v82, v159, v160
	v_cvt_pk_bf16_f32 v83, v161, v162
	v_add_u32_e32 v139, 0, v89
	ds_read_b64_tr_b16 v[50:51], v137 offset:40960
	ds_read_b64_tr_b16 v[48:49], v136 offset:40960
	s_waitcnt lgkmcnt(4)
	v_mfma_f32_16x16x32_bf16 v[60:63], v[32:35], v[80:83], v[40:43]
	v_add_u32_e32 v145, 0, v90
	ds_read_b64_tr_b16 v[32:33], v139 offset:32768
	ds_read_b64_tr_b16 v[34:35], v145 offset:32768
	ds_read_b64_tr_b16 v[42:43], v145 offset:40960
	ds_read_b64_tr_b16 v[40:41], v139 offset:40960
	s_waitcnt lgkmcnt(6)
	v_mfma_f32_16x16x32_bf16 v[36:39], v[36:39], v[44:47], 0
	v_add_u32_e32 v140, 0, v91
	v_lshlrev_b32_e32 v56, 4, v52
	v_add_u32_e32 v147, 0, v94
	s_waitcnt lgkmcnt(4)
	v_mfma_f32_16x16x32_bf16 v[52:55], v[48:51], v[80:83], v[36:39]
	s_nop 2
	ds_read_b64_tr_b16 v[36:37], v140 offset:32768
	ds_read_b64_tr_b16 v[38:39], v147 offset:32768
	v_or3_b32 v89, v56, v93, v92
	v_or_b32_e32 v56, 14, v84
	s_waitcnt lgkmcnt(4)
	v_mfma_f32_16x16x32_bf16 v[32:35], v[32:35], v[44:47], 0
	v_bitop3_b32 v57, v85, v56, v87 bitop3:0x36
	v_add_u32_e32 v148, 0, v95
	v_add_u32_e32 v149, 0, v133
	s_waitcnt lgkmcnt(2)
	v_mfma_f32_16x16x32_bf16 v[48:51], v[40:43], v[80:83], v[32:35]
	s_nop 2
	ds_read_b64_tr_b16 v[34:35], v147 offset:40960
	ds_read_b64_tr_b16 v[32:33], v140 offset:40960
	v_lshlrev_b32_e32 v40, 4, v57
	v_or3_b32 v94, v40, v86, v92
	s_waitcnt lgkmcnt(2)
	v_mfma_f32_16x16x32_bf16 v[36:39], v[36:39], v[44:47], 0
	ds_read_b64_tr_b16 v[40:41], v148 offset:32768
	ds_read_b64_tr_b16 v[42:43], v149 offset:32768
	v_add_u32_e32 v133, 0, v134
	v_bitop3_b32 v88, v88, v56, v85 bitop3:0x36
	s_waitcnt lgkmcnt(2)
	v_mfma_f32_16x16x32_bf16 v[56:59], v[32:35], v[80:83], v[36:39]
	ds_read_b64_tr_b16 v[34:35], v149 offset:40960
	ds_read_b64_tr_b16 v[32:33], v148 offset:40960
	v_add_u32_e32 v134, 0, v135
	ds_read_b64_tr_b16 v[36:37], v133 offset:32768
	ds_read_b64_tr_b16 v[38:39], v134 offset:32768
	s_waitcnt lgkmcnt(4)
	v_mfma_f32_16x16x32_bf16 v[40:43], v[40:43], v[44:47], 0
	ds_read_b64_tr_b16 v[86:87], v134 offset:40960
	ds_read_b64_tr_b16 v[84:85], v133 offset:40960
	v_add_u32_e32 v135, 0, v138
	v_add_u32_e32 v138, 0, v89
	s_waitcnt lgkmcnt(4)
	v_mfma_f32_16x16x32_bf16 v[32:35], v[32:35], v[80:83], v[40:43]
	s_nop 2
	ds_read_b64_tr_b16 v[40:41], v135 offset:32768
	ds_read_b64_tr_b16 v[42:43], v138 offset:32768
	v_lshlrev_b32_e32 v95, 4, v88
	ds_read_b64_tr_b16 v[90:91], v138 offset:40960
	ds_read_b64_tr_b16 v[88:89], v135 offset:40960
	s_waitcnt lgkmcnt(6)
	v_mfma_f32_16x16x32_bf16 v[36:39], v[36:39], v[44:47], 0
	v_add_u32_e32 v141, 0, v94
	s_and_b64 vcc, exec, s[6:7]
	s_waitcnt lgkmcnt(4)
	v_mfma_f32_16x16x32_bf16 v[36:39], v[84:87], v[80:83], v[36:39]
	v_or3_b32 v84, v95, v93, v92
	v_add_u32_e32 v143, 0, v84
	ds_read_b64_tr_b16 v[84:85], v141 offset:32768
	ds_read_b64_tr_b16 v[86:87], v143 offset:32768
	s_waitcnt lgkmcnt(4)
	v_mfma_f32_16x16x32_bf16 v[40:43], v[40:43], v[44:47], 0
	s_waitcnt lgkmcnt(2)
	v_mfma_f32_16x16x32_bf16 v[40:43], v[88:91], v[80:83], v[40:43]
	ds_read_b64_tr_b16 v[90:91], v143 offset:40960
	ds_read_b64_tr_b16 v[88:89], v141 offset:40960
	s_waitcnt lgkmcnt(2)
	v_mfma_f32_16x16x32_bf16 v[44:47], v[84:87], v[44:47], 0
	s_waitcnt lgkmcnt(0)
	v_mfma_f32_16x16x32_bf16 v[44:47], v[88:91], v[80:83], v[44:47]
	s_cbranch_vccnz .LBB0_1913
	v_add_u32_e32 v80, 0, v109
	s_waitcnt vmcnt(3)
	ds_write_b128 v100, v[16:19]
	s_waitcnt vmcnt(2)
	ds_write_b128 v124, v[20:23]
	s_waitcnt vmcnt(1)
	ds_write_b128 v80, v[24:27] offset:49152
	v_add_u32_e32 v80, 0, v112
	s_waitcnt vmcnt(0)
	ds_write_b128 v80, v[28:31] offset:49152

.LBB0_1917:
	s_waitcnt lgkmcnt(2)
	v_sub_f32_e32 v72, v72, v88
	v_sub_f32_e32 v73, v73, v89
	v_sub_f32_e32 v74, v74, v90
	v_sub_f32_e32 v75, v75, v91
	v_add_f32_e32 v88, 0, v97
	v_add_f32_e32 v88, v98, v88
	v_add_f32_e32 v88, v99, v88
	v_add_f32_e32 v88, v150, v88
	v_add_f32_e32 v88, v151, v88
	v_add_f32_e32 v88, v152, v88
	v_add_f32_e32 v88, v153, v88
	v_add_f32_e32 v88, v154, v88
	v_add_f32_e32 v88, v155, v88
	v_sub_f32_e32 v76, v76, v92
	s_waitcnt lgkmcnt(1)
	v_add_f32_e32 v88, v156, v88
	v_sub_f32_e32 v77, v77, v93
	v_sub_f32_e32 v64, v64, v84
	v_add_f32_e32 v88, v157, v88
	v_exp_f32_e32 v76, v76
	v_exp_f32_e32 v77, v77
	v_exp_f32_e32 v64, v64
	v_add_f32_e32 v88, v158, v88
	v_sub_f32_e32 v78, v78, v94
	v_add_f32_e32 v88, v159, v88
	v_exp_f32_e32 v78, v78
	v_sub_f32_e32 v79, v79, v95
	v_sub_f32_e32 v65, v65, v85
	v_add_f32_e32 v88, v160, v88
	v_exp_f32_e32 v79, v79
	v_sub_f32_e32 v66, v66, v86
	v_add_f32_e32 v88, v161, v88
	v_cndmask_b32_e64 v76, 0, v76, s[36:37]
	v_cndmask_b32_e64 v77, 0, v77, s[38:39]
	v_exp_f32_e32 v72, v72
	v_exp_f32_e32 v73, v73
	v_exp_f32_e32 v66, v66
	v_sub_f32_e32 v67, v67, v87
	v_cndmask_b32_e64 v84, 0, v64, s[18:19]
	s_waitcnt lgkmcnt(0)
	v_add_f32_e32 v88, v162, v88
	v_sub_f32_e32 v64, v68, v80
	v_cvt_pk_bf16_f32 v68, v76, v77
	v_add_f32_e32 v76, v88, v76
	v_cndmask_b32_e64 v78, 0, v78, s[40:41]
	v_exp_f32_e32 v74, v74
	v_add_f32_e32 v76, v77, v76
	v_cndmask_b32_e64 v79, 0, v79, s[42:43]
	v_exp_f32_e32 v75, v75
	v_exp_f32_e32 v65, v65
	v_add_f32_e32 v76, v78, v76
	v_cndmask_b32_e64 v72, 0, v72, s[26:27]
	v_cndmask_b32_e64 v73, 0, v73, s[28:29]
	v_cndmask_b32_e64 v86, 0, v66, s[22:23]
	v_add_f32_e32 v76, v79, v76
	v_exp_f32_e32 v67, v67
	v_sub_f32_e32 v66, v70, v82
	v_cvt_pk_bf16_f32 v70, v72, v73
	v_add_f32_e32 v72, v72, v76
	v_cndmask_b32_e64 v74, 0, v74, s[30:31]
	v_add_f32_e32 v72, v73, v72
	v_cndmask_b32_e64 v75, 0, v75, s[34:35]
	v_cndmask_b32_e64 v85, 0, v65, s[20:21]
	v_add_f32_e32 v72, v74, v72
	v_exp_f32_e32 v64, v64
	v_sub_f32_e32 v65, v69, v81
	v_add_f32_e32 v72, v75, v72
	v_cndmask_b32_e64 v87, 0, v67, s[24:25]
	v_exp_f32_e32 v65, v65
	v_add_f32_e32 v72, v84, v72
	v_exp_f32_e32 v66, v66
	v_sub_f32_e32 v67, v71, v83
	v_add_f32_e32 v72, v85, v72
	v_exp_f32_e32 v67, v67
	v_add_f32_e32 v72, v86, v72
	v_cndmask_b32_e64 v80, 0, v64, s[10:11]
	v_add_f32_e32 v72, v87, v72
	v_cndmask_b32_e64 v81, 0, v65, s[12:13]
	v_add_f32_e32 v72, v80, v72
	v_cndmask_b32_e64 v82, 0, v66, s[14:15]
	v_add_f32_e32 v72, v81, v72
	v_cndmask_b32_e64 v83, 0, v67, s[16:17]
	v_add_f32_e32 v72, v82, v72
	v_cvt_pk_bf16_f32 v69, v78, v79
	v_cvt_pk_bf16_f32 v71, v74, v75
	v_cvt_pk_bf16_f32 v64, v84, v85
	v_cvt_pk_bf16_f32 v65, v86, v87
	v_cvt_pk_bf16_f32 v66, v80, v81
	v_cvt_pk_bf16_f32 v67, v82, v83
	v_add_f32_e32 v150, v83, v72
	s_waitcnt lgkmcnt(0)
	s_barrier
	v_lshlrev_b32_e32 v151, 5, v96
	s_mov_b32 s12, 2
	s_mov_b32 s5, s81
	s_mov_b32 s10, s66
	s_mov_b32 s11, s64
	s_and_b64 vcc, exec, s[8:9]
	s_cbranch_vccnz .LBB0_1919

.LBB0_1919:
	ds_read_b128 v[88:91], v129
	ds_read_b128 v[92:95], v129 offset:1024
	ds_read_b128 v[96:99], v130
	ds_read_b128 v[152:155], v130 offset:1024
	ds_read_b128 v[176:179], v131
	ds_read_b128 v[180:183], v131 offset:1024
	ds_read_b128 v[184:187], v132
	ds_read_b128 v[188:191], v132 offset:1024
	ds_read_b128 v[192:195], v129 offset:8192
	ds_read_b128 v[196:199], v129 offset:9216
	ds_read_b128 v[200:203], v130 offset:8192
	ds_read_b128 v[204:207], v130 offset:9216
	ds_read_b128 v[208:211], v131 offset:8192
	ds_read_b128 v[212:215], v131 offset:9216
	ds_read_b128 v[216:219], v132 offset:8192
	s_and_b64 vcc, exec, s[6:7]
	s_waitcnt lgkmcnt(11)
	v_mfma_f32_16x16x32_bf16 v[72:75], v[88:91], v[0:3], v[240:243]
	ds_read_b128 v[220:223], v132 offset:9216
	ds_read_b64_tr_b16 v[224:225], v142 offset:49152
	ds_read_b64_tr_b16 v[226:227], v146 offset:49152
	ds_read_b64_tr_b16 v[230:231], v146 offset:57344
	v_mfma_f32_16x16x32_bf16 v[72:75], v[96:99], v[4:7], v[72:75]
	v_mfma_f32_16x16x32_bf16 v[76:79], v[92:95], v[0:3], v[240:243]
	s_waitcnt lgkmcnt(11)
	v_mfma_f32_16x16x32_bf16 v[72:75], v[176:179], v[8:11], v[72:75]
	ds_read_b64_tr_b16 v[228:229], v142 offset:57344
	ds_read_b64_tr_b16 v[88:89], v136 offset:49152
	ds_read_b64_tr_b16 v[90:91], v137 offset:49152
	ds_read_b64_tr_b16 v[98:99], v137 offset:57344
	v_mfma_f32_16x16x32_bf16 v[84:87], v[184:187], v[12:15], v[72:75]
	v_mfma_f32_16x16x32_bf16 v[72:75], v[152:155], v[4:7], v[76:79]
	v_mfma_f32_16x16x32_bf16 v[72:75], v[180:183], v[8:11], v[72:75]
	v_mfma_f32_16x16x32_bf16 v[80:83], v[188:191], v[12:15], v[72:75]
	s_waitcnt lgkmcnt(11)
	s_nop 5
	v_mfma_f32_16x16x32_bf16 v[72:75], v[192:195], v[0:3], v[240:243]
	ds_read_b64_tr_b16 v[96:97], v136 offset:57344
	ds_read_b64_tr_b16 v[92:93], v139 offset:49152
	ds_read_b64_tr_b16 v[94:95], v145 offset:49152
	ds_read_b64_tr_b16 v[178:179], v145 offset:57344
	v_mfma_f32_16x16x32_bf16 v[72:75], v[200:203], v[4:7], v[72:75]
	s_waitcnt lgkmcnt(11)
	v_mfma_f32_16x16x32_bf16 v[72:75], v[208:211], v[8:11], v[72:75]
	ds_read_b64_tr_b16 v[176:177], v139 offset:57344
	ds_read_b64_tr_b16 v[184:185], v140 offset:49152
	ds_read_b64_tr_b16 v[186:187], v147 offset:49152
	ds_read_b64_tr_b16 v[154:155], v147 offset:57344
	v_mfma_f32_16x16x32_bf16 v[76:79], v[216:219], v[12:15], v[72:75]
	v_mfma_f32_16x16x32_bf16 v[72:75], v[196:199], v[0:3], v[240:243]
	v_mfma_f32_16x16x32_bf16 v[72:75], v[204:207], v[4:7], v[72:75]
	s_waitcnt lgkmcnt(10)
	v_mfma_f32_16x16x32_bf16 v[60:63], v[224:227], v[68:71], v[60:63]
	ds_read_b64_tr_b16 v[152:153], v140 offset:57344
	ds_read_b64_tr_b16 v[180:181], v148 offset:49152
	ds_read_b64_tr_b16 v[182:183], v149 offset:49152
	ds_read_b64_tr_b16 v[190:191], v149 offset:57344
	ds_read_b64_tr_b16 v[188:189], v148 offset:57344
	v_mfma_f32_16x16x32_bf16 v[60:63], v[228:231], v[64:67], v[60:63]
	s_waitcnt lgkmcnt(11)
	v_mfma_f32_16x16x32_bf16 v[52:55], v[88:91], v[68:71], v[52:55]
	ds_read_b64_tr_b16 v[192:193], v133 offset:49152
	ds_read_b64_tr_b16 v[194:195], v134 offset:49152
	ds_read_b64_tr_b16 v[202:203], v134 offset:57344
	ds_read_b64_tr_b16 v[200:201], v133 offset:57344
	v_mfma_f32_16x16x32_bf16 v[52:55], v[96:99], v[64:67], v[52:55]
	s_waitcnt lgkmcnt(11)
	v_mfma_f32_16x16x32_bf16 v[48:51], v[92:95], v[68:71], v[48:51]
	ds_read_b64_tr_b16 v[208:209], v135 offset:49152
	ds_read_b64_tr_b16 v[210:211], v138 offset:49152
	ds_read_b64_tr_b16 v[218:219], v138 offset:57344
	ds_read_b64_tr_b16 v[216:217], v135 offset:57344
	v_mfma_f32_16x16x32_bf16 v[48:51], v[176:179], v[64:67], v[48:51]
	s_waitcnt lgkmcnt(11)
	v_mfma_f32_16x16x32_bf16 v[56:59], v[184:187], v[68:71], v[56:59]
	ds_read_b64_tr_b16 v[196:197], v141 offset:49152
	ds_read_b64_tr_b16 v[198:199], v143 offset:49152
	ds_read_b64_tr_b16 v[206:207], v143 offset:57344
	ds_read_b64_tr_b16 v[204:205], v141 offset:57344
	v_mfma_f32_16x16x32_bf16 v[56:59], v[152:155], v[64:67], v[56:59]
	s_waitcnt lgkmcnt(11)
	v_mfma_f32_16x16x32_bf16 v[32:35], v[180:183], v[68:71], v[32:35]
	v_mfma_f32_16x16x32_bf16 v[32:35], v[188:191], v[64:67], v[32:35]
	s_waitcnt lgkmcnt(7)
	v_mfma_f32_16x16x32_bf16 v[36:39], v[192:195], v[68:71], v[36:39]
	v_mfma_f32_16x16x32_bf16 v[36:39], v[200:203], v[64:67], v[36:39]
	s_waitcnt lgkmcnt(3)
	v_mfma_f32_16x16x32_bf16 v[40:43], v[208:211], v[68:71], v[40:43]
	v_mfma_f32_16x16x32_bf16 v[40:43], v[216:219], v[64:67], v[40:43]
	v_mfma_f32_16x16x32_bf16 v[72:75], v[212:215], v[8:11], v[72:75]
	s_waitcnt lgkmcnt(0)
	v_mfma_f32_16x16x32_bf16 v[44:47], v[196:199], v[68:71], v[44:47]
	v_mfma_f32_16x16x32_bf16 v[72:75], v[220:223], v[12:15], v[72:75]
	v_mfma_f32_16x16x32_bf16 v[44:47], v[204:207], v[64:67], v[44:47]
	s_cbranch_vccnz .LBB0_1921
	v_add_u32_e32 v64, 0, v109
	s_waitcnt vmcnt(3)
	ds_write_b128 v100, v[16:19] offset:16384
	s_waitcnt vmcnt(2)
	ds_write_b128 v124, v[20:23] offset:16384
	s_waitcnt vmcnt(1)
	ds_write_b128 v64, v[24:27] offset:32768
	v_add_u32_e32 v64, 0, v112
	s_waitcnt vmcnt(0)
	ds_write_b128 v64, v[28:31] offset:32768

.LBB0_1927:
	ds_read_b128 v[168:171], v129 offset:16384
	ds_read_b128 v[172:175], v130 offset:16384
	ds_read_b128 v[176:179], v131 offset:16384
	ds_read_b128 v[180:183], v129 offset:17408
	ds_read_b128 v[184:187], v132 offset:16384
	ds_read_b128 v[188:191], v130 offset:17408
	ds_read_b128 v[192:195], v131 offset:17408
	ds_read_b128 v[196:199], v129 offset:24576
	ds_read_b128 v[200:203], v132 offset:17408
	ds_read_b128 v[204:207], v130 offset:24576
	ds_read_b128 v[208:211], v131 offset:24576
	ds_read_b128 v[212:215], v129 offset:25600
	ds_read_b128 v[216:219], v132 offset:24576
	ds_read_b128 v[220:223], v130 offset:25600
	ds_read_b128 v[224:227], v131 offset:25600
	v_sub_f32_e32 v64, v84, v96
	v_exp_f32_e32 v96, v64
	v_sub_f32_e32 v64, v85, v97
	v_exp_f32_e32 v97, v64
	v_sub_f32_e32 v64, v86, v98
	v_exp_f32_e32 v98, v64
	v_sub_f32_e32 v64, v87, v99
	v_exp_f32_e32 v99, v64
	v_sub_f32_e32 v64, v80, v92
	v_exp_f32_e32 v153, v64
	v_sub_f32_e32 v64, v81, v93
	v_exp_f32_e32 v154, v64
	v_sub_f32_e32 v64, v82, v94
	v_exp_f32_e32 v155, v64
	v_sub_f32_e32 v64, v83, v95
	s_waitcnt lgkmcnt(11)
	v_mfma_f32_16x16x32_bf16 v[84:87], v[168:171], v[0:3], v[240:243]
	ds_read_b128 v[228:231], v132 offset:25600
	ds_read_b64_tr_b16 v[168:169], v142 offset:32768
	ds_read_b64_tr_b16 v[170:171], v146 offset:32768
	v_exp_f32_e32 v156, v64
	v_sub_f32_e32 v64, v76, v88
	v_exp_f32_e32 v157, v64
	v_mfma_f32_16x16x32_bf16 v[92:95], v[180:183], v[0:3], v[240:243]
	ds_read_b64_tr_b16 v[182:183], v146 offset:40960
	v_sub_f32_e32 v64, v77, v89
	v_sub_f32_e32 v70, v73, v67
	v_mfma_f32_16x16x32_bf16 v[84:87], v[172:175], v[4:7], v[84:87]
	v_exp_f32_e32 v158, v64
	v_sub_f32_e32 v64, v78, v90
	v_exp_f32_e32 v159, v64
	v_sub_f32_e32 v64, v79, v91
	s_waitcnt lgkmcnt(10)
	v_mfma_f32_16x16x32_bf16 v[88:91], v[188:191], v[4:7], v[92:95]
	ds_read_b64_tr_b16 v[180:181], v142 offset:40960
	ds_read_b64_tr_b16 v[172:173], v136 offset:32768
	ds_read_b64_tr_b16 v[174:175], v137 offset:32768
	ds_read_b64_tr_b16 v[190:191], v137 offset:40960
	ds_read_b64_tr_b16 v[188:189], v136 offset:40960
	v_exp_f32_e32 v160, v64
	v_mfma_f32_16x16x32_bf16 v[80:83], v[176:179], v[8:11], v[84:87]
	v_sub_f32_e32 v64, v72, v66
	v_exp_f32_e32 v161, v64
	v_mfma_f32_16x16x32_bf16 v[76:79], v[192:195], v[8:11], v[88:91]
	v_sub_f32_e32 v68, v74, v68
	s_and_b64 vcc, exec, s[6:7]
	v_mfma_f32_16x16x32_bf16 v[92:95], v[196:199], v[0:3], v[240:243]
	v_mfma_f32_16x16x32_bf16 v[80:83], v[184:187], v[12:15], v[80:83]
	v_exp_f32_e32 v162, v70
	v_exp_f32_e32 v163, v68
	v_mfma_f32_16x16x32_bf16 v[76:79], v[200:203], v[12:15], v[76:79]
	s_waitcnt lgkmcnt(11)
	v_mfma_f32_16x16x32_bf16 v[88:91], v[204:207], v[4:7], v[92:95]
	ds_read_b64_tr_b16 v[176:177], v139 offset:32768
	ds_read_b64_tr_b16 v[178:179], v145 offset:32768
	ds_read_b64_tr_b16 v[194:195], v145 offset:40960
	ds_read_b64_tr_b16 v[192:193], v139 offset:40960
	v_sub_f32_e32 v68, v75, v69
	v_mfma_f32_16x16x32_bf16 v[84:87], v[208:211], v[8:11], v[88:91]
	v_cvt_pk_bf16_f32 v92, v96, v97
	v_cvt_pk_bf16_f32 v93, v98, v99
	v_cvt_pk_bf16_f32 v94, v153, v154
	v_mfma_f32_16x16x32_bf16 v[64:67], v[216:219], v[12:15], v[84:87]
	v_cvt_pk_bf16_f32 v95, v155, v156
	v_mfma_f32_16x16x32_bf16 v[84:87], v[212:215], v[0:3], v[240:243]
	v_exp_f32_e32 v164, v68
	s_waitcnt lgkmcnt(11)
	v_mfma_f32_16x16x32_bf16 v[84:87], v[220:223], v[4:7], v[84:87]
	ds_read_b64_tr_b16 v[196:197], v140 offset:32768
	ds_read_b64_tr_b16 v[198:199], v147 offset:32768
	ds_read_b64_tr_b16 v[186:187], v147 offset:40960
	ds_read_b64_tr_b16 v[184:185], v140 offset:40960
	v_mfma_f32_16x16x32_bf16 v[68:71], v[224:227], v[8:11], v[84:87]
	s_nop 2
	v_cvt_pk_bf16_f32 v84, v157, v158
	v_mfma_f32_16x16x32_bf16 v[68:71], v[228:231], v[12:15], v[68:71]
	v_cvt_pk_bf16_f32 v85, v159, v160
	v_cvt_pk_bf16_f32 v86, v161, v162
	s_waitcnt lgkmcnt(11)
	v_mfma_f32_16x16x32_bf16 v[60:63], v[168:171], v[92:95], v[60:63]
	ds_read_b64_tr_b16 v[200:201], v148 offset:32768
	ds_read_b64_tr_b16 v[202:203], v149 offset:32768
	ds_read_b64_tr_b16 v[206:207], v149 offset:40960
	ds_read_b64_tr_b16 v[204:205], v148 offset:40960
	v_cvt_pk_bf16_f32 v87, v163, v164
	s_nop 1
	v_mfma_f32_16x16x32_bf16 v[60:63], v[180:183], v[84:87], v[60:63]
	s_waitcnt lgkmcnt(11)
	v_mfma_f32_16x16x32_bf16 v[52:55], v[172:175], v[92:95], v[52:55]
	ds_read_b64_tr_b16 v[208:209], v133 offset:32768
	ds_read_b64_tr_b16 v[210:211], v134 offset:32768
	ds_read_b64_tr_b16 v[218:219], v134 offset:40960
	ds_read_b64_tr_b16 v[216:217], v133 offset:40960
	v_mfma_f32_16x16x32_bf16 v[52:55], v[188:191], v[84:87], v[52:55]
	s_waitcnt lgkmcnt(11)
	v_mfma_f32_16x16x32_bf16 v[48:51], v[176:179], v[92:95], v[48:51]
	ds_read_b64_tr_b16 v[212:213], v135 offset:32768
	ds_read_b64_tr_b16 v[214:215], v138 offset:32768
	ds_read_b64_tr_b16 v[222:223], v138 offset:40960
	ds_read_b64_tr_b16 v[220:221], v135 offset:40960
	v_mfma_f32_16x16x32_bf16 v[48:51], v[192:195], v[84:87], v[48:51]
	s_waitcnt lgkmcnt(11)
	v_mfma_f32_16x16x32_bf16 v[56:59], v[196:199], v[92:95], v[56:59]
	ds_read_b64_tr_b16 v[224:225], v141 offset:32768
	ds_read_b64_tr_b16 v[226:227], v143 offset:32768
	ds_read_b64_tr_b16 v[230:231], v143 offset:40960
	ds_read_b64_tr_b16 v[228:229], v141 offset:40960
	v_mfma_f32_16x16x32_bf16 v[56:59], v[184:187], v[84:87], v[56:59]
	s_waitcnt lgkmcnt(11)
	v_mfma_f32_16x16x32_bf16 v[32:35], v[200:203], v[92:95], v[32:35]
	v_mfma_f32_16x16x32_bf16 v[32:35], v[204:207], v[84:87], v[32:35]
	s_waitcnt lgkmcnt(7)
	v_mfma_f32_16x16x32_bf16 v[36:39], v[208:211], v[92:95], v[36:39]
	v_mfma_f32_16x16x32_bf16 v[36:39], v[216:219], v[84:87], v[36:39]
	s_waitcnt lgkmcnt(3)
	v_mfma_f32_16x16x32_bf16 v[40:43], v[212:215], v[92:95], v[40:43]
	v_mfma_f32_16x16x32_bf16 v[40:43], v[220:223], v[84:87], v[40:43]
	s_waitcnt lgkmcnt(0)
	v_mfma_f32_16x16x32_bf16 v[44:47], v[224:227], v[92:95], v[44:47]
	v_mfma_f32_16x16x32_bf16 v[44:47], v[228:231], v[84:87], v[44:47]
	s_cbranch_vccnz .LBB0_1929
	v_add_u32_e32 v72, 0, v109
	s_waitcnt vmcnt(3)
	ds_write_b128 v100, v[16:19]
	s_waitcnt vmcnt(2)
	ds_write_b128 v124, v[20:23]
	s_waitcnt vmcnt(1)
	ds_write_b128 v72, v[24:27] offset:49152
	v_add_u32_e32 v72, 0, v112
	s_waitcnt vmcnt(0)
	ds_write_b128 v72, v[28:31] offset:49152

.LBB0_1933:
	v_add_f32_e32 v96, v150, v96
	v_add_f32_e32 v96, v97, v96
	v_add_f32_e32 v96, v98, v96
	v_add_f32_e32 v96, v99, v96
	v_add_f32_e32 v96, v153, v96
	v_add_f32_e32 v96, v154, v96
	v_add_f32_e32 v96, v155, v96
	v_add_f32_e32 v96, v156, v96
	v_add_f32_e32 v96, v157, v96
	v_add_f32_e32 v96, v158, v96
	v_add_f32_e32 v96, v159, v96
	s_waitcnt lgkmcnt(3)
	v_add_f32_e32 v96, v160, v96
	v_sub_f32_e32 v80, v80, v92
	v_add_f32_e32 v96, v161, v96
	v_exp_f32_e32 v80, v80
	v_sub_f32_e32 v81, v81, v93
	v_add_f32_e32 v96, v162, v96
	v_exp_f32_e32 v81, v81
	v_sub_f32_e32 v82, v82, v94
	v_add_f32_e32 v96, v163, v96
	v_exp_f32_e32 v82, v82
	v_sub_f32_e32 v83, v83, v95
	s_waitcnt lgkmcnt(2)
	v_add_f32_e32 v96, v164, v96
	v_exp_f32_e32 v83, v83
	v_sub_f32_e32 v76, v76, v88
	v_add_f32_e32 v92, v96, v80
	v_exp_f32_e32 v76, v76
	v_sub_f32_e32 v77, v77, v89
	v_add_f32_e32 v92, v81, v92
	v_exp_f32_e32 v77, v77
	v_sub_f32_e32 v78, v78, v90
	v_add_f32_e32 v92, v82, v92
	v_exp_f32_e32 v78, v78
	v_sub_f32_e32 v79, v79, v91
	s_waitcnt lgkmcnt(1)
	v_add_f32_e32 v92, v83, v92
	v_exp_f32_e32 v79, v79
	v_sub_f32_e32 v64, v64, v84
	s_waitcnt lgkmcnt(0)
	v_add_f32_e32 v88, v76, v92
	v_exp_f32_e32 v64, v64
	v_sub_f32_e32 v65, v65, v85
	v_sub_f32_e32 v68, v68, v72
	v_add_f32_e32 v88, v77, v88
	v_exp_f32_e32 v65, v65
	v_sub_f32_e32 v66, v66, v86
	v_exp_f32_e32 v72, v68
	v_add_f32_e32 v88, v78, v88
	v_exp_f32_e32 v66, v66
	v_sub_f32_e32 v67, v67, v87
	v_sub_f32_e32 v68, v69, v73
	v_add_f32_e32 v88, v79, v88
	v_exp_f32_e32 v67, v67
	v_exp_f32_e32 v73, v68
	v_add_f32_e32 v84, v64, v88
	v_sub_f32_e32 v68, v70, v74
	v_add_f32_e32 v84, v65, v84
	v_exp_f32_e32 v74, v68
	v_add_f32_e32 v84, v66, v84
	v_sub_f32_e32 v68, v71, v75
	v_add_f32_e32 v84, v67, v84
	v_exp_f32_e32 v75, v68
	v_add_f32_e32 v68, v72, v84
	v_add_f32_e32 v68, v73, v68
	v_add_f32_e32 v68, v74, v68
	v_add_f32_e32 v150, v75, v68
	v_cvt_pk_bf16_f32 v68, v80, v81
	v_cvt_pk_bf16_f32 v69, v82, v83
	v_cvt_pk_bf16_f32 v70, v76, v77
	v_cvt_pk_bf16_f32 v71, v78, v79
	v_cvt_pk_bf16_f32 v64, v64, v65
	v_cvt_pk_bf16_f32 v65, v66, v67
	v_cvt_pk_bf16_f32 v66, v72, v73
	v_cvt_pk_bf16_f32 v67, v74, v75
	s_waitcnt lgkmcnt(0)
	s_barrier
	s_add_i32 s13, s12, 2
	s_add_i32 s11, s11, -2
	s_add_i32 s10, s10, 0xffd10000
	s_addk_i32 s5, 0xfe00
	s_cmp_ge_u32 s12, s4
	s_cbranch_scc1 .LBB0_1935
	s_mov_b32 s12, s13
	s_and_b64 vcc, exec, s[8:9]
	s_cbranch_vccz .LBB0_1918
	s_branch .LBB0_1919

.LBB0_1937:
	ds_read_b64_tr_b16 v[0:1], v142 offset:49152
	ds_read_b64_tr_b16 v[2:3], v146 offset:49152
	ds_read_b64_tr_b16 v[6:7], v146 offset:57344
	ds_read_b64_tr_b16 v[4:5], v142 offset:57344
	ds_read_b64_tr_b16 v[8:9], v136 offset:49152
	ds_read_b64_tr_b16 v[10:11], v137 offset:49152
	ds_read_b64_tr_b16 v[14:15], v137 offset:57344
	ds_read_b64_tr_b16 v[12:13], v136 offset:57344
	s_add_u32 s10, s46, s0
	s_waitcnt lgkmcnt(6)
	v_mfma_f32_16x16x32_bf16 v[0:3], v[0:3], v[68:71], v[60:63]
	s_addc_u32 s11, s47, 0
	s_waitcnt lgkmcnt(2)
	v_mfma_f32_16x16x32_bf16 v[8:11], v[8:11], v[68:71], v[52:55]
	v_mfma_f32_16x16x32_bf16 v[0:3], v[4:7], v[64:67], v[0:3]
	ds_read_b64_tr_b16 v[4:5], v139 offset:49152
	ds_read_b64_tr_b16 v[6:7], v145 offset:49152
	s_waitcnt lgkmcnt(2)
	v_mfma_f32_16x16x32_bf16 v[8:11], v[12:15], v[64:67], v[8:11]
	ds_read_b64_tr_b16 v[14:15], v145 offset:57344
	ds_read_b64_tr_b16 v[12:13], v139 offset:57344
	s_waitcnt vmcnt(3)
	ds_read_b64_tr_b16 v[16:17], v140 offset:49152
	ds_read_b64_tr_b16 v[18:19], v147 offset:49152
	s_waitcnt lgkmcnt(4)
	v_mfma_f32_16x16x32_bf16 v[4:7], v[4:7], v[68:71], v[48:51]
	s_waitcnt lgkmcnt(2)
	v_mfma_f32_16x16x32_bf16 v[4:7], v[12:15], v[64:67], v[4:7]
	ds_read_b64_tr_b16 v[14:15], v147 offset:57344
	ds_read_b64_tr_b16 v[12:13], v140 offset:57344
	s_waitcnt vmcnt(2)
	ds_read_b64_tr_b16 v[20:21], v148 offset:49152
	ds_read_b64_tr_b16 v[22:23], v149 offset:49152
	s_waitcnt vmcnt(1)
	ds_read_b64_tr_b16 v[26:27], v149 offset:57344
	ds_read_b64_tr_b16 v[24:25], v148 offset:57344
	v_lshlrev_b32_e32 v48, 2, v126
	s_waitcnt lgkmcnt(6)
	v_mfma_f32_16x16x32_bf16 v[16:19], v[16:19], v[68:71], v[56:59]
	s_waitcnt vmcnt(0)
	v_xor_b32_e32 v28, 64, v48
	v_mov_b32_e32 v126, v108
	s_waitcnt lgkmcnt(2)
	v_mfma_f32_16x16x32_bf16 v[20:23], v[20:23], v[68:71], v[32:35]
	s_nop 2
	ds_bpermute_b32 v32, v28, v150
	v_mfma_f32_16x16x32_bf16 v[12:15], v[12:15], v[64:67], v[16:19]
	s_nop 2
	ds_read_b64_tr_b16 v[16:17], v133 offset:49152
	ds_read_b64_tr_b16 v[18:19], v134 offset:49152
	ds_read_b64_tr_b16 v[30:31], v134 offset:57344
	ds_read_b64_tr_b16 v[28:29], v133 offset:57344
	s_waitcnt lgkmcnt(4)
	v_add_f32_e32 v49, v150, v32
	v_xor_b32_e32 v32, 0x80, v48
	v_mfma_f32_16x16x32_bf16 v[20:23], v[24:27], v[64:67], v[20:23]
	ds_read_b64_tr_b16 v[24:25], v135 offset:49152
	ds_read_b64_tr_b16 v[26:27], v138 offset:49152
	s_waitcnt lgkmcnt(4)
	v_mfma_f32_16x16x32_bf16 v[16:19], v[16:19], v[68:71], v[36:39]
	s_nop 2
	ds_bpermute_b32 v36, v32, v49
	ds_read_b64_tr_b16 v[34:35], v138 offset:57344
	ds_read_b64_tr_b16 v[32:33], v135 offset:57344
	s_waitcnt lgkmcnt(5)
	v_mfma_f32_16x16x32_bf16 v[16:19], v[28:31], v[64:67], v[16:19]
	ds_read_b64_tr_b16 v[28:29], v141 offset:49152
	ds_read_b64_tr_b16 v[30:31], v143 offset:49152
	s_waitcnt lgkmcnt(4)
	v_add_f32_e32 v36, v49, v36
	v_mfma_f32_16x16x32_bf16 v[24:27], v[24:27], v[68:71], v[40:43]
	v_div_scale_f32 v37, s[4:5], v36, v36, 1.0
	v_rcp_f32_e32 v38, v37
	s_waitcnt lgkmcnt(2)
	v_mfma_f32_16x16x32_bf16 v[24:27], v[32:35], v[64:67], v[24:27]
	ds_read_b64_tr_b16 v[34:35], v143 offset:57344
	ds_read_b64_tr_b16 v[32:33], v141 offset:57344
	s_lshl_b32 s4, s1, 7
	v_fma_f32 v39, -v37, v38, 1.0
	s_waitcnt lgkmcnt(2)
	v_mfma_f32_16x16x32_bf16 v[28:31], v[28:31], v[68:71], v[44:47]
	v_fmac_f32_e32 v38, v39, v38
	v_div_scale_f32 v39, vcc, 1.0, v36, 1.0
	v_mul_f32_e32 v40, v39, v38
	s_waitcnt lgkmcnt(0)
	v_mfma_f32_16x16x32_bf16 v[28:31], v[32:35], v[64:67], v[28:31]
	v_fma_f32 v32, -v37, v40, v39
	v_fmac_f32_e32 v40, v32, v38
	v_fma_f32 v32, -v37, v40, v39
	v_div_fmas_f32 v32, v32, v38, v40
	v_div_fixup_f32 v32, v32, v36, 1.0
	v_lshl_add_u32 v33, v125, 12, v128
	v_pk_mul_f32 v[0:1], v[0:1], v[32:33] op_sel_hi:[1,0]
	v_pk_mul_f32 v[2:3], v[2:3], v[32:33] op_sel_hi:[1,0]
	v_cvt_pk_bf16_f32 v0, v0, v1
	v_cvt_pk_bf16_f32 v1, v2, v3
	global_store_dwordx2 v33, v[0:1], s[10:11]
	v_pk_mul_f32 v[0:1], v[8:9], v[32:33] op_sel_hi:[1,0]
	v_pk_mul_f32 v[2:3], v[10:11], v[32:33] op_sel_hi:[1,0]
	v_cvt_pk_bf16_f32 v0, v0, v1
	v_cvt_pk_bf16_f32 v1, v2, v3
	global_store_dwordx2 v33, v[0:1], s[10:11] offset:32
	v_pk_mul_f32 v[0:1], v[4:5], v[32:33] op_sel_hi:[1,0]
	v_pk_mul_f32 v[2:3], v[6:7], v[32:33] op_sel_hi:[1,0]
	v_cvt_pk_bf16_f32 v0, v0, v1
	v_cvt_pk_bf16_f32 v1, v2, v3
	global_store_dwordx2 v33, v[0:1], s[10:11] offset:64
	v_pk_mul_f32 v[0:1], v[12:13], v[32:33] op_sel_hi:[1,0]
	v_pk_mul_f32 v[2:3], v[14:15], v[32:33] op_sel_hi:[1,0]
	v_cvt_pk_bf16_f32 v0, v0, v1
	v_cvt_pk_bf16_f32 v1, v2, v3
	global_store_dwordx2 v33, v[0:1], s[10:11] offset:96
	v_pk_mul_f32 v[0:1], v[20:21], v[32:33] op_sel_hi:[1,0]
	v_pk_mul_f32 v[2:3], v[22:23], v[32:33] op_sel_hi:[1,0]
	v_cvt_pk_bf16_f32 v0, v0, v1
	v_cvt_pk_bf16_f32 v1, v2, v3
	global_store_dwordx2 v33, v[0:1], s[10:11] offset:128
	v_pk_mul_f32 v[0:1], v[16:17], v[32:33] op_sel_hi:[1,0]
	v_pk_mul_f32 v[2:3], v[18:19], v[32:33] op_sel_hi:[1,0]
	v_cvt_pk_bf16_f32 v0, v0, v1
	v_cvt_pk_bf16_f32 v1, v2, v3
	global_store_dwordx2 v33, v[0:1], s[10:11] offset:160
	v_pk_mul_f32 v[0:1], v[24:25], v[32:33] op_sel_hi:[1,0]
	v_pk_mul_f32 v[2:3], v[26:27], v[32:33] op_sel_hi:[1,0]
	v_cvt_pk_bf16_f32 v0, v0, v1
	v_cvt_pk_bf16_f32 v1, v2, v3
	global_store_dwordx2 v33, v[0:1], s[10:11] offset:192
	v_pk_mul_f32 v[0:1], v[28:29], v[32:33] op_sel_hi:[1,0]
	v_pk_mul_f32 v[2:3], v[30:31], v[32:33] op_sel_hi:[1,0]
	v_cvt_pk_bf16_f32 v0, v0, v1
	v_cvt_pk_bf16_f32 v1, v2, v3
	global_store_dwordx2 v33, v[0:1], s[10:11] offset:224
	s_add_i32 s0, s4, s57
	v_and_b32_e32 v32, 15, v126
	v_or_b32_e32 v125, s0, v32
	v_and_b32_e32 v0, -16, v126
	v_mad_u64_u32 v[8:9], s[12:13], v125, s59, v[0:1]
	v_add_u32_e32 v4, 64, v8
	v_add_u32_e32 v9, 0x80, v8
	v_add_u32_e32 v12, 0xc0, v8
	global_load_dwordx4 v[0:3], v8, s[44:45] offset:3072
	s_nop 0
	global_load_dwordx4 v[4:7], v4, s[44:45] offset:3072
	s_nop 0
	global_load_dwordx4 v[8:11], v9, s[44:45] offset:3072
	s_nop 0
	global_load_dwordx4 v[12:15], v12, s[44:45] offset:3072
	v_lshl_add_u32 v16, v125, 2, 0
	v_add_u32_e32 v16, 0x10000, v16
	ds_read_b32 v128, v16
	s_lshl_b32 s0, s1, 1
	s_or_b32 s5, s0, 1
	s_waitcnt lgkmcnt(0)
	v_mov_b32_e32 v240, v128
	v_mov_b32_e32 v241, v128
	v_mov_b32_e32 v242, v128
	v_mov_b32_e32 v243, v128
	s_waitcnt lgkmcnt(0)
	s_barrier
	s_mul_i32 s12, s5, 0x178000
	s_add_u32 s14, s48, s12
	s_addc_u32 s15, s49, 0
	v_lshl_add_u64 v[16:17], s[14:15], 0, v[104:105]
	v_add_co_u32_e32 v20, vcc, 0xbc000, v16
	s_nop 1
	v_addc_co_u32_e32 v21, vcc, 0, v17, vcc
	global_load_dwordx4 v[16:19], v[16:17], off
	s_nop 0
	global_load_dwordx4 v[20:23], v[20:21], off
	s_waitcnt vmcnt(1)
	ds_write_b128 v100, v[16:19]
	s_waitcnt vmcnt(0)
	ds_write_b128 v124, v[20:23]
	s_waitcnt lgkmcnt(0)
	s_waitcnt lgkmcnt(0)
	s_barrier
	s_and_b64 vcc, exec, s[6:7]
	s_cbranch_vccnz .LBB0_1939
	s_mul_i32 s13, s1, 0x2f0000
	s_add_u32 s14, s48, s13
	s_addc_u32 s15, s49, 0
	v_lshl_add_u64 v[16:17], s[14:15], 0, v[104:105]
	s_add_u32 s14, s68, s12
	v_add_co_u32_e32 v20, vcc, 0xbc000, v16
	s_addc_u32 s15, s69, 0
	s_nop 0
	v_addc_co_u32_e32 v21, vcc, 0, v17, vcc
	v_lshl_add_u64 v[24:25], s[14:15], 0, v[104:105]
	v_add_co_u32_e32 v28, vcc, 0xbc000, v24
	global_load_dwordx4 v[16:19], v[16:17], off
	s_nop 0
	global_load_dwordx4 v[20:23], v[20:21], off
	v_addc_co_u32_e32 v29, vcc, 0, v25, vcc
	global_load_dwordx4 v[24:27], v[24:25], off
	s_nop 0
	global_load_dwordx4 v[28:31], v[28:29], off
	s_waitcnt lgkmcnt(0)

.LBB0_1949:
	v_sub_f32_e32 v44, v44, v60
	v_exp_f32_e32 v44, v44
	v_sub_f32_e32 v45, v45, v61
	v_cmp_le_i32_e32 vcc, v64, v125
	v_exp_f32_e32 v45, v45
	v_bfe_u32 v84, v126, 1, 1
	v_cndmask_b32_e32 v97, 0, v44, vcc
	v_sub_f32_e32 v44, v46, v62
	v_exp_f32_e32 v44, v44
	v_cmp_lt_i32_e32 vcc, v64, v125
	v_sub_f32_e32 v46, v47, v63
	v_cndmask_b32_e32 v98, 0, v45, vcc
	v_or_b32_e32 v45, 2, v64
	v_cmp_le_i32_e32 vcc, v45, v125
	v_exp_f32_e32 v46, v46
	v_cndmask_b32_e32 v99, 0, v44, vcc
	v_or_b32_e32 v44, 3, v64
	v_cmp_le_i32_e32 vcc, v44, v125
	v_sub_f32_e32 v40, v40, v56
	v_exp_f32_e32 v40, v40
	v_or_b32_e32 v44, 4, v64
	v_sub_f32_e32 v41, v41, v57
	v_cndmask_b32_e32 v150, 0, v46, vcc
	v_exp_f32_e32 v41, v41
	v_cmp_le_i32_e32 vcc, v44, v125
	v_cvt_pk_bf16_f32 v44, v97, v98
	v_cvt_pk_bf16_f32 v45, v99, v150
	v_cndmask_b32_e32 v151, 0, v40, vcc
	v_or_b32_e32 v40, 5, v64
	v_cmp_le_i32_e32 vcc, v40, v125
	v_sub_f32_e32 v40, v42, v58
	v_cndmask_b32_e32 v152, 0, v41, vcc
	v_exp_f32_e32 v40, v40
	v_or_b32_e32 v41, 6, v64
	v_sub_f32_e32 v42, v43, v59
	v_cmp_le_i32_e32 vcc, v41, v125
	v_exp_f32_e32 v42, v42
	v_sub_f32_e32 v36, v36, v52
	v_exp_f32_e32 v36, v36
	v_cndmask_b32_e32 v153, 0, v40, vcc
	v_or_b32_e32 v40, 7, v64
	v_cmp_le_i32_e32 vcc, v40, v125
	v_add_u32_e32 v40, 32, v64
	v_cndmask_b32_e32 v154, 0, v42, vcc
	v_cmp_le_i32_e32 vcc, v40, v125
	v_sub_f32_e32 v37, v37, v53
	v_exp_f32_e32 v37, v37
	v_cndmask_b32_e32 v155, 0, v36, vcc
	v_add_u32_e32 v36, 33, v64
	v_cmp_le_i32_e32 vcc, v36, v125
	v_sub_f32_e32 v36, v38, v54
	v_exp_f32_e32 v36, v36
	v_cndmask_b32_e32 v156, 0, v37, vcc
	v_add_u32_e32 v37, 34, v64
	v_cmp_le_i32_e32 vcc, v37, v125
	v_sub_f32_e32 v38, v39, v55
	v_cndmask_b32_e32 v157, 0, v36, vcc
	v_add_u32_e32 v36, 35, v64
	v_cmp_le_i32_e32 vcc, v36, v125
	v_exp_f32_e32 v38, v38
	v_sub_f32_e32 v32, v32, v48
	v_exp_f32_e32 v32, v32
	v_add_u32_e32 v36, 36, v64
	v_cndmask_b32_e32 v158, 0, v38, vcc
	v_cmp_le_i32_e32 vcc, v36, v125
	v_sub_f32_e32 v33, v33, v49
	v_exp_f32_e32 v33, v33
	v_cndmask_b32_e32 v159, 0, v32, vcc
	v_add_u32_e32 v32, 37, v64
	v_cmp_le_i32_e32 vcc, v32, v125
	v_sub_f32_e32 v32, v34, v50
	v_exp_f32_e32 v32, v32
	v_sub_f32_e32 v34, v35, v51
	v_cndmask_b32_e32 v160, 0, v33, vcc
	v_add_u32_e32 v33, 38, v64
	v_exp_f32_e32 v34, v34
	v_cmp_le_i32_e32 vcc, v33, v125
	v_lshrrev_b32_e32 v33, 1, v126
	v_and_b32_e32 v33, 0x7ffffff8, v33
	v_cndmask_b32_e32 v161, 0, v32, vcc
	v_add_u32_e32 v32, 39, v64
	v_cmp_le_i32_e32 vcc, v32, v125
	v_bfe_u32 v32, v126, 2, 2
	v_lshlrev_b32_e32 v85, 2, v32
	v_cndmask_b32_e32 v162, 0, v34, vcc
	v_lshlrev_b32_e32 v34, 3, v126
	v_and_b32_e32 v92, 8, v34
	v_or_b32_e32 v34, v33, v32
	v_or_b32_e32 v33, 4, v33
	v_or_b32_e32 v32, v33, v32
	v_bfe_u32 v88, v33, 2, 2
	v_lshlrev_b32_e32 v86, 8, v34
	v_lshrrev_b32_e32 v34, 3, v126
	v_lshlrev_b32_e32 v93, 8, v32
	v_bitop3_b32 v32, v88, v84, v85 bitop3:0x36
	v_and_b32_e32 v87, 2, v34
	v_lshlrev_b32_e32 v32, 4, v32
	v_or_b32_e32 v34, v85, v87
	v_or3_b32 v61, v32, v93, v92
	v_or_b32_e32 v32, 2, v84
	v_or_b32_e32 v34, v34, v84
	v_bitop3_b32 v33, v85, v32, v87 bitop3:0x36
	v_lshlrev_b32_e32 v34, 4, v34
	v_lshlrev_b32_e32 v33, 4, v33
	v_or3_b32 v60, v34, v86, v92
	v_or3_b32 v62, v33, v86, v92
	v_bitop3_b32 v36, v88, v32, v85 bitop3:0x36
	ds_read_b128 v[32:35], v129 offset:16384
	v_lshlrev_b32_e32 v36, 4, v36
	v_or3_b32 v63, v36, v93, v92
	ds_read_b128 v[36:39], v130 offset:16384
	s_waitcnt lgkmcnt(1)
	v_mfma_f32_16x16x32_bf16 v[32:35], v[32:35], v[0:3], v[240:243]
	v_or_b32_e32 v64, 4, v84
	v_bitop3_b32 v40, v85, v64, v87 bitop3:0x36
	v_lshlrev_b32_e32 v52, 4, v40
	ds_read_b128 v[40:43], v131 offset:16384
	ds_read_b128 v[48:51], v129 offset:17408
	s_waitcnt lgkmcnt(2)
	v_mfma_f32_16x16x32_bf16 v[32:35], v[36:39], v[4:7], v[32:35]
	v_or3_b32 v89, v52, v86, v92
	ds_read_b128 v[52:55], v132 offset:16384
	ds_read_b128 v[56:59], v130 offset:17408
	v_bitop3_b32 v36, v88, v64, v85 bitop3:0x36
	s_waitcnt lgkmcnt(3)
	v_mfma_f32_16x16x32_bf16 v[32:35], v[40:43], v[8:11], v[32:35]
	v_lshlrev_b32_e32 v64, 4, v36
	v_or3_b32 v90, v64, v93, v92
	v_or_b32_e32 v64, 6, v84
	s_waitcnt lgkmcnt(1)
	v_mfma_f32_16x16x32_bf16 v[76:79], v[52:55], v[12:15], v[32:35]
	ds_read_b128 v[36:39], v131 offset:17408
	ds_read_b128 v[40:43], v132 offset:17408
	v_or_b32_e32 v52, 8, v84
	v_bitop3_b32 v32, v85, v64, v87 bitop3:0x36
	v_lshlrev_b32_e32 v32, 4, v32
	v_or3_b32 v91, v32, v86, v92
	v_mfma_f32_16x16x32_bf16 v[32:35], v[48:51], v[0:3], v[240:243]
	v_bitop3_b32 v48, v88, v64, v85 bitop3:0x36
	v_lshlrev_b32_e32 v48, 4, v48
	v_or3_b32 v94, v48, v93, v92
	s_waitcnt lgkmcnt(2)
	v_mfma_f32_16x16x32_bf16 v[32:35], v[56:59], v[4:7], v[32:35]
	ds_read_b128 v[48:51], v129 offset:24576
	v_bitop3_b32 v53, v85, v52, v87 bitop3:0x36
	v_bitop3_b32 v52, v88, v52, v85 bitop3:0x36
	s_waitcnt lgkmcnt(2)
	v_mfma_f32_16x16x32_bf16 v[32:35], v[36:39], v[8:11], v[32:35]
	v_lshlrev_b32_e32 v36, 4, v53
	v_or3_b32 v95, v36, v86, v92
	ds_read_b128 v[36:39], v130 offset:24576
	s_waitcnt lgkmcnt(1)
	v_mfma_f32_16x16x32_bf16 v[48:51], v[48:51], v[0:3], v[240:243]
	v_lshlrev_b32_e32 v64, 4, v52
	v_or3_b32 v133, v64, v93, v92
	v_or_b32_e32 v64, 10, v84
	v_mfma_f32_16x16x32_bf16 v[72:75], v[40:43], v[12:15], v[32:35]
	s_nop 2
	ds_read_b128 v[32:35], v131 offset:24576
	ds_read_b128 v[40:43], v129 offset:25600
	ds_read_b128 v[52:55], v132 offset:24576
	ds_read_b128 v[56:59], v130 offset:25600
	v_add_u32_e32 v146, 0, v60
	s_waitcnt lgkmcnt(4)
	v_mfma_f32_16x16x32_bf16 v[36:39], v[36:39], v[4:7], v[48:51]
	v_add_u32_e32 v148, 0, v61
	v_cvt_pk_bf16_f32 v46, v151, v152
	v_cvt_pk_bf16_f32 v47, v153, v154
	s_waitcnt lgkmcnt(3)
	v_mfma_f32_16x16x32_bf16 v[32:35], v[32:35], v[8:11], v[36:39]
	ds_read_b128 v[48:51], v131 offset:25600
	v_add_u32_e32 v139, 0, v62
	v_add_u32_e32 v142, 0, v63
	s_waitcnt lgkmcnt(2)
	v_mfma_f32_16x16x32_bf16 v[68:71], v[52:55], v[12:15], v[32:35]
	v_bitop3_b32 v36, v85, v64, v87 bitop3:0x36
	v_lshlrev_b32_e32 v65, 4, v36
	ds_read_b128 v[36:39], v132 offset:25600
	v_bitop3_b32 v32, v88, v64, v85 bitop3:0x36
	v_lshlrev_b32_e32 v52, 4, v32
	v_mfma_f32_16x16x32_bf16 v[32:35], v[40:43], v[0:3], v[240:243]
	v_or_b32_e32 v40, 12, v84
	v_bitop3_b32 v41, v85, v40, v87 bitop3:0x36
	v_lshlrev_b32_e32 v41, 4, v41
	s_waitcnt lgkmcnt(2)
	v_mfma_f32_16x16x32_bf16 v[32:35], v[56:59], v[4:7], v[32:35]
	v_or3_b32 v135, v52, v93, v92
	v_or3_b32 v136, v41, v86, v92
	v_bitop3_b32 v52, v88, v40, v85 bitop3:0x36
	s_waitcnt lgkmcnt(1)
	v_mfma_f32_16x16x32_bf16 v[32:35], v[48:51], v[8:11], v[32:35]
	ds_read_b64_tr_b16 v[40:41], v146 offset:32768
	ds_read_b64_tr_b16 v[42:43], v148 offset:32768
	v_or3_b32 v134, v65, v86, v92
	v_cvt_pk_bf16_f32 v80, v155, v156
	s_waitcnt lgkmcnt(2)
	v_mfma_f32_16x16x32_bf16 v[64:67], v[36:39], v[12:15], v[32:35]
	s_nop 2
	ds_read_b64_tr_b16 v[34:35], v148 offset:40960
	ds_read_b64_tr_b16 v[32:33], v146 offset:40960
	ds_read_b64_tr_b16 v[36:37], v139 offset:32768
	ds_read_b64_tr_b16 v[38:39], v142 offset:32768
	v_cvt_pk_bf16_f32 v81, v157, v158
	s_waitcnt lgkmcnt(4)
	v_mfma_f32_16x16x32_bf16 v[40:43], v[40:43], v[44:47], 0
	v_cvt_pk_bf16_f32 v82, v159, v160
	v_cvt_pk_bf16_f32 v83, v161, v162
	v_add_u32_e32 v141, 0, v89
	ds_read_b64_tr_b16 v[50:51], v142 offset:40960
	ds_read_b64_tr_b16 v[48:49], v139 offset:40960
	s_waitcnt lgkmcnt(4)
	v_mfma_f32_16x16x32_bf16 v[60:63], v[32:35], v[80:83], v[40:43]
	v_add_u32_e32 v145, 0, v90
	ds_read_b64_tr_b16 v[32:33], v141 offset:32768
	ds_read_b64_tr_b16 v[34:35], v145 offset:32768
	ds_read_b64_tr_b16 v[42:43], v145 offset:40960
	ds_read_b64_tr_b16 v[40:41], v141 offset:40960
	s_waitcnt lgkmcnt(6)
	v_mfma_f32_16x16x32_bf16 v[36:39], v[36:39], v[44:47], 0
	v_add_u32_e32 v140, 0, v91
	v_add_u32_e32 v143, 0, v94
	v_lshlrev_b32_e32 v52, 4, v52
	s_waitcnt lgkmcnt(4)
	v_mfma_f32_16x16x32_bf16 v[56:59], v[48:51], v[80:83], v[36:39]
	s_nop 2
	ds_read_b64_tr_b16 v[36:37], v140 offset:32768
	ds_read_b64_tr_b16 v[38:39], v143 offset:32768
	v_or_b32_e32 v48, 14, v84
	v_bitop3_b32 v49, v85, v48, v87 bitop3:0x36
	s_waitcnt lgkmcnt(4)
	v_mfma_f32_16x16x32_bf16 v[32:35], v[32:35], v[44:47], 0
	v_or3_b32 v89, v52, v93, v92
	v_add_u32_e32 v147, 0, v95
	v_add_u32_e32 v149, 0, v133
	s_waitcnt lgkmcnt(2)
	v_mfma_f32_16x16x32_bf16 v[52:55], v[40:43], v[80:83], v[32:35]
	s_nop 2
	ds_read_b64_tr_b16 v[34:35], v143 offset:40960
	ds_read_b64_tr_b16 v[32:33], v140 offset:40960
	v_lshlrev_b32_e32 v40, 4, v49
	v_or3_b32 v94, v40, v86, v92
	s_waitcnt lgkmcnt(2)
	v_mfma_f32_16x16x32_bf16 v[36:39], v[36:39], v[44:47], 0
	ds_read_b64_tr_b16 v[40:41], v147 offset:32768
	ds_read_b64_tr_b16 v[42:43], v149 offset:32768
	v_add_u32_e32 v133, 0, v134
	v_bitop3_b32 v88, v88, v48, v85 bitop3:0x36
	s_waitcnt lgkmcnt(2)
	v_mfma_f32_16x16x32_bf16 v[48:51], v[32:35], v[80:83], v[36:39]
	ds_read_b64_tr_b16 v[34:35], v149 offset:40960
	ds_read_b64_tr_b16 v[32:33], v147 offset:40960
	v_add_u32_e32 v134, 0, v135
	ds_read_b64_tr_b16 v[36:37], v133 offset:32768
	ds_read_b64_tr_b16 v[38:39], v134 offset:32768
	s_waitcnt lgkmcnt(4)
	v_mfma_f32_16x16x32_bf16 v[40:43], v[40:43], v[44:47], 0
	ds_read_b64_tr_b16 v[86:87], v134 offset:40960
	ds_read_b64_tr_b16 v[84:85], v133 offset:40960
	v_add_u32_e32 v135, 0, v136
	v_add_u32_e32 v136, 0, v89
	s_waitcnt lgkmcnt(4)
	v_mfma_f32_16x16x32_bf16 v[32:35], v[32:35], v[80:83], v[40:43]
	s_nop 2
	ds_read_b64_tr_b16 v[40:41], v135 offset:32768
	ds_read_b64_tr_b16 v[42:43], v136 offset:32768
	v_lshlrev_b32_e32 v95, 4, v88
	ds_read_b64_tr_b16 v[90:91], v136 offset:40960
	ds_read_b64_tr_b16 v[88:89], v135 offset:40960
	s_waitcnt lgkmcnt(6)
	v_mfma_f32_16x16x32_bf16 v[36:39], v[36:39], v[44:47], 0
	v_add_u32_e32 v137, 0, v94
	s_and_b64 vcc, exec, s[6:7]
	s_waitcnt lgkmcnt(4)
	v_mfma_f32_16x16x32_bf16 v[36:39], v[84:87], v[80:83], v[36:39]
	v_or3_b32 v84, v95, v93, v92
	v_add_u32_e32 v138, 0, v84
	ds_read_b64_tr_b16 v[84:85], v137 offset:32768
	ds_read_b64_tr_b16 v[86:87], v138 offset:32768
	s_waitcnt lgkmcnt(4)
	v_mfma_f32_16x16x32_bf16 v[40:43], v[40:43], v[44:47], 0
	s_waitcnt lgkmcnt(2)
	v_mfma_f32_16x16x32_bf16 v[40:43], v[88:91], v[80:83], v[40:43]
	ds_read_b64_tr_b16 v[90:91], v138 offset:40960
	ds_read_b64_tr_b16 v[88:89], v137 offset:40960
	s_waitcnt lgkmcnt(2)
	v_mfma_f32_16x16x32_bf16 v[44:47], v[84:87], v[44:47], 0
	s_waitcnt lgkmcnt(0)
	v_mfma_f32_16x16x32_bf16 v[44:47], v[88:91], v[80:83], v[44:47]
	s_cbranch_vccnz .LBB0_1951
	v_add_u32_e32 v80, 0, v109
	s_waitcnt vmcnt(3)
	ds_write_b128 v100, v[16:19]
	s_waitcnt vmcnt(2)
	ds_write_b128 v124, v[20:23]
	s_waitcnt vmcnt(1)
	ds_write_b128 v80, v[24:27] offset:49152
	v_add_u32_e32 v80, 0, v112
	s_waitcnt vmcnt(0)
	ds_write_b128 v80, v[28:31] offset:49152

.LBB0_1955:
	v_add_f32_e32 v97, 0, v97
	v_add_f32_e32 v97, v98, v97
	v_add_f32_e32 v97, v99, v97
	v_add_f32_e32 v97, v150, v97
	v_add_f32_e32 v97, v151, v97
	v_add_f32_e32 v97, v152, v97
	s_waitcnt lgkmcnt(3)
	v_add_f32_e32 v97, v153, v97
	v_sub_f32_e32 v76, v76, v92
	v_add_f32_e32 v97, v154, v97
	v_exp_f32_e32 v76, v76
	v_sub_f32_e32 v77, v77, v93
	v_add_f32_e32 v97, v155, v97
	v_exp_f32_e32 v77, v77
	v_add_f32_e32 v97, v156, v97
	v_add_f32_e32 v97, v157, v97
	v_cmp_le_i32_e32 vcc, v163, v125
	v_add_f32_e32 v97, v158, v97
	v_cndmask_b32_e32 v76, 0, v76, vcc
	v_cmp_lt_i32_e32 vcc, v163, v125
	v_sub_f32_e32 v78, v78, v94
	v_or_b32_e32 v93, 2, v163
	v_add_f32_e32 v97, v159, v97
	v_cndmask_b32_e32 v77, 0, v77, vcc
	v_cmp_le_i32_e32 vcc, v93, v125
	v_add_f32_e32 v97, v160, v97
	v_exp_f32_e32 v78, v78
	v_sub_f32_e32 v79, v79, v95
	v_add_f32_e32 v97, v161, v97
	v_exp_f32_e32 v79, v79
	v_add_f32_e32 v97, v162, v97
	s_waitcnt lgkmcnt(2)
	v_add_f32_e32 v92, v97, v76
	v_or_b32_e32 v93, 3, v163
	v_sub_f32_e32 v72, v72, v88
	v_add_f32_e32 v92, v77, v92
	v_cndmask_b32_e32 v78, 0, v78, vcc
	v_cmp_le_i32_e32 vcc, v93, v125
	v_exp_f32_e32 v72, v72
	v_add_f32_e32 v92, v78, v92
	v_cndmask_b32_e32 v79, 0, v79, vcc
	v_sub_f32_e32 v73, v73, v89
	v_add_f32_e32 v88, v79, v92
	v_or_b32_e32 v92, 4, v163
	v_exp_f32_e32 v73, v73
	v_cmp_le_i32_e32 vcc, v92, v125
	v_or_b32_e32 v89, 5, v163
	s_waitcnt lgkmcnt(1)
	v_cndmask_b32_e32 v72, 0, v72, vcc
	v_cmp_le_i32_e32 vcc, v89, v125
	v_sub_f32_e32 v74, v74, v90
	v_or_b32_e32 v89, 6, v163
	v_cndmask_b32_e32 v73, 0, v73, vcc
	v_cmp_le_i32_e32 vcc, v89, v125
	v_exp_f32_e32 v74, v74
	v_sub_f32_e32 v75, v75, v91
	v_exp_f32_e32 v75, v75
	v_add_f32_e32 v88, v72, v88
	v_or_b32_e32 v89, 7, v163
	v_sub_f32_e32 v68, v68, v84
	v_add_f32_e32 v88, v73, v88
	v_cndmask_b32_e32 v74, 0, v74, vcc
	v_cmp_le_i32_e32 vcc, v89, v125
	v_exp_f32_e32 v68, v68
	v_add_f32_e32 v88, v74, v88
	v_cndmask_b32_e32 v75, 0, v75, vcc
	v_add_f32_e32 v84, v75, v88
	v_add_u32_e32 v88, 32, v163
	v_cmp_le_i32_e32 vcc, v88, v125
	s_nop 1
	v_cndmask_b32_e32 v88, 0, v68, vcc
	v_sub_f32_e32 v68, v69, v85
	v_exp_f32_e32 v68, v68
	v_add_f32_e32 v69, v88, v84
	v_add_u32_e32 v84, 33, v163
	v_cmp_le_i32_e32 vcc, v84, v125
	s_nop 1
	v_cndmask_b32_e32 v84, 0, v68, vcc
	v_sub_f32_e32 v68, v70, v86
	v_exp_f32_e32 v68, v68
	v_add_u32_e32 v70, 34, v163
	v_cmp_le_i32_e32 vcc, v70, v125
	v_add_u32_e32 v70, 35, v163
	v_add_f32_e32 v69, v84, v69
	v_cndmask_b32_e32 v85, 0, v68, vcc
	v_sub_f32_e32 v68, v71, v87
	v_exp_f32_e32 v68, v68
	v_cmp_le_i32_e32 vcc, v70, v125
	v_add_f32_e32 v69, v85, v69
	v_cvt_pk_bf16_f32 v70, v72, v73
	v_cndmask_b32_e32 v86, 0, v68, vcc
	s_waitcnt lgkmcnt(0)
	v_sub_f32_e32 v64, v64, v80
	v_exp_f32_e32 v64, v64
	v_add_f32_e32 v68, v86, v69
	v_add_u32_e32 v69, 36, v163
	v_cmp_le_i32_e32 vcc, v69, v125
	v_cvt_pk_bf16_f32 v69, v78, v79
	v_cvt_pk_bf16_f32 v71, v74, v75
	v_cndmask_b32_e32 v80, 0, v64, vcc
	v_sub_f32_e32 v64, v65, v81
	v_exp_f32_e32 v64, v64
	v_add_f32_e32 v65, v80, v68
	v_add_u32_e32 v68, 37, v163
	v_cmp_le_i32_e32 vcc, v68, v125
	v_cvt_pk_bf16_f32 v68, v76, v77
	s_nop 0
	v_cndmask_b32_e32 v81, 0, v64, vcc
	v_sub_f32_e32 v64, v66, v82
	v_exp_f32_e32 v64, v64
	v_add_u32_e32 v66, 38, v163
	v_cmp_le_i32_e32 vcc, v66, v125
	v_add_u32_e32 v66, 39, v163
	v_add_f32_e32 v65, v81, v65
	v_cndmask_b32_e32 v82, 0, v64, vcc
	v_sub_f32_e32 v64, v67, v83
	v_exp_f32_e32 v64, v64
	v_cmp_le_i32_e32 vcc, v66, v125
	v_add_f32_e32 v65, v82, v65
	v_cvt_pk_bf16_f32 v66, v80, v81
	v_cndmask_b32_e32 v67, 0, v64, vcc
	v_add_f32_e32 v150, v67, v65
	v_cvt_pk_bf16_f32 v64, v88, v84
	v_cvt_pk_bf16_f32 v65, v85, v86
	v_cvt_pk_bf16_f32 v67, v82, v67
	s_waitcnt lgkmcnt(0)
	s_barrier
	s_cmp_eq_u32 s1, 0
	s_cbranch_scc1 .LBB0_1974
	v_lshl_add_u32 v151, v96, 5, s94
	s_mov_b32 s12, 2
	s_mov_b32 s4, s93
	s_mov_b32 s5, s92
	s_and_b64 vcc, exec, s[8:9]
	s_cbranch_vccnz .LBB0_1958

.LBB0_1958:
	ds_read_b128 v[88:91], v129
	ds_read_b128 v[92:95], v129 offset:1024
	ds_read_b128 v[96:99], v130
	ds_read_b128 v[152:155], v130 offset:1024
	ds_read_b128 v[172:175], v131
	ds_read_b128 v[176:179], v131 offset:1024
	ds_read_b128 v[180:183], v132
	ds_read_b128 v[184:187], v132 offset:1024
	ds_read_b128 v[188:191], v129 offset:8192
	ds_read_b128 v[192:195], v129 offset:9216
	ds_read_b128 v[196:199], v130 offset:8192
	ds_read_b128 v[200:203], v130 offset:9216
	ds_read_b128 v[204:207], v131 offset:8192
	ds_read_b128 v[208:211], v131 offset:9216
	ds_read_b128 v[212:215], v132 offset:8192
	s_and_b64 vcc, exec, s[6:7]
	s_waitcnt lgkmcnt(11)
	v_mfma_f32_16x16x32_bf16 v[72:75], v[88:91], v[0:3], v[240:243]
	ds_read_b128 v[216:219], v132 offset:9216
	ds_read_b64_tr_b16 v[220:221], v146 offset:49152
	ds_read_b64_tr_b16 v[222:223], v148 offset:49152
	ds_read_b64_tr_b16 v[226:227], v148 offset:57344
	v_mfma_f32_16x16x32_bf16 v[72:75], v[96:99], v[4:7], v[72:75]
	v_mfma_f32_16x16x32_bf16 v[76:79], v[92:95], v[0:3], v[240:243]
	s_waitcnt lgkmcnt(11)
	v_mfma_f32_16x16x32_bf16 v[72:75], v[172:175], v[8:11], v[72:75]
	ds_read_b64_tr_b16 v[224:225], v146 offset:57344
	ds_read_b64_tr_b16 v[228:229], v139 offset:49152
	ds_read_b64_tr_b16 v[230:231], v142 offset:49152
	ds_read_b64_tr_b16 v[90:91], v142 offset:57344
	v_mfma_f32_16x16x32_bf16 v[84:87], v[180:183], v[12:15], v[72:75]
	v_mfma_f32_16x16x32_bf16 v[72:75], v[152:155], v[4:7], v[76:79]
	v_mfma_f32_16x16x32_bf16 v[72:75], v[176:179], v[8:11], v[72:75]
	v_mfma_f32_16x16x32_bf16 v[80:83], v[184:187], v[12:15], v[72:75]
	s_waitcnt lgkmcnt(11)
	s_nop 5
	v_mfma_f32_16x16x32_bf16 v[72:75], v[188:191], v[0:3], v[240:243]
	ds_read_b64_tr_b16 v[88:89], v139 offset:57344
	ds_read_b64_tr_b16 v[96:97], v141 offset:49152
	ds_read_b64_tr_b16 v[98:99], v145 offset:49152
	ds_read_b64_tr_b16 v[94:95], v145 offset:57344
	v_mfma_f32_16x16x32_bf16 v[72:75], v[196:199], v[4:7], v[72:75]
	s_waitcnt lgkmcnt(11)
	v_mfma_f32_16x16x32_bf16 v[72:75], v[204:207], v[8:11], v[72:75]
	ds_read_b64_tr_b16 v[92:93], v141 offset:57344
	ds_read_b64_tr_b16 v[172:173], v140 offset:49152
	ds_read_b64_tr_b16 v[174:175], v143 offset:49152
	ds_read_b64_tr_b16 v[182:183], v143 offset:57344
	v_mfma_f32_16x16x32_bf16 v[76:79], v[212:215], v[12:15], v[72:75]
	v_mfma_f32_16x16x32_bf16 v[72:75], v[192:195], v[0:3], v[240:243]
	v_mfma_f32_16x16x32_bf16 v[72:75], v[200:203], v[4:7], v[72:75]
	s_waitcnt lgkmcnt(10)
	v_mfma_f32_16x16x32_bf16 v[60:63], v[220:223], v[68:71], v[60:63]
	ds_read_b64_tr_b16 v[180:181], v140 offset:57344
	ds_read_b64_tr_b16 v[152:153], v147 offset:49152
	ds_read_b64_tr_b16 v[154:155], v149 offset:49152
	ds_read_b64_tr_b16 v[178:179], v149 offset:57344
	ds_read_b64_tr_b16 v[176:177], v147 offset:57344
	v_mfma_f32_16x16x32_bf16 v[60:63], v[224:227], v[64:67], v[60:63]
	s_waitcnt lgkmcnt(11)
	v_mfma_f32_16x16x32_bf16 v[56:59], v[228:231], v[68:71], v[56:59]
	ds_read_b64_tr_b16 v[184:185], v133 offset:49152
	ds_read_b64_tr_b16 v[186:187], v134 offset:49152
	ds_read_b64_tr_b16 v[190:191], v134 offset:57344
	ds_read_b64_tr_b16 v[188:189], v133 offset:57344
	v_mfma_f32_16x16x32_bf16 v[56:59], v[88:91], v[64:67], v[56:59]
	s_waitcnt lgkmcnt(11)
	v_mfma_f32_16x16x32_bf16 v[52:55], v[96:99], v[68:71], v[52:55]
	ds_read_b64_tr_b16 v[196:197], v135 offset:49152
	ds_read_b64_tr_b16 v[198:199], v136 offset:49152
	ds_read_b64_tr_b16 v[206:207], v136 offset:57344
	ds_read_b64_tr_b16 v[204:205], v135 offset:57344
	v_mfma_f32_16x16x32_bf16 v[52:55], v[92:95], v[64:67], v[52:55]
	s_waitcnt lgkmcnt(11)
	v_mfma_f32_16x16x32_bf16 v[48:51], v[172:175], v[68:71], v[48:51]
	ds_read_b64_tr_b16 v[212:213], v137 offset:49152
	ds_read_b64_tr_b16 v[214:215], v138 offset:49152
	ds_read_b64_tr_b16 v[194:195], v138 offset:57344
	ds_read_b64_tr_b16 v[192:193], v137 offset:57344
	v_mfma_f32_16x16x32_bf16 v[48:51], v[180:183], v[64:67], v[48:51]
	s_waitcnt lgkmcnt(11)
	v_mfma_f32_16x16x32_bf16 v[32:35], v[152:155], v[68:71], v[32:35]
	v_mfma_f32_16x16x32_bf16 v[32:35], v[176:179], v[64:67], v[32:35]
	s_waitcnt lgkmcnt(7)
	v_mfma_f32_16x16x32_bf16 v[36:39], v[184:187], v[68:71], v[36:39]
	v_mfma_f32_16x16x32_bf16 v[36:39], v[188:191], v[64:67], v[36:39]
	s_waitcnt lgkmcnt(3)
	v_mfma_f32_16x16x32_bf16 v[40:43], v[196:199], v[68:71], v[40:43]
	v_mfma_f32_16x16x32_bf16 v[40:43], v[204:207], v[64:67], v[40:43]
	v_mfma_f32_16x16x32_bf16 v[72:75], v[208:211], v[8:11], v[72:75]
	s_waitcnt lgkmcnt(0)
	v_mfma_f32_16x16x32_bf16 v[44:47], v[212:215], v[68:71], v[44:47]
	v_mfma_f32_16x16x32_bf16 v[72:75], v[216:219], v[12:15], v[72:75]
	v_mfma_f32_16x16x32_bf16 v[44:47], v[192:195], v[64:67], v[44:47]
	s_cbranch_vccnz .LBB0_1960
	v_add_u32_e32 v64, 0, v109
	s_waitcnt vmcnt(3)
	ds_write_b128 v100, v[16:19] offset:16384
	s_waitcnt vmcnt(2)
	ds_write_b128 v124, v[20:23] offset:16384
	s_waitcnt vmcnt(1)
	ds_write_b128 v64, v[24:27] offset:32768
	v_add_u32_e32 v64, 0, v112
	s_waitcnt vmcnt(0)
	ds_write_b128 v64, v[28:31] offset:32768

.LBB0_1966:
	ds_read_b128 v[164:167], v129 offset:16384
	ds_read_b128 v[168:171], v130 offset:16384
	ds_read_b128 v[172:175], v131 offset:16384
	ds_read_b128 v[176:179], v129 offset:17408
	ds_read_b128 v[180:183], v132 offset:16384
	ds_read_b128 v[184:187], v130 offset:17408
	ds_read_b128 v[188:191], v131 offset:17408
	ds_read_b128 v[192:195], v129 offset:24576
	ds_read_b128 v[196:199], v132 offset:17408
	ds_read_b128 v[200:203], v130 offset:24576
	ds_read_b128 v[204:207], v131 offset:24576
	ds_read_b128 v[208:211], v129 offset:25600
	ds_read_b128 v[212:215], v132 offset:24576
	ds_read_b128 v[216:219], v130 offset:25600
	ds_read_b128 v[220:223], v131 offset:25600
	v_sub_f32_e32 v64, v84, v96
	v_exp_f32_e32 v96, v64
	v_sub_f32_e32 v64, v85, v97
	v_exp_f32_e32 v97, v64
	v_sub_f32_e32 v64, v86, v98
	v_exp_f32_e32 v98, v64
	v_sub_f32_e32 v64, v87, v99
	v_exp_f32_e32 v99, v64
	v_sub_f32_e32 v64, v80, v92
	v_exp_f32_e32 v152, v64
	v_sub_f32_e32 v64, v81, v93
	v_exp_f32_e32 v153, v64
	v_sub_f32_e32 v64, v82, v94
	v_exp_f32_e32 v154, v64
	v_sub_f32_e32 v64, v83, v95
	s_waitcnt lgkmcnt(11)
	v_mfma_f32_16x16x32_bf16 v[84:87], v[164:167], v[0:3], v[240:243]
	ds_read_b128 v[224:227], v132 offset:25600
	ds_read_b64_tr_b16 v[228:229], v146 offset:32768
	ds_read_b64_tr_b16 v[230:231], v148 offset:32768
	ds_read_b64_tr_b16 v[166:167], v148 offset:40960
	v_exp_f32_e32 v155, v64
	v_sub_f32_e32 v64, v76, v88
	v_mfma_f32_16x16x32_bf16 v[84:87], v[168:171], v[4:7], v[84:87]
	v_exp_f32_e32 v156, v64
	v_sub_f32_e32 v64, v77, v89
	v_mfma_f32_16x16x32_bf16 v[92:95], v[176:179], v[0:3], v[240:243]
	v_exp_f32_e32 v157, v64
	v_sub_f32_e32 v64, v78, v90
	v_exp_f32_e32 v158, v64
	v_sub_f32_e32 v64, v79, v91
	s_waitcnt lgkmcnt(10)
	v_mfma_f32_16x16x32_bf16 v[88:91], v[184:187], v[4:7], v[92:95]
	ds_read_b64_tr_b16 v[164:165], v146 offset:40960
	ds_read_b64_tr_b16 v[168:169], v139 offset:32768
	ds_read_b64_tr_b16 v[170:171], v142 offset:32768
	ds_read_b64_tr_b16 v[178:179], v142 offset:40960
	ds_read_b64_tr_b16 v[176:177], v139 offset:40960
	v_exp_f32_e32 v159, v64
	v_mfma_f32_16x16x32_bf16 v[80:83], v[172:175], v[8:11], v[84:87]
	v_sub_f32_e32 v64, v72, v66
	v_sub_f32_e32 v70, v73, v67
	v_mfma_f32_16x16x32_bf16 v[76:79], v[188:191], v[8:11], v[88:91]
	v_sub_f32_e32 v68, v74, v68
	s_and_b64 vcc, exec, s[6:7]
	v_mfma_f32_16x16x32_bf16 v[92:95], v[192:195], v[0:3], v[240:243]
	v_mfma_f32_16x16x32_bf16 v[76:79], v[196:199], v[12:15], v[76:79]
	s_waitcnt lgkmcnt(11)
	v_mfma_f32_16x16x32_bf16 v[88:91], v[200:203], v[4:7], v[92:95]
	ds_read_b64_tr_b16 v[184:185], v141 offset:32768
	ds_read_b64_tr_b16 v[186:187], v145 offset:32768
	ds_read_b64_tr_b16 v[174:175], v145 offset:40960
	ds_read_b64_tr_b16 v[172:173], v141 offset:40960
	v_mfma_f32_16x16x32_bf16 v[80:83], v[180:183], v[12:15], v[80:83]
	v_exp_f32_e32 v160, v64
	v_exp_f32_e32 v161, v70
	v_mfma_f32_16x16x32_bf16 v[84:87], v[204:207], v[8:11], v[88:91]
	v_exp_f32_e32 v162, v68
	v_mfma_f32_16x16x32_bf16 v[64:67], v[212:215], v[12:15], v[84:87]
	v_sub_f32_e32 v68, v75, v69
	v_exp_f32_e32 v163, v68
	v_mfma_f32_16x16x32_bf16 v[84:87], v[208:211], v[0:3], v[240:243]
	v_cvt_pk_bf16_f32 v92, v96, v97
	v_cvt_pk_bf16_f32 v93, v98, v99
	s_waitcnt lgkmcnt(11)
	v_mfma_f32_16x16x32_bf16 v[84:87], v[216:219], v[4:7], v[84:87]
	ds_read_b64_tr_b16 v[188:189], v140 offset:32768
	ds_read_b64_tr_b16 v[190:191], v143 offset:32768
	ds_read_b64_tr_b16 v[194:195], v143 offset:40960
	ds_read_b64_tr_b16 v[192:193], v140 offset:40960
	v_cvt_pk_bf16_f32 v94, v152, v153
	v_cvt_pk_bf16_f32 v95, v154, v155
	v_mfma_f32_16x16x32_bf16 v[68:71], v[220:223], v[8:11], v[84:87]
	s_nop 2
	v_cvt_pk_bf16_f32 v84, v156, v157
	v_mfma_f32_16x16x32_bf16 v[68:71], v[224:227], v[12:15], v[68:71]
	v_cvt_pk_bf16_f32 v85, v158, v159
	v_cvt_pk_bf16_f32 v86, v160, v161
	s_waitcnt lgkmcnt(11)
	v_mfma_f32_16x16x32_bf16 v[60:63], v[228:231], v[92:95], v[60:63]
	ds_read_b64_tr_b16 v[196:197], v147 offset:32768
	ds_read_b64_tr_b16 v[198:199], v149 offset:32768
	ds_read_b64_tr_b16 v[202:203], v149 offset:40960
	ds_read_b64_tr_b16 v[200:201], v147 offset:40960
	v_cvt_pk_bf16_f32 v87, v162, v163
	s_nop 1
	v_mfma_f32_16x16x32_bf16 v[60:63], v[164:167], v[84:87], v[60:63]
	s_waitcnt lgkmcnt(11)
	v_mfma_f32_16x16x32_bf16 v[56:59], v[168:171], v[92:95], v[56:59]
	ds_read_b64_tr_b16 v[180:181], v133 offset:32768
	ds_read_b64_tr_b16 v[182:183], v134 offset:32768
	ds_read_b64_tr_b16 v[206:207], v134 offset:40960
	ds_read_b64_tr_b16 v[204:205], v133 offset:40960
	v_mfma_f32_16x16x32_bf16 v[56:59], v[176:179], v[84:87], v[56:59]
	s_waitcnt lgkmcnt(11)
	v_mfma_f32_16x16x32_bf16 v[52:55], v[184:187], v[92:95], v[52:55]
	ds_read_b64_tr_b16 v[212:213], v135 offset:32768
	ds_read_b64_tr_b16 v[214:215], v136 offset:32768
	ds_read_b64_tr_b16 v[210:211], v136 offset:40960
	ds_read_b64_tr_b16 v[208:209], v135 offset:40960
	v_mfma_f32_16x16x32_bf16 v[52:55], v[172:175], v[84:87], v[52:55]
	s_waitcnt lgkmcnt(11)
	v_mfma_f32_16x16x32_bf16 v[48:51], v[188:191], v[92:95], v[48:51]
	ds_read_b64_tr_b16 v[216:217], v137 offset:32768
	ds_read_b64_tr_b16 v[218:219], v138 offset:32768
	ds_read_b64_tr_b16 v[222:223], v138 offset:40960
	ds_read_b64_tr_b16 v[220:221], v137 offset:40960
	v_mfma_f32_16x16x32_bf16 v[48:51], v[192:195], v[84:87], v[48:51]
	s_waitcnt lgkmcnt(11)
	v_mfma_f32_16x16x32_bf16 v[32:35], v[196:199], v[92:95], v[32:35]
	v_mfma_f32_16x16x32_bf16 v[32:35], v[200:203], v[84:87], v[32:35]
	s_waitcnt lgkmcnt(7)
	v_mfma_f32_16x16x32_bf16 v[36:39], v[180:183], v[92:95], v[36:39]
	v_mfma_f32_16x16x32_bf16 v[36:39], v[204:207], v[84:87], v[36:39]
	s_waitcnt lgkmcnt(3)
	v_mfma_f32_16x16x32_bf16 v[40:43], v[212:215], v[92:95], v[40:43]
	v_mfma_f32_16x16x32_bf16 v[40:43], v[208:211], v[84:87], v[40:43]
	s_waitcnt lgkmcnt(0)
	v_mfma_f32_16x16x32_bf16 v[44:47], v[216:219], v[92:95], v[44:47]
	v_mfma_f32_16x16x32_bf16 v[44:47], v[220:223], v[84:87], v[44:47]
	s_cbranch_vccnz .LBB0_1968
	v_add_u32_e32 v72, 0, v109
	s_waitcnt vmcnt(3)
	ds_write_b128 v100, v[16:19]
	s_waitcnt vmcnt(2)
	ds_write_b128 v124, v[20:23]
	s_waitcnt vmcnt(1)
	ds_write_b128 v72, v[24:27] offset:49152
	v_add_u32_e32 v72, 0, v112
	s_waitcnt vmcnt(0)
	ds_write_b128 v72, v[28:31] offset:49152

.LBB0_1972:
	v_add_f32_e32 v96, v150, v96
	v_add_f32_e32 v96, v97, v96
	v_add_f32_e32 v96, v98, v96
	v_add_f32_e32 v96, v99, v96
	v_add_f32_e32 v96, v152, v96
	v_add_f32_e32 v96, v153, v96
	v_add_f32_e32 v96, v154, v96
	v_add_f32_e32 v96, v155, v96
	v_add_f32_e32 v96, v156, v96
	v_add_f32_e32 v96, v157, v96
	v_add_f32_e32 v96, v158, v96
	s_waitcnt lgkmcnt(3)
	v_add_f32_e32 v96, v159, v96
	v_sub_f32_e32 v80, v80, v92
	v_add_f32_e32 v96, v160, v96
	v_exp_f32_e32 v80, v80
	v_sub_f32_e32 v81, v81, v93
	v_add_f32_e32 v96, v161, v96
	v_exp_f32_e32 v81, v81
	v_sub_f32_e32 v82, v82, v94
	v_add_f32_e32 v96, v162, v96
	v_exp_f32_e32 v82, v82
	v_sub_f32_e32 v83, v83, v95
	s_waitcnt lgkmcnt(2)
	v_add_f32_e32 v96, v163, v96
	v_exp_f32_e32 v83, v83
	v_sub_f32_e32 v76, v76, v88
	v_add_f32_e32 v92, v96, v80
	v_exp_f32_e32 v76, v76
	v_sub_f32_e32 v77, v77, v89
	v_add_f32_e32 v92, v81, v92
	v_exp_f32_e32 v77, v77
	v_sub_f32_e32 v78, v78, v90
	v_add_f32_e32 v92, v82, v92
	v_exp_f32_e32 v78, v78
	v_sub_f32_e32 v79, v79, v91
	s_waitcnt lgkmcnt(1)
	v_add_f32_e32 v92, v83, v92
	v_exp_f32_e32 v79, v79
	v_sub_f32_e32 v64, v64, v84
	s_waitcnt lgkmcnt(0)
	v_add_f32_e32 v88, v76, v92
	v_exp_f32_e32 v64, v64
	v_sub_f32_e32 v65, v65, v85
	v_sub_f32_e32 v68, v68, v72
	v_add_f32_e32 v88, v77, v88
	v_exp_f32_e32 v65, v65
	v_sub_f32_e32 v66, v66, v86
	v_exp_f32_e32 v72, v68
	v_add_f32_e32 v88, v78, v88
	v_exp_f32_e32 v66, v66
	v_sub_f32_e32 v67, v67, v87
	v_sub_f32_e32 v68, v69, v73
	v_add_f32_e32 v88, v79, v88
	v_exp_f32_e32 v67, v67
	v_exp_f32_e32 v73, v68
	v_add_f32_e32 v84, v64, v88
	v_sub_f32_e32 v68, v70, v74
	v_add_f32_e32 v84, v65, v84
	v_exp_f32_e32 v74, v68
	v_add_f32_e32 v84, v66, v84
	v_sub_f32_e32 v68, v71, v75
	v_add_f32_e32 v84, v67, v84
	v_exp_f32_e32 v75, v68
	v_add_f32_e32 v68, v72, v84
	v_add_f32_e32 v68, v73, v68
	v_add_f32_e32 v68, v74, v68
	v_add_f32_e32 v150, v75, v68
	v_cvt_pk_bf16_f32 v68, v80, v81
	v_cvt_pk_bf16_f32 v69, v82, v83
	v_cvt_pk_bf16_f32 v70, v76, v77
	v_cvt_pk_bf16_f32 v71, v78, v79
	v_cvt_pk_bf16_f32 v64, v64, v65
	v_cvt_pk_bf16_f32 v65, v66, v67
	v_cvt_pk_bf16_f32 v66, v72, v73
	v_cvt_pk_bf16_f32 v67, v74, v75
	s_waitcnt lgkmcnt(0)
	s_barrier
	s_add_i32 s13, s12, 2
	s_add_i32 s5, s5, -2
	s_add_i32 s4, s4, 0xffd10000
	s_cmp_ge_u32 s12, s0
	v_add_u32_e32 v151, 0xfffffe00, v151
	s_cbranch_scc1 .LBB0_1974
	s_mov_b32 s12, s13
	s_and_b64 vcc, exec, s[8:9]
	s_cbranch_vccz .LBB0_1957
	s_branch .LBB0_1958
